# v74 with the compress-stage-1 GEMM split four ways along K (64 workgroups, three partial sets added by the first) and token-shift / V-transpose on workgroups 64..
# baseline (speedup 1.0000x reference)
; #define PHASE_END   } if (gp + 1 < hi) xcd_barrier(bar); } ++gp;
; #define RELAUNDER() do { asm volatile("" : "+v"(pc.tid), "+s"(pc.bid)); pc.lane = pc.tid & 63; pc.wave = __builtin_amdgcn_readfirstlane(pc.tid >> 6); } while (0)
; __global__ void __launch_bounds__(512, 2) fwd_kernel(Args args) {
;     ...
;             PHASE_BEGIN(16) {
;                 { pg8::Gemm g{proj, wb + WB_W1T, 16 * PLD, 2048, 2048, (unsigned)PLD * 2}; pg8::Sched S; S.init(16, 1, c.G, c.bid, 1, 0, 0, 0, 0); S.mode = 1;
;                   pg8::EpiCmp1 E{hidb, (const float*)(wb + WB_BH)}; pg8::gemm_phase(c.lds, c.tid, g, S, E); }
;                 RELAUNDER();
;                 if (c.bid >= 16) { Ctx cv = c; cv.bid = c.bid - 16; cv.G = c.G - 16; phase_lora_a(cv, args, layer, proj, alora); vt_transpose(cv, proj, vtb); } } PHASE_END
.LBB0_75:
	s_add_u32 s2, s76, 0x10000
	s_addc_u32 s3, s77, 0
	s_add_u32 s78, s76, 0x68e0000
	v_writelane_b32 v251, s2, 6
	s_addc_u32 s79, s77, 0
	s_load_dwordx2 s[0:1], s[0:1], 0xf0
	v_writelane_b32 v251, s3, 7
	s_add_u32 s2, s76, 0x2650000
	v_writelane_b32 v251, s2, 8
	s_addc_u32 s2, s77, 0
	v_writelane_b32 v251, s2, 9
	s_add_u32 s2, s76, 0x2450000
	v_writelane_b32 v251, s2, 10
	s_addc_u32 s2, s77, 0
	v_writelane_b32 v251, s2, 11
	s_add_u32 s2, s76, 0x2390000
	s_addc_u32 s3, s77, 0
	v_writelane_b32 v251, s2, 12
	v_mbcnt_lo_u32_b32 v2, -1, 0
	s_mov_b32 s43, 0
	v_writelane_b32 v251, s3, 13
	s_add_u32 s2, s76, 0x1e10000
	s_addc_u32 s3, s77, 0
	v_writelane_b32 v251, s2, 14
	s_mov_b32 s63, 0x20000
	s_brev_b32 s62, -2
	v_writelane_b32 v251, s3, 15
	s_add_u32 s2, s76, 0x1310000
	s_addc_u32 s3, s77, 0
	v_writelane_b32 v251, s2, 16
	v_mov_b32_e32 v186, 0x3a27c5ac
	v_mov_b32_e32 v234, 0x358637bd
	v_writelane_b32 v251, s3, 17
	s_add_u32 s2, s76, 0x1110000
	s_addc_u32 s3, s77, 0
	v_writelane_b32 v251, s2, 18
	v_mov_b32_e32 v188, 0x41b17218
	v_mov_b32_e32 v190, 0xf149f2ca
	v_writelane_b32 v251, s3, 19
	s_add_u32 s2, s76, 0xe10000
	v_writelane_b32 v251, s2, 20
	s_addc_u32 s2, s77, 0
	v_writelane_b32 v251, s2, 21
	s_lshl_b32 s2, s74, 1
	v_writelane_b32 v251, s2, 22
	s_add_u32 s2, s76, 0x200
	s_addc_u32 s3, s77, 0
	v_writelane_b32 v251, s2, 23
	v_mbcnt_hi_u32_b32 v244, -1, v2
	v_mov_b32_e32 v194, 0xff800000
	v_writelane_b32 v251, s3, 24
	s_add_u32 s2, s76, 0x1000
	s_addc_u32 s3, s77, 0
	v_writelane_b32 v251, s2, 25
	s_movk_i32 s96, 0x7f
	s_movk_i32 s23, 0x100
	v_writelane_b32 v251, s3, 26
	s_add_u32 s2, s76, 0x1100
	s_addc_u32 s3, s77, 0
	v_writelane_b32 v251, s2, 27
	s_movk_i32 s67, 0x90
	s_movk_i32 s97, 0x1000
	v_writelane_b32 v251, s3, 28
	s_add_u32 s2, s76, 0x1200
	s_addc_u32 s3, s77, 0
	v_writelane_b32 v251, s2, 29
	s_mov_b32 s16, 1
	s_mov_b32 s33, 0x800000
	v_writelane_b32 v251, s3, 30
	s_add_u32 s2, s76, 0x1300
	s_addc_u32 s3, s77, 0
	v_writelane_b32 v251, s2, 31
	s_cmp_eq_u32 s24, 15
	s_mov_b32 s72, 0xf149f2ca
	v_writelane_b32 v251, s3, 32
	s_cselect_b64 s[2:3], -1, 0
	v_writelane_b32 v251, s2, 33
	s_cmp_eq_u32 s24, 14
	s_movk_i32 s73, 0x4c
	v_writelane_b32 v251, s3, 34
	s_cselect_b64 s[2:3], -1, 0
	v_writelane_b32 v251, s2, 35
	s_cmp_eq_u32 s24, 13
	s_movk_i32 s25, 0x315
	v_writelane_b32 v251, s3, 36
	s_cselect_b64 s[2:3], -1, 0
	v_writelane_b32 v251, s2, 37
	s_cmp_eq_u32 s24, 12
	s_mov_b32 s30, 0xefa18f08
	v_writelane_b32 v251, s3, 38
	s_cselect_b64 s[2:3], -1, 0
	v_writelane_b32 v251, s2, 39
	s_cmp_eq_u32 s24, 11
	s_mov_b32 s31, 0xe1fc780f
	v_writelane_b32 v251, s3, 40
	s_cselect_b64 s[2:3], -1, 0
	v_writelane_b32 v251, s2, 41
	s_cmp_eq_u32 s24, 10
	s_movk_i32 s18, 0xfb78
	v_writelane_b32 v251, s3, 42
	s_cselect_b64 s[2:3], -1, 0
	v_writelane_b32 v251, s2, 43
	s_cmp_eq_u32 s24, 9
	s_movk_i32 s19, 0x380
	v_writelane_b32 v251, s3, 44
	s_cselect_b64 s[2:3], -1, 0
	v_writelane_b32 v251, s2, 45
	s_cmp_eq_u32 s24, 8
	s_movk_i32 s34, 0x3f0
	v_writelane_b32 v251, s3, 46
	s_cselect_b64 s[2:3], -1, 0
	v_writelane_b32 v251, s2, 47
	s_cmp_eq_u32 s24, 7
	s_movk_i32 s35, 0x101f
	v_writelane_b32 v251, s3, 48
	s_cselect_b64 s[2:3], -1, 0
	v_writelane_b32 v251, s2, 49
	s_cmp_eq_u32 s24, 6
	s_mov_b64 s[44:45], 0x80
	v_writelane_b32 v251, s3, 50
	s_cselect_b64 s[2:3], -1, 0
	v_writelane_b32 v251, s2, 51
	s_cmp_eq_u32 s24, 5
	s_nop 0
	v_writelane_b32 v251, s3, 52
	s_cselect_b64 s[2:3], -1, 0
	v_writelane_b32 v251, s2, 53
	s_cmp_eq_u32 s24, 4
	s_nop 0
	v_writelane_b32 v251, s3, 54
	s_cselect_b64 s[2:3], -1, 0
	v_writelane_b32 v251, s2, 55
	s_cmp_eq_u32 s24, 3
	s_nop 0
	v_writelane_b32 v251, s3, 56
	s_cselect_b64 s[2:3], -1, 0
	v_writelane_b32 v251, s2, 57
	s_cmp_eq_u32 s24, 2
	s_nop 0
	v_writelane_b32 v251, s3, 58
	s_cselect_b64 s[2:3], -1, 0
	v_writelane_b32 v251, s2, 59
	s_cmp_eq_u32 s24, 1
	s_nop 0
	v_writelane_b32 v251, s3, 60
	s_cselect_b64 s[2:3], -1, 0
	v_writelane_b32 v251, s2, 61
	s_cmp_eq_u32 s24, 0
	s_nop 0
	v_writelane_b32 v251, s3, 62
	s_cselect_b64 s[2:3], -1, 0
	v_writelane_b32 v251, s2, 63
	s_nop 1
	v_writelane_b32 v252, s3, 0
	s_lshl_b32 s2, s24, 8
	s_add_u32 s2, s76, s2
	s_addc_u32 s3, s77, 0
	s_add_u32 s4, s2, 0x1400
	s_addc_u32 s5, s3, 0
	v_writelane_b32 v252, s4, 1
	s_add_u32 s2, s2, 0x2400
	s_addc_u32 s3, s3, 0
	v_writelane_b32 v252, s5, 2
	v_writelane_b32 v252, s2, 3
	s_mov_b32 s24, 0xbfb8aa3b
	s_nop 0
	v_writelane_b32 v252, s3, 4
	s_add_u32 s2, s76, 0x3400
	s_addc_u32 s3, s77, 0
	v_writelane_b32 v252, s2, 5
	s_nop 1
	v_writelane_b32 v252, s3, 6
	s_add_u32 s2, s76, 0x3500
	s_addc_u32 s3, s77, 0
	v_writelane_b32 v252, s2, 7
	s_nop 1
	v_writelane_b32 v252, s3, 8
	s_add_i32 s2, s74, -1
	v_writelane_b32 v252, s2, 9
	s_add_u32 s2, s76, 0x2690000
	s_addc_u32 s3, s77, 0
	v_writelane_b32 v252, s2, 10
	s_nop 1
	v_writelane_b32 v252, s3, 11
	s_add_u32 s2, s76, 0x26c0000
	s_addc_u32 s3, s77, 0
	s_add_u32 s80, s76, 0x7f00000
	v_writelane_b32 v252, s2, 12
	s_addc_u32 s81, s77, 0
	s_mov_b32 s8, s80
	v_writelane_b32 v252, s3, 13
	s_add_u32 s2, s76, 0xff00000
	v_writelane_b32 v252, s2, 14
	s_addc_u32 s2, s77, 0
	s_ashr_i32 s75, s74, 31
	v_writelane_b32 v252, s2, 15
	s_add_u32 s2, s76, 0x67e0000
	s_addc_u32 s3, s77, 0
	v_writelane_b32 v252, s2, 16
	s_nop 1
	v_writelane_b32 v252, s3, 17
	s_add_i32 s2, s74, -64
	s_add_u32 s4, s76, 0x6b00000
	s_addc_u32 s5, s77, 0
	v_writelane_b32 v252, s4, 18
	s_nop 1
	v_writelane_b32 v252, s5, 19
	s_lshl_b32 s4, s2, 4
	s_add_u32 s82, s76, 0x7300000
	s_addc_u32 s83, s77, 0
	s_add_u32 s84, s76, 0x1cf00000
	s_addc_u32 s85, s77, 0
	v_writelane_b32 v252, s2, 20
	s_add_u32 s2, s76, 0x6760000
	s_addc_u32 s3, s77, 0
; #define LAS __attribute__((address_space(3)))
; __global__ void __launch_bounds__(512, 2) fwd_kernel(Args args) {
;     extern __shared__ __attribute__((aligned(16))) unsigned char lds_raw[];
;     Ctx c0; c0.lds = (LAS unsigned char*)lds_raw; c0.tid = threadIdx.x; c0.lane = c0.tid & 63; c0.wave = __builtin_amdgcn_readfirstlane(c0.tid >> 6); c0.G = gridDim.x; c0.bid = blockIdx.x; const Ctx& c = c0;
;     unsigned char* ws = args.ws;
;     volatile LAS unsigned* misc = (volatile LAS unsigned*)(c.lds + LDS_MISC);
;     if (c.tid < 4) misc[c.tid] = 0u;
;     if (c.tid < 30) { const unsigned long long pv = (unsigned long long)args.in[c.tid & 31]; misc[16 + 2 * c.tid] = (unsigned)pv; misc[17 + 2 * c.tid] = (unsigned)(pv >> 32); }
;     __syncthreads();
;     XcdBarrier bar; bar.bar = (unsigned*)(ws + WS_CTL); bar.x = 0; bar.st = misc;
;     const int lo = args.lo, hi = args.hi;
;     const int wave0 = __builtin_amdgcn_readfirstlane(c0.tid >> 6);
;     const bool multi = (hi - lo) > 1;
;     if (multi) bar = xcd_barrier_post((unsigned*)(ws + WS_CTL), misc);
;     int gp = 0;
	s_add_u32 s86, s76, 0x67a0000
	s_addc_u32 s87, s77, 0
	s_add_u32 s88, s76, 0x1df00000
	s_addc_u32 s89, s77, 0
	s_add_u32 s90, s76, 0x1ef00000
	s_addc_u32 s91, s77, 0
	s_add_u32 s40, s76, 0x15f00000
	v_writelane_b32 v252, s2, 21
	s_addc_u32 s41, s77, 0
	s_mov_b32 s68, s40
	v_writelane_b32 v252, s3, 22
	s_add_u32 s2, s76, 0x66e0000
	v_writelane_b32 v252, s2, 23
	s_addc_u32 s2, s77, 0
	v_writelane_b32 v252, s2, 24
	s_add_u32 s2, s76, 0x1af00000
	s_addc_u32 s3, s77, 0
	v_writelane_b32 v252, s2, 25
	s_nop 1
	v_writelane_b32 v252, s3, 26
	s_add_u32 s2, s76, 0x19f00000
	v_writelane_b32 v252, s2, 27
	s_addc_u32 s2, s77, 0
	v_writelane_b32 v252, s2, 28
	s_add_u32 s2, s76, 0x8000
	v_writelane_b32 v252, s2, 29
	s_addc_u32 s2, s77, 0
	s_add_u32 s92, s76, 0x7f01e00
	s_addc_u32 s93, s77, 0
	s_add_u32 s94, s76, 0x7f01600
	s_addc_u32 s95, s77, 0
	v_writelane_b32 v252, s2, 30
	s_add_u32 s2, s76, 0x7f01400
	v_writelane_b32 v252, s2, 31
	s_addc_u32 s2, s77, 0
	s_and_b32 s69, s41, 0xffff
	v_writelane_b32 v252, s2, 32
	s_add_u32 s2, s76, 0x4000
	v_writelane_b32 v252, s2, 33
	s_addc_u32 s2, s77, 0
	v_writelane_b32 v252, s2, 34
	s_add_u32 s2, s76, 0x6860000
	s_addc_u32 s3, s77, 0
	v_writelane_b32 v252, s2, 35
	s_and_b32 s9, s81, 0xffff
	s_nop 0
	v_writelane_b32 v252, s3, 36
	s_add_u32 s2, s76, 0xd700000
	v_writelane_b32 v252, s2, 37
	s_addc_u32 s2, s77, 0
	v_writelane_b32 v252, s2, 38
	s_abs_i32 s2, s74
	v_cvt_f32_u32_e32 v1, s2
	v_writelane_b32 v252, s2, 39
	s_sub_i32 s2, 0, s2
	s_ashr_i32 s5, s4, 31
	v_rcp_iflag_f32_e32 v1, v1
	s_nop 0
	v_mul_f32_e32 v1, 0x4f7ffffe, v1
	v_cvt_u32_f32_e32 v1, v1
	s_nop 0
	v_readfirstlane_b32 s3, v1
	s_mul_i32 s2, s2, s3
	s_mul_hi_u32 s2, s3, s2
	s_add_i32 s2, s3, s2
	v_writelane_b32 v252, s2, 40
	v_writelane_b32 v252, s8, 41
	v_mov_b32_e32 v1, 0
	s_nop 0
	v_writelane_b32 v252, s9, 42
	v_writelane_b32 v252, s10, 43
	v_writelane_b32 v252, s11, 44
	s_waitcnt lgkmcnt(0)
	v_writelane_b32 v252, s0, 45
	s_mov_b32 s10, s43
	s_nop 0
	v_writelane_b32 v252, s1, 46
	s_lshl_b64 s[0:1], s[4:5], 9
	v_writelane_b32 v252, s0, 47
	s_nop 1
	v_writelane_b32 v252, s1, 48
	s_add_u32 s0, s76, 0x7f00c00
	s_addc_u32 s1, s77, 0
	v_writelane_b32 v252, s0, 49
	s_ashr_i32 s37, s36, 31
	s_add_i32 s64, 0, 0x260f8
	v_writelane_b32 v252, s1, 50
	s_lshl_b32 s0, s74, 6
	v_writelane_b32 v252, s0, 51
	s_addk_i32 s0, 0xf000
	v_writelane_b32 v252, s0, 52
	s_add_i32 s0, 0, 0x26048
	v_writelane_b32 v252, s0, 53
	s_add_i32 s0, 0, 0x2604c
	v_writelane_b32 v252, s0, 54
	s_add_i32 s0, 0, 0x26098
	v_writelane_b32 v252, s0, 55
	s_add_i32 s0, 0, 0x2609c
	v_writelane_b32 v252, s0, 56
	s_add_i32 s0, 0, 0x26090
	v_writelane_b32 v252, s0, 57
	s_add_i32 s0, 0, 0x26094
	v_writelane_b32 v252, s0, 58
	s_add_i32 s0, 0, 0x26080
	v_writelane_b32 v252, s0, 59
	s_add_i32 s0, 0, 0x26084
	v_writelane_b32 v252, s0, 60
	s_add_i32 s0, 0, 0x26128
	v_writelane_b32 v252, s0, 61
	s_add_i32 s0, 0, 0x2612c
	v_writelane_b32 v252, s0, 62
	s_add_i32 s0, 0, 0x26058
	v_writelane_b32 v252, s0, 63
	s_add_i32 s0, 0, 0x2605c
	v_writelane_b32 v253, s0, 0
	s_add_i32 s0, 0, 0x26110
	v_writelane_b32 v253, s0, 1
	s_add_i32 s0, 0, 0x26114
	v_writelane_b32 v253, s0, 2
	s_add_i32 s0, 0, 0x26068
	v_writelane_b32 v253, s0, 3
	s_add_i32 s0, 0, 0x2606c
	v_writelane_b32 v253, s0, 4
	s_add_i32 s0, 0, 0x26108
	v_writelane_b32 v253, s0, 5
	s_add_i32 s0, 0, 0x2610c
	v_writelane_b32 v253, s0, 6
	s_add_i32 s0, 0, 0x26000
	v_writelane_b32 v253, s0, 7
	s_add_i32 s0, 0, 0x26004
	v_writelane_b32 v253, s0, 8
	s_add_i32 s0, 0, 0x26070
	v_writelane_b32 v253, s0, 9
	s_add_i32 s0, 0, 0x26074
	v_writelane_b32 v253, s0, 10
	s_add_i32 s0, 0, 0x18300
	v_writelane_b32 v253, s0, 11
	s_add_i32 s0, 0, 0x1a700
	v_writelane_b32 v253, s0, 12
	s_add_i32 s0, 0, 0x1cb00
	v_writelane_b32 v253, s0, 13
	s_add_i32 s0, 0, 0x26078
	v_writelane_b32 v253, s0, 14
	s_add_i32 s0, 0, 0x2607c
	v_writelane_b32 v253, s0, 15
	s_add_i32 s0, 0, 0x26088
	v_writelane_b32 v253, s0, 16
	s_add_i32 s0, 0, 0x2608c
	v_writelane_b32 v253, s0, 17
	s_add_i32 s0, 0, 0x260a0
	v_writelane_b32 v253, s0, 18
	s_add_i32 s0, 0, 0x260a4
	v_writelane_b32 v253, s0, 19
	s_add_i32 s0, 0, 0x260a8
	v_writelane_b32 v253, s0, 20
	s_add_i32 s0, 0, 0x260ac
	v_writelane_b32 v253, s0, 21
	s_add_i32 s0, 0, 0x260b0
	v_writelane_b32 v253, s0, 22
	s_add_i32 s0, 0, 0x260b4
	v_writelane_b32 v253, s0, 23
	s_add_i32 s0, 0, 0x26100
	v_writelane_b32 v253, s0, 24
	s_add_i32 s0, 0, 0x26104
	v_writelane_b32 v253, s0, 25
	s_add_i32 s0, 0, 0x14400
	v_writelane_b32 v253, s0, 26
	s_add_i32 s0, 0, 0x26400
	v_writelane_b32 v253, s0, 27
	s_add_i32 s0, 0, 0x260b8
	v_writelane_b32 v253, s0, 28
	s_add_i32 s0, 0, 0x260bc
	v_writelane_b32 v253, s0, 29
	s_add_i32 s0, 0, 0x260c0
	v_writelane_b32 v253, s0, 30
	s_add_i32 s0, 0, 0x260c4
	v_writelane_b32 v253, s0, 31
	s_add_i32 s0, 0, 0x24880
	v_writelane_b32 v253, s0, 32
	s_add_i32 s0, 0, 0x254a0
	v_writelane_b32 v253, s0, 33
	s_add_i32 s0, 0, 0x254a8
	v_writelane_b32 v253, s0, 34
	s_add_i32 s0, 0, 0x254b0
	v_writelane_b32 v253, s0, 35
	s_add_i32 s0, 0, 0x25480
	v_writelane_b32 v253, s0, 36
	s_add_i32 s0, 0, 0x26050
	v_writelane_b32 v253, s0, 37
	s_add_i32 s0, 0, 0x26054
	v_writelane_b32 v253, s0, 38
	s_add_i32 s0, 0, 0x26060
	v_writelane_b32 v253, s0, 39
	s_add_i32 s0, 0, 0x26064
	v_writelane_b32 v253, s0, 40
	v_cmp_eq_u32_e64 s[0:1], 0, v0
	s_add_i32 s65, 0, 0x260fc
	s_nop 0
	v_writelane_b32 v253, s0, 41
	s_nop 1
	v_writelane_b32 v253, s1, 42
	s_mov_b32 s0, s4
	v_writelane_b32 v253, s0, 43
	s_nop 1
	v_writelane_b32 v253, s1, 44
	s_lshl_b64 s[0:1], s[4:5], 13
	v_writelane_b32 v253, s0, 45
	s_nop 1
	v_writelane_b32 v253, s1, 46
	s_mov_b32 s0, s36
	v_writelane_b32 v253, s0, 47
	s_nop 1
	v_writelane_b32 v253, s1, 48
	s_lshl_b64 s[0:1], s[36:37], 15
	v_writelane_b32 v253, s0, 49
	s_nop 1
	v_writelane_b32 v253, s1, 50
	v_writelane_b32 v253, s74, 51
	v_writelane_b32 v253, s76, 52
	s_nop 1
	v_writelane_b32 v253, s77, 53
	v_writelane_b32 v253, s78, 54
	s_nop 1
	v_writelane_b32 v253, s79, 55
	v_writelane_b32 v253, s80, 56
	s_nop 1
	v_writelane_b32 v253, s81, 57
	v_writelane_b32 v253, s75, 58
	v_writelane_b32 v253, s82, 59
	s_nop 1
	v_writelane_b32 v253, s83, 60
	v_writelane_b32 v253, s84, 61
	s_nop 1
	v_writelane_b32 v253, s85, 62
	v_writelane_b32 v253, s86, 63
	s_nop 1
	v_writelane_b32 v254, s87, 0
	v_writelane_b32 v254, s88, 1
	s_nop 1
	v_writelane_b32 v254, s89, 2
	v_writelane_b32 v254, s90, 3
	s_nop 1
	v_writelane_b32 v254, s91, 4
	v_writelane_b32 v254, s92, 5
	v_writelane_b32 v254, s93, 6
	v_writelane_b32 v254, s94, 7
	v_writelane_b32 v254, s95, 8
	v_writelane_b32 v254, s64, 9
	v_writelane_b32 v254, s65, 10
	s_branch .LBB0_79

; __global__ void __launch_bounds__(512, 2) fwd_kernel(Args args) {
;     ...
;             PHASE_BEGIN(16) {
;                 { pg8::Gemm g{proj, wb + WB_W1T, 16 * PLD, 2048, 2048, (unsigned)PLD * 2}; pg8::Sched S; S.init(16, 1, c.G, c.bid, 1, 0, 0, 0, 0); S.mode = 1;
;                   pg8::EpiCmp1 E{hidb, (const float*)(wb + WB_BH)}; pg8::gemm_phase(c.lds, c.tid, g, S, E); }
.LBB0_473:
	s_andn2_b64 vcc, exec, s[0:1]
	s_cbranch_vccnz .LBB0_553
	v_readlane_b32 s0, v251, 5
	v_mbcnt_lo_u32_b32 v0, -1, 0
	v_mbcnt_hi_u32_b32 v0, -1, v0
	v_readlane_b32 s14, v251, 0
	s_nop 0
	v_or_b32_e32 v151, s0, v0
	s_cmp_gt_i32 s14, 63
	v_readfirstlane_b32 s15, v151
	s_cbranch_scc1 .LBB0_494
	s_ashr_i32 s16, s14, 31
	s_lshr_b32 s0, s16, 29
	s_and_b32 s3, s14, 15
	s_and_b32 s0, s3, -8
	s_sub_i32 s4, s3, s0
	s_cmp_gt_i32 s4, -1
	s_mov_b64 s[0:1], -1
	s_cbranch_scc0 .LBB0_477
	s_lshl_b32 s2, s4, 1
	s_mov_b64 s[0:1], 0

; #define PG8_STAGE(bufoff, gbase, voff) do { _Pragma("unroll") for (int _i = 0; _i < 2; ++_i) \
;         __builtin_amdgcn_global_load_lds((const unsigned*)((const char*)(gbase) + (voff)[_i]), (LAS unsigned*)(lds + (bufoff) + ldsw + _i * 8192), 16, 0, 0); } while (0)
; #define PG8_WAIT_V(n) asm volatile("s_waitcnt vmcnt(" #n ")" ::: "memory")
; #define PG8_BAR __builtin_amdgcn_s_barrier()
; template <class Epi>
; __device__ __forceinline__ void gemm_phase(LAS unsigned char* lds, const int tid, const Gemm g, const Sched& S, const Epi& E) {
;     const int wid = __builtin_amdgcn_readfirstlane(tid >> 6), lane = tid & 63, wr = wid >> 2, wc = wid & 3, fr = lane & 15, fq = lane >> 4;
;     const int K = g.K, nt = K / BK;
;     unsigned voffA[2], voffB[2];
; #pragma unroll
;     for (int i = 0; i < 2; ++i) { int R, C; stage_rc(tid * 16 + i * 8192, R, C); const int Rb = Epi::PERM ? ((R & ~31) + perm32(R & 31)) : R;
;         voffA[i] = (unsigned)(R * g.lda + C) * 2u; voffB[i] = (unsigned)(Rb * g.ldb + C) * 2u; }
;     const size_t kstep = (size_t)(BK * 2), kstA = g.kstepA;
;     const size_t hstepA = (size_t)HALF * g.lda * 2, hstepB = (size_t)HALF * g.ldb * 2;
;     const unsigned ldsw = (unsigned)wid * 1024u;
;     const int aoff = lds_byte(wr * 64 + fr, fq * 8), boff = lds_byte(wc * 32 + fr, fq * 8);
;     ...
;     Unit cur, nxt; int ui = 0;
;     if (!S.next(0, cur)) return;
;     f32x4 acc[2][2][4][2];
; #pragma unroll
;     for (int a = 0; a < 2; ++a)
; #pragma unroll
;         for (int b = 0; b < 2; ++b)
; #pragma unroll
;             for (int m = 0; m < 4; ++m)
; #pragma unroll
;                 for (int n = 0; n < 2; ++n) acc[a][b][m][n] = (f32x4){0.f, 0.f, 0.f, 0.f};
;     bf16x8 At[4][2], B0[2][2], B1[2][2];
;     const char* cA = (const char*)g.A + cur.aoff; const char* cB = (const char*)g.Bt + cur.boff;
;     PG8_STAGE(PG8_SB(0, 0), cB, voffB); PG8_STAGE(PG8_SA(0, 0), cA, voffA); PG8_STAGE(PG8_SB(0, 1), cB + hstepB, voffB); PG8_STAGE(PG8_SA(0, 1), cA + hstepA, voffA);
;     if (wr == 1) PG8_BAR;
;     PG8_WAIT_V(4); PG8_BAR;
;     PG8_STAGE(PG8_SB(1, 0), cB + kstep, voffB); PG8_STAGE(PG8_SA(1, 0), cA + kstA, voffA); PG8_STAGE(PG8_SB(1, 1), cB + hstepB + kstep, voffB);
;     PG8_WAIT_V(6); PG8_BAR;
.LBB0_479:
	v_ashrrev_i32_e32 v2, 31, v151
	v_lshrrev_b32_e32 v2, 26, v2
	v_add_u32_e32 v2, v151, v2
	v_ashrrev_i32_e32 v6, 6, v2
	v_bfe_i32 v2, v151, 27, 1
	v_lshlrev_b32_e32 v0, 4, v151
	v_lshrrev_b32_e32 v2, 22, v2
	v_add_u32_e32 v2, v0, v2
	v_and_b32_e32 v2, 0xfffffc00, v2
	v_sub_u32_e32 v2, v0, v2
	v_lshrrev_b32_e32 v3, 4, v2
	v_bitop3_b32 v2, v3, v2, 32 bitop3:0x6c
	v_ashrrev_i32_e32 v4, 31, v2
	v_lshrrev_b32_e32 v4, 26, v4
	v_add_u32_e32 v4, v2, v4
	v_lshlrev_b32_e32 v3, 3, v6
	v_ashrrev_i32_e32 v7, 6, v4
	v_and_b32_e32 v4, 0xc0, v4
	v_and_b32_e32 v3, -16, v3
	v_sub_u32_e32 v2, v2, v4
	v_mov_b32_e32 v11, 1
	v_add_u32_e32 v3, v7, v3
	v_ashrrev_i16_sdwa v2, v11, sext(v2) dst_sel:DWORD dst_unused:UNUSED_PAD src0_sel:DWORD src1_sel:BYTE_0
	v_lshlrev_b32_e32 v5, 5, v6
	v_bfe_i32 v8, v2, 0, 16
	v_lshlrev_b32_e32 v2, 1, v3
	v_lshrrev_b32_e32 v4, 2, v3
	v_and_b32_e32 v9, 3, v7
	s_mov_b32 s1, 0xfffe0
	v_and_b32_e32 v5, 32, v5
	v_and_b32_e32 v2, 24, v2
	v_and_b32_e32 v4, 4, v4
	v_and_or_b32 v9, v3, s1, v9
	v_or3_b32 v2, v9, v4, v2
	v_add_lshl_u32 v4, v5, v8, 1
	v_add_u32_e32 v0, 0x2000, v0
	v_lshl_add_u32 v144, v2, 12, v4
	v_ashrrev_i32_e32 v2, 31, v0
	v_lshrrev_b32_e32 v2, 22, v2
	v_add_u32_e32 v2, v0, v2
	v_ashrrev_i32_e32 v9, 10, v2
	v_mul_i32_i24_e32 v2, 0x400, v9
	v_sub_u32_e32 v0, v0, v2
	v_lshrrev_b32_e32 v2, 4, v0
	v_bitop3_b32 v0, v2, v0, 32 bitop3:0x6c
	s_add_i32 s22, s2, s3
	v_lshl_add_u32 v142, v3, 17, v4
	v_ashrrev_i32_e32 v3, 31, v0
	s_ashr_i32 s2, s22, 31
	v_lshrrev_b32_e32 v3, 26, v3
	s_lshr_b32 s2, s2, 29
	v_lshlrev_b32_e32 v2, 3, v9
	v_add_u32_e32 v3, v0, v3
	s_add_i32 s2, s22, s2
	v_and_b32_e32 v2, -16, v2
	v_ashrrev_i32_e32 v10, 6, v3
	s_and_b32 s2, s2, -8
	v_add_u32_e32 v2, v10, v2
	v_and_b32_e32 v5, 3, v10
	s_sub_i32 s2, s22, s2
	v_and_or_b32 v5, v2, s1, v5
	s_ashr_i32 s1, s15, 6
	s_lshl_b32 s3, s2, 25
	s_ashr_i32 s0, s15, 8
	s_lshl_b32 s17, s1, 10
	s_and_b32 s3, s3, 0x6000000
	s_cmp_lt_u32 s22, 8
	s_movk_i32 s4, 0x1200
	s_cselect_b32 s4, s4, 0x1300
	s_lshl_b32 s2, s2, 5
	s_and_b32 s2, s2, 0x80
	v_and_b32_e32 v3, 0xc0, v3
	s_or_b32 s2, s2, s3
	s_lshl_b32 s3, s22, 17
	v_sub_u32_e32 v0, v0, v3
	s_or_b32 s2, s2, s4
	s_and_b32 s3, s3, 0xfff00000
	v_readlane_b32 s4, v251, 10
	v_ashrrev_i16_sdwa v0, v11, sext(v0) dst_sel:DWORD dst_unused:UNUSED_PAD src0_sel:DWORD src1_sel:BYTE_0
	s_add_u32 s6, s4, s3
	v_readlane_b32 s3, v251, 11
	v_lshlrev_b32_e32 v4, 5, v9
	v_bfe_i32 v11, v0, 0, 16
	v_lshlrev_b32_e32 v0, 1, v2
	v_lshrrev_b32_e32 v3, 2, v2
	s_addc_u32 s7, s3, 0
	s_lshr_b32 s3, s14, 4
	s_lshl_b32 s3, s3, 10
	s_add_u32 s6, s6, s3
	s_addc_u32 s7, s7, 0
	s_add_i32 s20, s17, 0
	v_and_b32_e32 v4, 32, v4
	v_and_b32_e32 v0, 24, v0
	v_and_b32_e32 v3, 4, v3
	s_add_i32 m0, s20, 0x10000
	v_or3_b32 v0, v5, v3, v0
	v_add_lshl_u32 v3, v4, v11, 1
	global_load_lds_dwordx4 v144, s[6:7]
	s_add_i32 m0, s20, 0x12000
	v_lshl_add_u32 v148, v0, 12, v3
	s_add_u32 s8, s80, s2
	global_load_lds_dwordx4 v148, s[6:7]
	s_addc_u32 s9, s81, 0
	s_lshr_b32 s3, s14, 4
	s_lshl_b32 s3, s3, 16
	s_add_u32 s8, s8, s3
	s_addc_u32 s9, s9, 0
	s_mov_b32 m0, s20
	s_add_i32 s21, s20, 0x2000
	v_lshl_add_u32 v146, v2, 17, v3
	global_load_lds_dwordx4 v142, s[8:9]
	s_mov_b32 m0, s21
	s_add_u32 s2, s6, 0x80000
	global_load_lds_dwordx4 v146, s[8:9]
	s_addc_u32 s3, s7, 0
	s_add_i32 m0, s20, 0x14000
	v_mov_b32_e32 v145, v1
	global_load_lds_dwordx4 v144, s[2:3]
	s_add_i32 m0, s20, 0x16000
	v_mov_b32_e32 v149, v1
	global_load_lds_dwordx4 v148, s[2:3]
	s_add_u32 s2, s8, 0x1000000
	s_addc_u32 s3, s9, 0
	s_add_i32 s26, s20, 0x4000
	s_mov_b32 m0, s26
	s_add_i32 s27, s20, 0x6000
	global_load_lds_dwordx4 v142, s[2:3]
	s_mov_b32 m0, s27
	v_lshl_add_u64 v[2:3], s[6:7], 0, v[144:145]
	global_load_lds_dwordx4 v146, s[2:3]
	s_cmp_lg_u32 s0, 1
	v_lshl_add_u64 v[4:5], s[6:7], 0, v[148:149]
	s_cbranch_scc1 .LBB0_481
	s_barrier

; #define PG8_STAGE(bufoff, gbase, voff) do { _Pragma("unroll") for (int _i = 0; _i < 2; ++_i) \
;         __builtin_amdgcn_global_load_lds((const unsigned*)((const char*)(gbase) + (voff)[_i]), (LAS unsigned*)(lds + (bufoff) + ldsw + _i * 8192), 16, 0, 0); } while (0)
; #define PG8_LDA(dst, b, h) do { _Pragma("unroll") for (int m = 0; m < 4; ++m) _Pragma("unroll") for (int k = 0; k < 2; ++k) dst[m][k] = *(const LAS bf16x8*)(lds + PG8_SA(b, h) + aoff + m * 2048 + k * 1024); } while (0)
; #define PG8_LDB(dst, b, h) do { _Pragma("unroll") for (int n = 0; n < 2; ++n) _Pragma("unroll") for (int k = 0; k < 2; ++k) dst[n][k] = *(const LAS bf16x8*)(lds + PG8_SB(b, h) + boff + n * 2048 + k * 1024); } while (0)
; #define PG8_WAIT_L(n) asm volatile("s_waitcnt lgkmcnt(" #n ")" ::: "memory")
; #define PG8_BAR __builtin_amdgcn_s_barrier()
; #define PG8_SCHED __builtin_amdgcn_sched_barrier(0)
; template <class Epi>
; __device__ __forceinline__ void gemm_phase(LAS unsigned char* lds, const int tid, const Gemm g, const Sched& S, const Epi& E) {
;     ...
;         const bool has_next = S.next(ui + 1, nxt);
;         const char* nA = has_next ? (const char*)g.A + nxt.aoff : cA; const char* nB = has_next ? (const char*)g.Bt + nxt.boff : cB;
;         for (int t = 0; t < nt; t += 2) {
;             const bool last = (t == nt - 2);
;             const char* a1 = cA + (size_t)(t + 1) * kstA;
;             const char* a2 = last ? nA : cA + (size_t)(t + 2) * kstA; const char* b2 = last ? nB : cB + (size_t)(t + 2) * kstep;
;             const char* a3 = a2 + kstA; const char* b3 = b2 + kstep;
;             PG8_LDB(B0, 0, 0); PG8_SCHED; PG8_LDA(At, 0, 0); PG8_STAGE(PG8_SA(1, 1), a1 + hstepA, voffA);
;             PG8_WAIT_L(8); PG8_BAR; PG8_WAIT_L(0); PG8_MMA(0, 0, At, B0); PG8_BAR; PG8_SCHED;
;             PG8_LDB(B1, 0, 1); PG8_STAGE(PG8_SB(0, 0), b2, voffB);
;             PG8_BAR; PG8_WAIT_L(0); PG8_MMA(0, 1, At, B1); PG8_BAR;
;     ...
;         if (!keep) {
; #pragma unroll
;             for (int a = 0; a < 2; ++a)
; #pragma unroll
;                 for (int b = 0; b < 2; ++b)
; #pragma unroll
;                     for (int m = 0; m < 4; ++m)
; #pragma unroll
;                         for (int n = 0; n < 2; ++n) acc[a][b][m][n] = (f32x4){0.f, 0.f, 0.f, 0.f};
;         }
.LBB0_488:
	v_cmp_lt_i64_e64 s[10:11], s[2:3], 16
	s_add_u32 s2, s80, s38
	s_addc_u32 s3, s81, 0
	s_and_b64 s[4:5], s[10:11], exec
	v_readlane_b32 s4, v251, 10
	s_cselect_b32 s42, s3, s9
	s_cselect_b32 s46, s2, s8
	s_add_u32 s4, s4, s39
	v_readlane_b32 s5, v251, 11
	s_addc_u32 s5, s5, 0
	s_and_b64 s[10:11], s[10:11], exec
	s_cselect_b32 s47, s5, s7
	s_cselect_b32 s48, s4, s6
	s_add_u32 s49, s6, 0x100
	s_addc_u32 s50, s7, 0
	s_add_u32 s6, s8, 0x1002000
	v_mov_b32_e32 v2, 0
	s_addc_u32 s7, s9, 0
	s_mov_b32 s51, 22
	v_mov_b32_e32 v3, v2
	v_mov_b32_e32 v4, v2
	v_mov_b32_e32 v5, v2
	v_mov_b32_e32 v6, v2
	v_mov_b32_e32 v7, v2
	v_mov_b32_e32 v8, v2
	v_mov_b32_e32 v9, v2
	v_mov_b32_e32 v18, v2
	v_mov_b32_e32 v19, v2
	v_mov_b32_e32 v20, v2
	v_mov_b32_e32 v21, v2
	v_mov_b32_e32 v22, v2
	v_mov_b32_e32 v23, v2
	v_mov_b32_e32 v24, v2
	v_mov_b32_e32 v25, v2
	v_mov_b32_e32 v34, v2
	v_mov_b32_e32 v35, v2
	v_mov_b32_e32 v36, v2
	v_mov_b32_e32 v37, v2
	v_mov_b32_e32 v42, v2
	v_mov_b32_e32 v43, v2
	v_mov_b32_e32 v44, v2
	v_mov_b32_e32 v45, v2
	v_mov_b32_e32 v62, v2
	v_mov_b32_e32 v63, v2
	v_mov_b32_e32 v64, v2
	v_mov_b32_e32 v65, v2
	v_mov_b32_e32 v70, v2
	v_mov_b32_e32 v71, v2
	v_mov_b32_e32 v72, v2
	v_mov_b32_e32 v73, v2
	v_mov_b32_e32 v10, v2
	v_mov_b32_e32 v11, v2
	v_mov_b32_e32 v12, v2
	v_mov_b32_e32 v13, v2
	v_mov_b32_e32 v14, v2
	v_mov_b32_e32 v15, v2
	v_mov_b32_e32 v16, v2
	v_mov_b32_e32 v17, v2
	v_mov_b32_e32 v26, v2
	v_mov_b32_e32 v27, v2
	v_mov_b32_e32 v28, v2
	v_mov_b32_e32 v29, v2
	v_mov_b32_e32 v30, v2
	v_mov_b32_e32 v31, v2
	v_mov_b32_e32 v32, v2
	v_mov_b32_e32 v33, v2
	v_mov_b32_e32 v50, v2
	v_mov_b32_e32 v51, v2
	v_mov_b32_e32 v52, v2
	v_mov_b32_e32 v53, v2
	v_mov_b32_e32 v58, v2
	v_mov_b32_e32 v59, v2
	v_mov_b32_e32 v60, v2
	v_mov_b32_e32 v61, v2
	v_mov_b32_e32 v74, v2
	v_mov_b32_e32 v75, v2
	v_mov_b32_e32 v76, v2
	v_mov_b32_e32 v77, v2
	v_mov_b32_e32 v78, v2
	v_mov_b32_e32 v79, v2
	v_mov_b32_e32 v80, v2
	v_mov_b32_e32 v81, v2
	v_mov_b32_e32 v82, v2
	v_mov_b32_e32 v83, v2
	v_mov_b32_e32 v84, v2
	v_mov_b32_e32 v85, v2
	v_mov_b32_e32 v86, v2
	v_mov_b32_e32 v87, v2
	v_mov_b32_e32 v88, v2
	v_mov_b32_e32 v89, v2
	v_mov_b32_e32 v98, v2
	v_mov_b32_e32 v99, v2
	v_mov_b32_e32 v100, v2
	v_mov_b32_e32 v101, v2
	v_mov_b32_e32 v102, v2
	v_mov_b32_e32 v103, v2
	v_mov_b32_e32 v104, v2
	v_mov_b32_e32 v105, v2
	v_mov_b32_e32 v114, v2
	v_mov_b32_e32 v115, v2
	v_mov_b32_e32 v116, v2
	v_mov_b32_e32 v117, v2
	v_mov_b32_e32 v118, v2
	v_mov_b32_e32 v119, v2
	v_mov_b32_e32 v120, v2
	v_mov_b32_e32 v121, v2
	v_mov_b32_e32 v130, v2
	v_mov_b32_e32 v131, v2
	v_mov_b32_e32 v132, v2
	v_mov_b32_e32 v133, v2
	v_mov_b32_e32 v134, v2
	v_mov_b32_e32 v135, v2
	v_mov_b32_e32 v136, v2
	v_mov_b32_e32 v137, v2
	v_mov_b32_e32 v90, v2
	v_mov_b32_e32 v91, v2
	v_mov_b32_e32 v92, v2
	v_mov_b32_e32 v93, v2
	v_mov_b32_e32 v94, v2
	v_mov_b32_e32 v95, v2
	v_mov_b32_e32 v96, v2
	v_mov_b32_e32 v97, v2
	v_mov_b32_e32 v106, v2
	v_mov_b32_e32 v107, v2
	v_mov_b32_e32 v108, v2
	v_mov_b32_e32 v109, v2
	v_mov_b32_e32 v110, v2
	v_mov_b32_e32 v111, v2
	v_mov_b32_e32 v112, v2
	v_mov_b32_e32 v113, v2
	v_mov_b32_e32 v122, v2
	v_mov_b32_e32 v123, v2
	v_mov_b32_e32 v124, v2
	v_mov_b32_e32 v125, v2
	v_mov_b32_e32 v126, v2
	v_mov_b32_e32 v127, v2
	v_mov_b32_e32 v128, v2
	v_mov_b32_e32 v129, v2
	v_mov_b32_e32 v38, v2
	v_mov_b32_e32 v39, v2
	v_mov_b32_e32 v40, v2
	v_mov_b32_e32 v41, v2
	v_mov_b32_e32 v66, v2
	v_mov_b32_e32 v67, v2
	v_mov_b32_e32 v68, v2
	v_mov_b32_e32 v69, v2
.LBB0_489:
	s_add_u32 s8, s6, 0xff002000
	s_addc_u32 s9, s7, -1
	s_cmp_eq_u32 s51, 28
	s_cselect_b32 s12, s46, s8
	s_cselect_b32 s13, s42, s9
	s_cselect_b32 s8, s48, s49
	s_cselect_b32 s9, s47, s50
	s_add_u32 s10, s12, 0x2000
	s_addc_u32 s11, s13, 0
	s_add_i32 s52, 0, 0x10000
	v_add_u32_e32 v0, s52, v165
	ds_read_b128 v[46:49], v0
	ds_read_b128 v[54:57], v0 offset:1024
	ds_read_b128 v[138:141], v0 offset:2048
	ds_read_b128 v[158:161], v0 offset:3072
	v_lshl_add_u64 v[162:163], s[6:7], 0, v[154:155]
	s_add_i32 m0, s20, 0xc000
	ds_read_b128 v[168:171], v166
	ds_read_b128 v[172:175], v166 offset:1024
	ds_read_b128 v[176:179], v166 offset:2048
	ds_read_b128 v[180:183], v166 offset:3072
	ds_read_b128 v[196:199], v166 offset:4096
	ds_read_b128 v[200:203], v166 offset:5120
	ds_read_b128 v[204:207], v166 offset:6144
	ds_read_b128 v[208:211], v166 offset:7168
	global_load_lds_dwordx4 v[162:163], off
	v_lshl_add_u64 v[162:163], s[6:7], 0, v[156:157]
	s_add_i32 m0, s20, 0xe000
	s_nop 0
	global_load_lds_dwordx4 v[162:163], off
	s_waitcnt lgkmcnt(8)
	s_barrier
	s_waitcnt lgkmcnt(0)
	s_setprio 1
	s_waitcnt lgkmcnt(0)
	v_mfma_f32_16x16x32_bf16 v[66:69], v[46:49], v[168:171], v[66:69]
	v_mfma_f32_16x16x32_bf16 v[38:41], v[138:141], v[168:171], v[38:41]
	v_mfma_f32_16x16x32_bf16 v[126:129], v[46:49], v[176:179], v[126:129]
	v_mfma_f32_16x16x32_bf16 v[122:125], v[138:141], v[176:179], v[122:125]
	v_mfma_f32_16x16x32_bf16 v[110:113], v[46:49], v[196:199], v[110:113]
	v_mfma_f32_16x16x32_bf16 v[106:109], v[138:141], v[196:199], v[106:109]
	v_mfma_f32_16x16x32_bf16 v[94:97], v[46:49], v[204:207], v[94:97]
	v_mfma_f32_16x16x32_bf16 v[90:93], v[138:141], v[204:207], v[90:93]
	v_mfma_f32_16x16x32_bf16 v[66:69], v[54:57], v[172:175], v[66:69]
	v_mfma_f32_16x16x32_bf16 v[38:41], v[158:161], v[172:175], v[38:41]
	v_mfma_f32_16x16x32_bf16 v[126:129], v[54:57], v[180:183], v[126:129]
	v_mfma_f32_16x16x32_bf16 v[122:125], v[158:161], v[180:183], v[122:125]
	v_mfma_f32_16x16x32_bf16 v[110:113], v[54:57], v[200:203], v[110:113]
	v_mfma_f32_16x16x32_bf16 v[106:109], v[158:161], v[200:203], v[106:109]
	v_mfma_f32_16x16x32_bf16 v[94:97], v[54:57], v[208:211], v[94:97]
	v_mfma_f32_16x16x32_bf16 v[90:93], v[158:161], v[208:211], v[90:93]
	s_setprio 0
	s_barrier
; #define PG8_STAGE(bufoff, gbase, voff) do { _Pragma("unroll") for (int _i = 0; _i < 2; ++_i) \
;         __builtin_amdgcn_global_load_lds((const unsigned*)((const char*)(gbase) + (voff)[_i]), (LAS unsigned*)(lds + (bufoff) + ldsw + _i * 8192), 16, 0, 0); } while (0)
; #define PG8_LDA(dst, b, h) do { _Pragma("unroll") for (int m = 0; m < 4; ++m) _Pragma("unroll") for (int k = 0; k < 2; ++k) dst[m][k] = *(const LAS bf16x8*)(lds + PG8_SA(b, h) + aoff + m * 2048 + k * 1024); } while (0)
; #define PG8_LDB(dst, b, h) do { _Pragma("unroll") for (int n = 0; n < 2; ++n) _Pragma("unroll") for (int k = 0; k < 2; ++k) dst[n][k] = *(const LAS bf16x8*)(lds + PG8_SB(b, h) + boff + n * 2048 + k * 1024); } while (0)
; #define PG8_MMA(ai, bj, At, Bt) do { __builtin_amdgcn_s_setprio(1); _Pragma("unroll") for (int m = 0; m < 4; ++m) _Pragma("unroll") for (int n = 0; n < 2; ++n) _Pragma("unroll") for (int k = 0; k < 2; ++k) \
;         acc[ai][bj][m][n] = __builtin_amdgcn_mfma_f32_16x16x32_bf16(Bt[n][k], At[m][k], acc[ai][bj][m][n], 0, 0, 0); __builtin_amdgcn_s_setprio(0); } while (0)
; #define PG8_WAIT_V(n) asm volatile("s_waitcnt vmcnt(" #n ")" ::: "memory")
; #define PG8_WAIT_L(n) asm volatile("s_waitcnt lgkmcnt(" #n ")" ::: "memory")
; #define PG8_BAR __builtin_amdgcn_s_barrier()
; #define PG8_SCHED __builtin_amdgcn_sched_barrier(0)
; template <class Epi>
; __device__ __forceinline__ void gemm_phase(LAS unsigned char* lds, const int tid, const Gemm g, const Sched& S, const Epi& E) {
;     ...
;             PG8_LDB(B1, 0, 1); PG8_STAGE(PG8_SB(0, 0), b2, voffB);
;             PG8_BAR; PG8_WAIT_L(0); PG8_MMA(0, 1, At, B1); PG8_BAR;
;             PG8_LDA(At, 0, 1); PG8_STAGE(PG8_SA(0, 0), a2, voffA);
;             PG8_BAR; PG8_WAIT_L(0); PG8_MMA(1, 0, At, B0); PG8_BAR; PG8_SCHED;
;             PG8_STAGE(PG8_SB(0, 1), b2 + hstepB, voffB);
;             PG8_WAIT_V(6); PG8_BAR; PG8_MMA(1, 1, At, B1); PG8_BAR;
;             PG8_LDB(B0, 1, 0); PG8_SCHED; PG8_LDA(At, 1, 0); PG8_STAGE(PG8_SA(0, 1), a2 + hstepA, voffA);
;             PG8_WAIT_L(8); PG8_BAR; PG8_WAIT_L(0); PG8_MMA(0, 0, At, B0); PG8_BAR; PG8_SCHED;
;             PG8_LDB(B1, 1, 1); PG8_STAGE(PG8_SB(1, 0), b3, voffB);
;             PG8_BAR; PG8_WAIT_L(0); PG8_MMA(0, 1, At, B1); PG8_BAR;
	s_add_i32 s54, 0, 0x14000
	s_add_i32 s52, s52, s17
	v_add_u32_e32 v0, s54, v165
	v_lshl_add_u64 v[162:163], s[8:9], 0, v[144:145]
	s_mov_b32 m0, s52
	ds_read_b128 v[212:215], v0
	ds_read_b128 v[216:219], v0 offset:1024
	ds_read_b128 v[220:223], v0 offset:2048
	ds_read_b128 v[224:227], v0 offset:3072
	global_load_lds_dwordx4 v[162:163], off
	v_lshl_add_u64 v[184:185], s[8:9], 0, v[148:149]
	s_add_i32 m0, s52, 0x2000
	s_nop 0
	global_load_lds_dwordx4 v[184:185], off
	s_barrier
	s_waitcnt lgkmcnt(0)
	s_setprio 1
	s_waitcnt lgkmcnt(0)
	v_mfma_f32_16x16x32_bf16 v[134:137], v[212:215], v[168:171], v[134:137]
	v_mfma_f32_16x16x32_bf16 v[130:133], v[220:223], v[168:171], v[130:133]
	v_mfma_f32_16x16x32_bf16 v[118:121], v[212:215], v[176:179], v[118:121]
	v_mfma_f32_16x16x32_bf16 v[114:117], v[220:223], v[176:179], v[114:117]
	v_mfma_f32_16x16x32_bf16 v[102:105], v[212:215], v[196:199], v[102:105]
	v_mfma_f32_16x16x32_bf16 v[98:101], v[220:223], v[196:199], v[98:101]
	v_mfma_f32_16x16x32_bf16 v[86:89], v[212:215], v[204:207], v[86:89]
	v_mfma_f32_16x16x32_bf16 v[82:85], v[220:223], v[204:207], v[82:85]
	v_mfma_f32_16x16x32_bf16 v[134:137], v[216:219], v[172:175], v[134:137]
	v_mfma_f32_16x16x32_bf16 v[130:133], v[224:227], v[172:175], v[130:133]
	v_mfma_f32_16x16x32_bf16 v[118:121], v[216:219], v[180:183], v[118:121]
	v_mfma_f32_16x16x32_bf16 v[114:117], v[224:227], v[180:183], v[114:117]
	v_mfma_f32_16x16x32_bf16 v[102:105], v[216:219], v[200:203], v[102:105]
	v_mfma_f32_16x16x32_bf16 v[98:101], v[224:227], v[200:203], v[98:101]
	v_mfma_f32_16x16x32_bf16 v[86:89], v[216:219], v[208:211], v[86:89]
	v_mfma_f32_16x16x32_bf16 v[82:85], v[224:227], v[208:211], v[82:85]
	s_setprio 0
	s_mov_b32 m0, s20
	v_lshl_add_u64 v[228:229], s[12:13], 0, v[142:143]
	s_barrier
	ds_read_b128 v[168:171], v166 offset:16384
	ds_read_b128 v[172:175], v166 offset:17408
	ds_read_b128 v[176:179], v166 offset:18432
	ds_read_b128 v[180:183], v166 offset:19456
	ds_read_b128 v[196:199], v166 offset:20480
	ds_read_b128 v[200:203], v166 offset:21504
	ds_read_b128 v[204:207], v166 offset:22528
	ds_read_b128 v[208:211], v166 offset:23552
	global_load_lds_dwordx4 v[228:229], off
	v_lshl_add_u64 v[228:229], s[12:13], 0, v[146:147]
	s_mov_b32 m0, s21
	s_nop 0
	global_load_lds_dwordx4 v[228:229], off
	s_barrier
	s_waitcnt lgkmcnt(0)
	s_setprio 1
	s_waitcnt lgkmcnt(0)
	v_mfma_f32_16x16x32_bf16 v[78:81], v[46:49], v[168:171], v[78:81]
	v_mfma_f32_16x16x32_bf16 v[74:77], v[138:141], v[168:171], v[74:77]
	v_mfma_f32_16x16x32_bf16 v[58:61], v[46:49], v[176:179], v[58:61]
	v_mfma_f32_16x16x32_bf16 v[50:53], v[138:141], v[176:179], v[50:53]
	v_mfma_f32_16x16x32_bf16 v[30:33], v[46:49], v[196:199], v[30:33]
	v_mfma_f32_16x16x32_bf16 v[26:29], v[138:141], v[196:199], v[26:29]
	v_mfma_f32_16x16x32_bf16 v[14:17], v[46:49], v[204:207], v[14:17]
	v_mfma_f32_16x16x32_bf16 v[10:13], v[138:141], v[204:207], v[10:13]
	v_mfma_f32_16x16x32_bf16 v[78:81], v[54:57], v[172:175], v[78:81]
	v_mfma_f32_16x16x32_bf16 v[74:77], v[158:161], v[172:175], v[74:77]
	v_mfma_f32_16x16x32_bf16 v[58:61], v[54:57], v[180:183], v[58:61]
	v_mfma_f32_16x16x32_bf16 v[50:53], v[158:161], v[180:183], v[50:53]
	v_mfma_f32_16x16x32_bf16 v[30:33], v[54:57], v[200:203], v[30:33]
	v_mfma_f32_16x16x32_bf16 v[26:29], v[158:161], v[200:203], v[26:29]
	v_mfma_f32_16x16x32_bf16 v[14:17], v[54:57], v[208:211], v[14:17]
	v_mfma_f32_16x16x32_bf16 v[10:13], v[158:161], v[208:211], v[10:13]
	s_setprio 0
	s_barrier
	s_add_u32 s52, s8, 0x80000
	s_addc_u32 s53, s9, 0
	s_add_i32 s54, s54, s17
	v_lshl_add_u64 v[46:47], s[52:53], 0, v[144:145]
	s_mov_b32 m0, s54
	s_nop 0
	global_load_lds_dwordx4 v[46:47], off
	v_lshl_add_u64 v[46:47], s[52:53], 0, v[148:149]
	s_add_i32 m0, s54, 0x2000
	s_nop 0
	global_load_lds_dwordx4 v[46:47], off
	s_waitcnt vmcnt(6)
	s_barrier
	s_setprio 1
	v_mfma_f32_16x16x32_bf16 v[42:45], v[212:215], v[176:179], v[42:45]
	v_mfma_f32_16x16x32_bf16 v[34:37], v[220:223], v[176:179], v[34:37]
	v_mfma_f32_16x16x32_bf16 v[22:25], v[212:215], v[196:199], v[22:25]
	v_mfma_f32_16x16x32_bf16 v[18:21], v[220:223], v[196:199], v[18:21]
	v_mfma_f32_16x16x32_bf16 v[6:9], v[212:215], v[204:207], v[6:9]
	v_mfma_f32_16x16x32_bf16 v[2:5], v[220:223], v[204:207], v[2:5]
	v_mfma_f32_16x16x32_bf16 v[46:49], v[212:215], v[168:171], v[70:73]
	v_mfma_f32_16x16x32_bf16 v[54:57], v[220:223], v[168:171], v[62:65]
	v_mfma_f32_16x16x32_bf16 v[42:45], v[216:219], v[180:183], v[42:45]
	v_mfma_f32_16x16x32_bf16 v[34:37], v[224:227], v[180:183], v[34:37]
	v_mfma_f32_16x16x32_bf16 v[22:25], v[216:219], v[200:203], v[22:25]
	v_mfma_f32_16x16x32_bf16 v[18:21], v[224:227], v[200:203], v[18:21]
	v_mfma_f32_16x16x32_bf16 v[6:9], v[216:219], v[208:211], v[6:9]
	v_mfma_f32_16x16x32_bf16 v[2:5], v[224:227], v[208:211], v[2:5]
	v_mfma_f32_16x16x32_bf16 v[46:49], v[216:219], v[172:175], v[46:49]
	v_mfma_f32_16x16x32_bf16 v[54:57], v[224:227], v[172:175], v[54:57]
	s_setprio 0
	s_add_i32 s52, 0, 0x18000
	v_add_u32_e32 v0, s52, v165
	s_barrier
	ds_read_b128 v[62:65], v0
	ds_read_b128 v[70:73], v0 offset:1024
	ds_read_b128 v[138:141], v0 offset:2048
	ds_read_b128 v[158:161], v0 offset:3072
	s_add_u32 s12, s12, 0x1000000
	s_addc_u32 s13, s13, 0
	s_mov_b32 m0, s26
	v_lshl_add_u64 v[212:213], s[12:13], 0, v[142:143]
	ds_read_b128 v[168:171], v166 offset:32768
	ds_read_b128 v[172:175], v166 offset:33792
	ds_read_b128 v[176:179], v166 offset:34816
	ds_read_b128 v[180:183], v166 offset:35840
	ds_read_b128 v[196:199], v166 offset:36864
	ds_read_b128 v[200:203], v166 offset:37888
	ds_read_b128 v[204:207], v166 offset:38912
	ds_read_b128 v[208:211], v166 offset:39936
	global_load_lds_dwordx4 v[212:213], off
	v_lshl_add_u64 v[212:213], s[12:13], 0, v[146:147]
	s_mov_b32 m0, s27
	s_nop 0
	global_load_lds_dwordx4 v[212:213], off
	s_waitcnt lgkmcnt(8)
	s_barrier
; #define PG8_STAGE(bufoff, gbase, voff) do { _Pragma("unroll") for (int _i = 0; _i < 2; ++_i) \
;         __builtin_amdgcn_global_load_lds((const unsigned*)((const char*)(gbase) + (voff)[_i]), (LAS unsigned*)(lds + (bufoff) + ldsw + _i * 8192), 16, 0, 0); } while (0)
; #define PG8_LDA(dst, b, h) do { _Pragma("unroll") for (int m = 0; m < 4; ++m) _Pragma("unroll") for (int k = 0; k < 2; ++k) dst[m][k] = *(const LAS bf16x8*)(lds + PG8_SA(b, h) + aoff + m * 2048 + k * 1024); } while (0)
; #define PG8_LDB(dst, b, h) do { _Pragma("unroll") for (int n = 0; n < 2; ++n) _Pragma("unroll") for (int k = 0; k < 2; ++k) dst[n][k] = *(const LAS bf16x8*)(lds + PG8_SB(b, h) + boff + n * 2048 + k * 1024); } while (0)
; #define PG8_MMA(ai, bj, At, Bt) do { __builtin_amdgcn_s_setprio(1); _Pragma("unroll") for (int m = 0; m < 4; ++m) _Pragma("unroll") for (int n = 0; n < 2; ++n) _Pragma("unroll") for (int k = 0; k < 2; ++k) \
;         acc[ai][bj][m][n] = __builtin_amdgcn_mfma_f32_16x16x32_bf16(Bt[n][k], At[m][k], acc[ai][bj][m][n], 0, 0, 0); __builtin_amdgcn_s_setprio(0); } while (0)
; #define PG8_WAIT_V(n) asm volatile("s_waitcnt vmcnt(" #n ")" ::: "memory")
; #define PG8_WAIT_L(n) asm volatile("s_waitcnt lgkmcnt(" #n ")" ::: "memory")
; #define PG8_BAR __builtin_amdgcn_s_barrier()
; #define PG8_SCHED __builtin_amdgcn_sched_barrier(0)
; template <class Epi>
; __device__ __forceinline__ void gemm_phase(LAS unsigned char* lds, const int tid, const Gemm g, const Sched& S, const Epi& E) {
;     ...
;             PG8_LDB(B1, 1, 1); PG8_STAGE(PG8_SB(1, 0), b3, voffB);
;             PG8_BAR; PG8_WAIT_L(0); PG8_MMA(0, 1, At, B1); PG8_BAR;
;             PG8_LDA(At, 1, 1); PG8_STAGE(PG8_SA(1, 0), a3, voffA);
;             PG8_BAR; PG8_WAIT_L(0); PG8_MMA(1, 0, At, B0); PG8_BAR; PG8_SCHED;
;             PG8_STAGE(PG8_SB(1, 1), b3 + hstepB, voffB);
;             PG8_WAIT_V(6); PG8_BAR; PG8_MMA(1, 1, At, B1); PG8_BAR;
	s_waitcnt lgkmcnt(0)
	s_setprio 1
	s_waitcnt lgkmcnt(0)
	v_mfma_f32_16x16x32_bf16 v[66:69], v[62:65], v[168:171], v[66:69]
	v_mfma_f32_16x16x32_bf16 v[38:41], v[138:141], v[168:171], v[38:41]
	v_mfma_f32_16x16x32_bf16 v[126:129], v[62:65], v[176:179], v[126:129]
	v_mfma_f32_16x16x32_bf16 v[122:125], v[138:141], v[176:179], v[122:125]
	v_mfma_f32_16x16x32_bf16 v[110:113], v[62:65], v[196:199], v[110:113]
	v_mfma_f32_16x16x32_bf16 v[106:109], v[138:141], v[196:199], v[106:109]
	v_mfma_f32_16x16x32_bf16 v[94:97], v[62:65], v[204:207], v[94:97]
	v_mfma_f32_16x16x32_bf16 v[90:93], v[138:141], v[204:207], v[90:93]
	v_mfma_f32_16x16x32_bf16 v[66:69], v[70:73], v[172:175], v[66:69]
	v_mfma_f32_16x16x32_bf16 v[38:41], v[158:161], v[172:175], v[38:41]
	v_mfma_f32_16x16x32_bf16 v[126:129], v[70:73], v[180:183], v[126:129]
	v_mfma_f32_16x16x32_bf16 v[122:125], v[158:161], v[180:183], v[122:125]
	v_mfma_f32_16x16x32_bf16 v[110:113], v[70:73], v[200:203], v[110:113]
	v_mfma_f32_16x16x32_bf16 v[106:109], v[158:161], v[200:203], v[106:109]
	v_mfma_f32_16x16x32_bf16 v[94:97], v[70:73], v[208:211], v[94:97]
	v_mfma_f32_16x16x32_bf16 v[90:93], v[158:161], v[208:211], v[90:93]
	s_setprio 0
	s_barrier
	s_add_i32 s12, 0, 0x1c000
	s_add_i32 s13, s52, s17
	v_add_u32_e32 v0, s12, v165
	v_lshl_add_u64 v[162:163], v[162:163], 0, s[44:45]
	s_mov_b32 m0, s13
	ds_read_b128 v[212:215], v0
	ds_read_b128 v[216:219], v0 offset:1024
	ds_read_b128 v[220:223], v0 offset:2048
	ds_read_b128 v[224:227], v0 offset:3072
	global_load_lds_dwordx4 v[162:163], off
	v_lshl_add_u64 v[162:163], v[184:185], 0, s[44:45]
	s_add_i32 m0, s13, 0x2000
	s_nop 0
	global_load_lds_dwordx4 v[162:163], off
	s_barrier
	s_waitcnt lgkmcnt(0)
	s_setprio 1
	s_waitcnt lgkmcnt(0)
	v_mfma_f32_16x16x32_bf16 v[134:137], v[212:215], v[168:171], v[134:137]
	v_mfma_f32_16x16x32_bf16 v[130:133], v[220:223], v[168:171], v[130:133]
	v_mfma_f32_16x16x32_bf16 v[118:121], v[212:215], v[176:179], v[118:121]
	v_mfma_f32_16x16x32_bf16 v[114:117], v[220:223], v[176:179], v[114:117]
	v_mfma_f32_16x16x32_bf16 v[102:105], v[212:215], v[196:199], v[102:105]
	v_mfma_f32_16x16x32_bf16 v[98:101], v[220:223], v[196:199], v[98:101]
	v_mfma_f32_16x16x32_bf16 v[86:89], v[212:215], v[204:207], v[86:89]
	v_mfma_f32_16x16x32_bf16 v[82:85], v[220:223], v[204:207], v[82:85]
	v_mfma_f32_16x16x32_bf16 v[134:137], v[216:219], v[172:175], v[134:137]
	v_mfma_f32_16x16x32_bf16 v[130:133], v[224:227], v[172:175], v[130:133]
	v_mfma_f32_16x16x32_bf16 v[118:121], v[216:219], v[180:183], v[118:121]
	v_mfma_f32_16x16x32_bf16 v[114:117], v[224:227], v[180:183], v[114:117]
	v_mfma_f32_16x16x32_bf16 v[102:105], v[216:219], v[200:203], v[102:105]
	v_mfma_f32_16x16x32_bf16 v[98:101], v[224:227], v[200:203], v[98:101]
	v_mfma_f32_16x16x32_bf16 v[86:89], v[216:219], v[208:211], v[86:89]
	v_mfma_f32_16x16x32_bf16 v[82:85], v[224:227], v[208:211], v[82:85]
	s_setprio 0
	s_mov_b32 m0, s28
	v_lshl_add_u64 v[162:163], s[10:11], 0, v[142:143]
	s_barrier
	ds_read_b128 v[168:171], v166 offset:49152
	ds_read_b128 v[172:175], v166 offset:50176
	ds_read_b128 v[176:179], v166 offset:51200
	ds_read_b128 v[180:183], v166 offset:52224
	ds_read_b128 v[196:199], v166 offset:53248
	ds_read_b128 v[200:203], v166 offset:54272
	ds_read_b128 v[204:207], v166 offset:55296
	ds_read_b128 v[208:211], v166 offset:56320
	global_load_lds_dwordx4 v[162:163], off
	v_lshl_add_u64 v[162:163], s[10:11], 0, v[146:147]
	s_mov_b32 m0, s29
	s_nop 0
	global_load_lds_dwordx4 v[162:163], off
	s_barrier
	s_waitcnt lgkmcnt(0)
	s_setprio 1
	s_waitcnt lgkmcnt(0)
	v_mfma_f32_16x16x32_bf16 v[78:81], v[62:65], v[168:171], v[78:81]
	v_mfma_f32_16x16x32_bf16 v[74:77], v[138:141], v[168:171], v[74:77]
	v_mfma_f32_16x16x32_bf16 v[58:61], v[62:65], v[176:179], v[58:61]
	v_mfma_f32_16x16x32_bf16 v[50:53], v[138:141], v[176:179], v[50:53]
	v_mfma_f32_16x16x32_bf16 v[30:33], v[62:65], v[196:199], v[30:33]
	v_mfma_f32_16x16x32_bf16 v[26:29], v[138:141], v[196:199], v[26:29]
	v_mfma_f32_16x16x32_bf16 v[14:17], v[62:65], v[204:207], v[14:17]
	v_mfma_f32_16x16x32_bf16 v[10:13], v[138:141], v[204:207], v[10:13]
	v_mfma_f32_16x16x32_bf16 v[78:81], v[70:73], v[172:175], v[78:81]
	v_mfma_f32_16x16x32_bf16 v[74:77], v[158:161], v[172:175], v[74:77]
	v_mfma_f32_16x16x32_bf16 v[58:61], v[70:73], v[180:183], v[58:61]
	v_mfma_f32_16x16x32_bf16 v[50:53], v[158:161], v[180:183], v[50:53]
	v_mfma_f32_16x16x32_bf16 v[30:33], v[70:73], v[200:203], v[30:33]
	v_mfma_f32_16x16x32_bf16 v[26:29], v[158:161], v[200:203], v[26:29]
	v_mfma_f32_16x16x32_bf16 v[14:17], v[70:73], v[208:211], v[14:17]
	v_mfma_f32_16x16x32_bf16 v[10:13], v[158:161], v[208:211], v[10:13]
	s_setprio 0
	s_barrier
	s_add_u32 s8, s8, 0x80080
	s_addc_u32 s9, s9, 0
	s_add_i32 s10, s12, s17
	v_lshl_add_u64 v[62:63], s[8:9], 0, v[144:145]
	s_mov_b32 m0, s10
	s_nop 0
	global_load_lds_dwordx4 v[62:63], off
	v_lshl_add_u64 v[62:63], s[8:9], 0, v[148:149]
	s_add_i32 m0, s10, 0x2000
	s_nop 0
	global_load_lds_dwordx4 v[62:63], off
	s_waitcnt vmcnt(6)
	s_barrier
; #define PG8_MMA(ai, bj, At, Bt) do { __builtin_amdgcn_s_setprio(1); _Pragma("unroll") for (int m = 0; m < 4; ++m) _Pragma("unroll") for (int n = 0; n < 2; ++n) _Pragma("unroll") for (int k = 0; k < 2; ++k) \
;         acc[ai][bj][m][n] = __builtin_amdgcn_mfma_f32_16x16x32_bf16(Bt[n][k], At[m][k], acc[ai][bj][m][n], 0, 0, 0); __builtin_amdgcn_s_setprio(0); } while (0)
; #define PG8_WAIT_V(n) asm volatile("s_waitcnt vmcnt(" #n ")" ::: "memory")
; #define PG8_BAR __builtin_amdgcn_s_barrier()
; template <class Epi>
; __device__ __forceinline__ void gemm_phase(LAS unsigned char* lds, const int tid, const Gemm g, const Sched& S, const Epi& E) {
;     ...
;             PG8_WAIT_V(6); PG8_BAR; PG8_MMA(1, 1, At, B1); PG8_BAR;
;         }
;         bool keep = false;
;         if constexpr (!epi_after_drain<Epi>::value) keep = E(acc, cur, wr, wc, fr, fq);
	s_setprio 1
	v_mfma_f32_16x16x32_bf16 v[46:49], v[212:215], v[168:171], v[46:49]
	v_mfma_f32_16x16x32_bf16 v[70:73], v[216:219], v[172:175], v[46:49]
	v_mfma_f32_16x16x32_bf16 v[46:49], v[220:223], v[168:171], v[54:57]
	v_mfma_f32_16x16x32_bf16 v[42:45], v[212:215], v[176:179], v[42:45]
	v_mfma_f32_16x16x32_bf16 v[34:37], v[220:223], v[176:179], v[34:37]
	v_mfma_f32_16x16x32_bf16 v[22:25], v[212:215], v[196:199], v[22:25]
	v_mfma_f32_16x16x32_bf16 v[18:21], v[220:223], v[196:199], v[18:21]
	v_mfma_f32_16x16x32_bf16 v[6:9], v[212:215], v[204:207], v[6:9]
	v_mfma_f32_16x16x32_bf16 v[2:5], v[220:223], v[204:207], v[2:5]
	v_mfma_f32_16x16x32_bf16 v[62:65], v[224:227], v[172:175], v[46:49]
	v_mfma_f32_16x16x32_bf16 v[42:45], v[216:219], v[180:183], v[42:45]
	v_mfma_f32_16x16x32_bf16 v[34:37], v[224:227], v[180:183], v[34:37]
	v_mfma_f32_16x16x32_bf16 v[22:25], v[216:219], v[200:203], v[22:25]
	v_mfma_f32_16x16x32_bf16 v[18:21], v[224:227], v[200:203], v[18:21]
	v_mfma_f32_16x16x32_bf16 v[6:9], v[216:219], v[208:211], v[6:9]
	v_mfma_f32_16x16x32_bf16 v[2:5], v[224:227], v[208:211], v[2:5]
	s_setprio 0
	s_add_i32 s51, s51, 2
	s_add_u32 s49, s49, 0x100
	s_addc_u32 s50, s50, 0
	s_add_u32 s6, s6, 0x4000
	s_addc_u32 s7, s7, 0
	s_cmp_gt_u32 s51, 29
	s_barrier
	s_cbranch_scc0 .LBB0_489
	v_readlane_b32 s6, v251, 0
	s_cmp_lt_u32 s6, 16
	s_cbranch_scc1 .Lsk_A
	v_readlane_b32 s8, v253, 52
	v_readlane_b32 s9, v253, 53
	s_and_b32 s6, s6, 15
	s_lshl_b32 s6, s6, 18
	s_add_u32 s8, s8, s6
	s_addc_u32 s9, s9, 0
	s_add_u32 s8, s8, 0x1af00000
	s_addc_u32 s9, s9, 0
	v_lshlrev_b32_e32 v158, 4, v151
	v_readlane_b32 s6, v251, 0
	s_lshr_b32 s6, s6, 4
	s_add_i32 s6, s6, -1
	s_lshl_b32 s6, s6, 22
	s_add_u32 s8, s8, s6
	s_addc_u32 s9, s9, 0
	global_store_dwordx4 v158, v[2:5], s[8:9] sc0 sc1
	s_add_u32 s8, s8, 0x2000
	s_addc_u32 s9, s9, 0
	global_store_dwordx4 v158, v[6:9], s[8:9] sc0 sc1
	s_add_u32 s8, s8, 0x2000
	s_addc_u32 s9, s9, 0
	global_store_dwordx4 v158, v[10:13], s[8:9] sc0 sc1
	s_add_u32 s8, s8, 0x2000
	s_addc_u32 s9, s9, 0
	global_store_dwordx4 v158, v[14:17], s[8:9] sc0 sc1
	s_add_u32 s8, s8, 0x2000
	s_addc_u32 s9, s9, 0
	global_store_dwordx4 v158, v[18:21], s[8:9] sc0 sc1
	s_add_u32 s8, s8, 0x2000
	s_addc_u32 s9, s9, 0
	global_store_dwordx4 v158, v[22:25], s[8:9] sc0 sc1
	s_add_u32 s8, s8, 0x2000
	s_addc_u32 s9, s9, 0
	global_store_dwordx4 v158, v[26:29], s[8:9] sc0 sc1
	s_add_u32 s8, s8, 0x2000
	s_addc_u32 s9, s9, 0
	global_store_dwordx4 v158, v[30:33], s[8:9] sc0 sc1
	s_add_u32 s8, s8, 0x2000
	s_addc_u32 s9, s9, 0
	global_store_dwordx4 v158, v[34:37], s[8:9] sc0 sc1
	s_add_u32 s8, s8, 0x2000
	s_addc_u32 s9, s9, 0
	global_store_dwordx4 v158, v[38:41], s[8:9] sc0 sc1
	s_add_u32 s8, s8, 0x2000
	s_addc_u32 s9, s9, 0
	global_store_dwordx4 v158, v[42:45], s[8:9] sc0 sc1
	s_add_u32 s8, s8, 0x2000
	s_addc_u32 s9, s9, 0
	global_store_dwordx4 v158, v[50:53], s[8:9] sc0 sc1
	s_add_u32 s8, s8, 0x2000
	s_addc_u32 s9, s9, 0
	global_store_dwordx4 v158, v[58:61], s[8:9] sc0 sc1
	s_add_u32 s8, s8, 0x2000
	s_addc_u32 s9, s9, 0
	global_store_dwordx4 v158, v[62:65], s[8:9] sc0 sc1
	s_add_u32 s8, s8, 0x2000
	s_addc_u32 s9, s9, 0
	global_store_dwordx4 v158, v[66:69], s[8:9] sc0 sc1
	s_add_u32 s8, s8, 0x2000
	s_addc_u32 s9, s9, 0
	global_store_dwordx4 v158, v[70:73], s[8:9] sc0 sc1
	s_add_u32 s8, s8, 0x2000
	s_addc_u32 s9, s9, 0
	global_store_dwordx4 v158, v[74:77], s[8:9] sc0 sc1
	s_add_u32 s8, s8, 0x2000
	s_addc_u32 s9, s9, 0
	global_store_dwordx4 v158, v[78:81], s[8:9] sc0 sc1
	s_add_u32 s8, s8, 0x2000
	s_addc_u32 s9, s9, 0
	global_store_dwordx4 v158, v[82:85], s[8:9] sc0 sc1
	s_add_u32 s8, s8, 0x2000
	s_addc_u32 s9, s9, 0
	global_store_dwordx4 v158, v[86:89], s[8:9] sc0 sc1
	s_add_u32 s8, s8, 0x2000
	s_addc_u32 s9, s9, 0
	global_store_dwordx4 v158, v[90:93], s[8:9] sc0 sc1
	s_add_u32 s8, s8, 0x2000
	s_addc_u32 s9, s9, 0
	global_store_dwordx4 v158, v[94:97], s[8:9] sc0 sc1
	s_add_u32 s8, s8, 0x2000
	s_addc_u32 s9, s9, 0
	global_store_dwordx4 v158, v[98:101], s[8:9] sc0 sc1
	s_add_u32 s8, s8, 0x2000
	s_addc_u32 s9, s9, 0
	global_store_dwordx4 v158, v[102:105], s[8:9] sc0 sc1
	s_add_u32 s8, s8, 0x2000
	s_addc_u32 s9, s9, 0
	global_store_dwordx4 v158, v[106:109], s[8:9] sc0 sc1
	s_add_u32 s8, s8, 0x2000
	s_addc_u32 s9, s9, 0
	global_store_dwordx4 v158, v[110:113], s[8:9] sc0 sc1
	s_add_u32 s8, s8, 0x2000
	s_addc_u32 s9, s9, 0
	global_store_dwordx4 v158, v[114:117], s[8:9] sc0 sc1
	s_add_u32 s8, s8, 0x2000
	s_addc_u32 s9, s9, 0
	global_store_dwordx4 v158, v[118:121], s[8:9] sc0 sc1
	s_add_u32 s8, s8, 0x2000
	s_addc_u32 s9, s9, 0
	global_store_dwordx4 v158, v[122:125], s[8:9] sc0 sc1
	s_add_u32 s8, s8, 0x2000
	s_addc_u32 s9, s9, 0
	global_store_dwordx4 v158, v[126:129], s[8:9] sc0 sc1
	s_add_u32 s8, s8, 0x2000
	s_addc_u32 s9, s9, 0
	global_store_dwordx4 v158, v[130:133], s[8:9] sc0 sc1
	s_add_u32 s8, s8, 0x2000
	s_addc_u32 s9, s9, 0
	global_store_dwordx4 v158, v[134:137], s[8:9] sc0 sc1
	s_waitcnt vmcnt(0)
	s_branch .Lsk_bdone
.Lsk_A:
	v_readlane_b32 s6, v251, 0
	s_and_b32 s6, s6, 15
	s_lshl_b32 s6, s6, 6
	s_addk_i32 s6, 0x4000
	v_readlane_b32 s11, v252, 29
	v_readlane_b32 s13, v252, 30
	s_add_u32 s11, s11, s6
	s_addc_u32 s13, s13, 0
	v_mov_b32_e32 v160, s11
	v_mov_b32_e32 v161, s13
	v_readlane_b32 s11, v254, 27
	v_readlane_b32 s13, v254, 29
	s_lshr_b32 s11, s11, 4
	s_add_i32 s11, s11, s13
	s_add_i32 s11, s11, 1
	s_mul_i32 s11, s11, 3
	v_mov_b32_e32 v162, s11
	v_readlane_b32 s6, v251, 0
	v_readlane_b32 s8, v253, 52
	v_readlane_b32 s9, v253, 53
	s_and_b32 s6, s6, 15
	s_lshl_b32 s6, s6, 18
	s_add_u32 s8, s8, s6
	s_addc_u32 s9, s9, 0
	s_add_u32 s8, s8, 0x1af00000
	s_addc_u32 s9, s9, 0
	v_lshlrev_b32_e32 v158, 4, v151
	s_mov_b64 s[6:7], exec
	s_mov_b64 exec, 1
	s_mov_b32 s11, 0

; template <class Epi>
; __device__ __forceinline__ void gemm_phase(LAS unsigned char* lds, const int tid, const Gemm g, const Sched& S, const Epi& E) {
;     ...
;         if constexpr (!epi_after_drain<Epi>::value) keep = E(acc, cur, wr, wc, fr, fq);
.Lsk_go:
	s_mov_b64 exec, s[6:7]
	global_load_dwordx4 v[196:199], v158, s[8:9] sc0 sc1
	s_add_u32 s8, s8, 0x2000
	s_addc_u32 s9, s9, 0
	global_load_dwordx4 v[200:203], v158, s[8:9] sc0 sc1
	s_add_u32 s8, s8, 0x2000
	s_addc_u32 s9, s9, 0
	global_load_dwordx4 v[204:207], v158, s[8:9] sc0 sc1
	s_add_u32 s8, s8, 0x2000
	s_addc_u32 s9, s9, 0
	global_load_dwordx4 v[208:211], v158, s[8:9] sc0 sc1
	s_add_u32 s8, s8, 0x2000
	s_addc_u32 s9, s9, 0
	global_load_dwordx4 v[212:215], v158, s[8:9] sc0 sc1
	s_add_u32 s8, s8, 0x2000
	s_addc_u32 s9, s9, 0
	global_load_dwordx4 v[46:49], v158, s[8:9] sc0 sc1
	s_add_u32 s8, s8, 0x2000
	s_addc_u32 s9, s9, 0
	global_load_dwordx4 v[54:57], v158, s[8:9] sc0 sc1
	s_add_u32 s8, s8, 0x2000
	s_addc_u32 s9, s9, 0
	global_load_dwordx4 v[138:141], v158, s[8:9] sc0 sc1
	s_add_u32 s8, s8, 0x2000
	s_addc_u32 s9, s9, 0
	s_waitcnt vmcnt(7)
	v_pk_add_f32 v[2:3], v[2:3], v[196:197]
	v_pk_add_f32 v[4:5], v[4:5], v[198:199]
	s_waitcnt vmcnt(6)
	v_pk_add_f32 v[6:7], v[6:7], v[200:201]
	v_pk_add_f32 v[8:9], v[8:9], v[202:203]
	s_waitcnt vmcnt(5)
	v_pk_add_f32 v[10:11], v[10:11], v[204:205]
	v_pk_add_f32 v[12:13], v[12:13], v[206:207]
	s_waitcnt vmcnt(4)
	v_pk_add_f32 v[14:15], v[14:15], v[208:209]
	v_pk_add_f32 v[16:17], v[16:17], v[210:211]
	s_waitcnt vmcnt(3)
	v_pk_add_f32 v[18:19], v[18:19], v[212:213]
	v_pk_add_f32 v[20:21], v[20:21], v[214:215]
	s_waitcnt vmcnt(2)
	v_pk_add_f32 v[22:23], v[22:23], v[46:47]
	v_pk_add_f32 v[24:25], v[24:25], v[48:49]
	s_waitcnt vmcnt(1)
	v_pk_add_f32 v[26:27], v[26:27], v[54:55]
	v_pk_add_f32 v[28:29], v[28:29], v[56:57]
	s_waitcnt vmcnt(0)
	v_pk_add_f32 v[30:31], v[30:31], v[138:139]
	v_pk_add_f32 v[32:33], v[32:33], v[140:141]
	global_load_dwordx4 v[196:199], v158, s[8:9] sc0 sc1
	s_add_u32 s8, s8, 0x2000
	s_addc_u32 s9, s9, 0
	global_load_dwordx4 v[200:203], v158, s[8:9] sc0 sc1
	s_add_u32 s8, s8, 0x2000
	s_addc_u32 s9, s9, 0
	global_load_dwordx4 v[204:207], v158, s[8:9] sc0 sc1
	s_add_u32 s8, s8, 0x2000
	s_addc_u32 s9, s9, 0
	global_load_dwordx4 v[208:211], v158, s[8:9] sc0 sc1
	s_add_u32 s8, s8, 0x2000
	s_addc_u32 s9, s9, 0
	global_load_dwordx4 v[212:215], v158, s[8:9] sc0 sc1
	s_add_u32 s8, s8, 0x2000
	s_addc_u32 s9, s9, 0
	global_load_dwordx4 v[46:49], v158, s[8:9] sc0 sc1
	s_add_u32 s8, s8, 0x2000
	s_addc_u32 s9, s9, 0
	global_load_dwordx4 v[54:57], v158, s[8:9] sc0 sc1
	s_add_u32 s8, s8, 0x2000
	s_addc_u32 s9, s9, 0
	global_load_dwordx4 v[138:141], v158, s[8:9] sc0 sc1
	s_add_u32 s8, s8, 0x2000
	s_addc_u32 s9, s9, 0
	s_waitcnt vmcnt(7)
	v_pk_add_f32 v[34:35], v[34:35], v[196:197]
	v_pk_add_f32 v[36:37], v[36:37], v[198:199]
	s_waitcnt vmcnt(6)
	v_pk_add_f32 v[38:39], v[38:39], v[200:201]
	v_pk_add_f32 v[40:41], v[40:41], v[202:203]
	s_waitcnt vmcnt(5)
	v_pk_add_f32 v[42:43], v[42:43], v[204:205]
	v_pk_add_f32 v[44:45], v[44:45], v[206:207]
	s_waitcnt vmcnt(4)
	v_pk_add_f32 v[50:51], v[50:51], v[208:209]
	v_pk_add_f32 v[52:53], v[52:53], v[210:211]
	s_waitcnt vmcnt(3)
	v_pk_add_f32 v[58:59], v[58:59], v[212:213]
	v_pk_add_f32 v[60:61], v[60:61], v[214:215]
	s_waitcnt vmcnt(2)
	v_pk_add_f32 v[62:63], v[62:63], v[46:47]
	v_pk_add_f32 v[64:65], v[64:65], v[48:49]
	s_waitcnt vmcnt(1)
	v_pk_add_f32 v[66:67], v[66:67], v[54:55]
	v_pk_add_f32 v[68:69], v[68:69], v[56:57]
	s_waitcnt vmcnt(0)
	v_pk_add_f32 v[70:71], v[70:71], v[138:139]
	v_pk_add_f32 v[72:73], v[72:73], v[140:141]
	global_load_dwordx4 v[196:199], v158, s[8:9] sc0 sc1
	s_add_u32 s8, s8, 0x2000
	s_addc_u32 s9, s9, 0
	global_load_dwordx4 v[200:203], v158, s[8:9] sc0 sc1
	s_add_u32 s8, s8, 0x2000
	s_addc_u32 s9, s9, 0
	global_load_dwordx4 v[204:207], v158, s[8:9] sc0 sc1
	s_add_u32 s8, s8, 0x2000
	s_addc_u32 s9, s9, 0
	global_load_dwordx4 v[208:211], v158, s[8:9] sc0 sc1
	s_add_u32 s8, s8, 0x2000
	s_addc_u32 s9, s9, 0
	global_load_dwordx4 v[212:215], v158, s[8:9] sc0 sc1
	s_add_u32 s8, s8, 0x2000
	s_addc_u32 s9, s9, 0
	global_load_dwordx4 v[46:49], v158, s[8:9] sc0 sc1
	s_add_u32 s8, s8, 0x2000
	s_addc_u32 s9, s9, 0
	global_load_dwordx4 v[54:57], v158, s[8:9] sc0 sc1
	s_add_u32 s8, s8, 0x2000
	s_addc_u32 s9, s9, 0
	global_load_dwordx4 v[138:141], v158, s[8:9] sc0 sc1
	s_add_u32 s8, s8, 0x2000
	s_addc_u32 s9, s9, 0
	s_waitcnt vmcnt(7)
	v_pk_add_f32 v[74:75], v[74:75], v[196:197]
	v_pk_add_f32 v[76:77], v[76:77], v[198:199]
	s_waitcnt vmcnt(6)
	v_pk_add_f32 v[78:79], v[78:79], v[200:201]
	v_pk_add_f32 v[80:81], v[80:81], v[202:203]
	s_waitcnt vmcnt(5)
	v_pk_add_f32 v[82:83], v[82:83], v[204:205]
	v_pk_add_f32 v[84:85], v[84:85], v[206:207]
	s_waitcnt vmcnt(4)
	v_pk_add_f32 v[86:87], v[86:87], v[208:209]
	v_pk_add_f32 v[88:89], v[88:89], v[210:211]
	s_waitcnt vmcnt(3)
	v_pk_add_f32 v[90:91], v[90:91], v[212:213]
	v_pk_add_f32 v[92:93], v[92:93], v[214:215]
	s_waitcnt vmcnt(2)
	v_pk_add_f32 v[94:95], v[94:95], v[46:47]
	v_pk_add_f32 v[96:97], v[96:97], v[48:49]
	s_waitcnt vmcnt(1)
	v_pk_add_f32 v[98:99], v[98:99], v[54:55]
	v_pk_add_f32 v[100:101], v[100:101], v[56:57]
	s_waitcnt vmcnt(0)
	v_pk_add_f32 v[102:103], v[102:103], v[138:139]
	v_pk_add_f32 v[104:105], v[104:105], v[140:141]
	global_load_dwordx4 v[196:199], v158, s[8:9] sc0 sc1
	s_add_u32 s8, s8, 0x2000
	s_addc_u32 s9, s9, 0
	global_load_dwordx4 v[200:203], v158, s[8:9] sc0 sc1
	s_add_u32 s8, s8, 0x2000
	s_addc_u32 s9, s9, 0
	global_load_dwordx4 v[204:207], v158, s[8:9] sc0 sc1
	s_add_u32 s8, s8, 0x2000
	s_addc_u32 s9, s9, 0
	global_load_dwordx4 v[208:211], v158, s[8:9] sc0 sc1
	s_add_u32 s8, s8, 0x2000
	s_addc_u32 s9, s9, 0
	global_load_dwordx4 v[212:215], v158, s[8:9] sc0 sc1
	s_add_u32 s8, s8, 0x2000
	s_addc_u32 s9, s9, 0
	global_load_dwordx4 v[46:49], v158, s[8:9] sc0 sc1
	s_add_u32 s8, s8, 0x2000
	s_addc_u32 s9, s9, 0
	global_load_dwordx4 v[54:57], v158, s[8:9] sc0 sc1
	s_add_u32 s8, s8, 0x2000
	s_addc_u32 s9, s9, 0
	global_load_dwordx4 v[138:141], v158, s[8:9] sc0 sc1
	s_add_u32 s8, s8, 0x2000
	s_addc_u32 s9, s9, 0
	s_waitcnt vmcnt(7)
; template <class Epi>
; __device__ __forceinline__ void gemm_phase(LAS unsigned char* lds, const int tid, const Gemm g, const Sched& S, const Epi& E) {
;     ...
;         if constexpr (!epi_after_drain<Epi>::value) keep = E(acc, cur, wr, wc, fr, fq);
	v_pk_add_f32 v[106:107], v[106:107], v[196:197]
	v_pk_add_f32 v[108:109], v[108:109], v[198:199]
	s_waitcnt vmcnt(6)
	v_pk_add_f32 v[110:111], v[110:111], v[200:201]
	v_pk_add_f32 v[112:113], v[112:113], v[202:203]
	s_waitcnt vmcnt(5)
	v_pk_add_f32 v[114:115], v[114:115], v[204:205]
	v_pk_add_f32 v[116:117], v[116:117], v[206:207]
	s_waitcnt vmcnt(4)
	v_pk_add_f32 v[118:119], v[118:119], v[208:209]
	v_pk_add_f32 v[120:121], v[120:121], v[210:211]
	s_waitcnt vmcnt(3)
	v_pk_add_f32 v[122:123], v[122:123], v[212:213]
	v_pk_add_f32 v[124:125], v[124:125], v[214:215]
	s_waitcnt vmcnt(2)
	v_pk_add_f32 v[126:127], v[126:127], v[46:47]
	v_pk_add_f32 v[128:129], v[128:129], v[48:49]
	s_waitcnt vmcnt(1)
	v_pk_add_f32 v[130:131], v[130:131], v[54:55]
	v_pk_add_f32 v[132:133], v[132:133], v[56:57]
	s_waitcnt vmcnt(0)
	v_pk_add_f32 v[134:135], v[134:135], v[138:139]
	v_pk_add_f32 v[136:137], v[136:137], v[140:141]
	s_add_u32 s8, s8, 0x3c0000
	s_addc_u32 s9, s9, 0
	global_load_dwordx4 v[196:199], v158, s[8:9] sc0 sc1
	s_add_u32 s8, s8, 0x2000
	s_addc_u32 s9, s9, 0
	global_load_dwordx4 v[200:203], v158, s[8:9] sc0 sc1
	s_add_u32 s8, s8, 0x2000
	s_addc_u32 s9, s9, 0
	global_load_dwordx4 v[204:207], v158, s[8:9] sc0 sc1
	s_add_u32 s8, s8, 0x2000
	s_addc_u32 s9, s9, 0
	global_load_dwordx4 v[208:211], v158, s[8:9] sc0 sc1
	s_add_u32 s8, s8, 0x2000
	s_addc_u32 s9, s9, 0
	global_load_dwordx4 v[212:215], v158, s[8:9] sc0 sc1
	s_add_u32 s8, s8, 0x2000
	s_addc_u32 s9, s9, 0
	global_load_dwordx4 v[46:49], v158, s[8:9] sc0 sc1
	s_add_u32 s8, s8, 0x2000
	s_addc_u32 s9, s9, 0
	global_load_dwordx4 v[54:57], v158, s[8:9] sc0 sc1
	s_add_u32 s8, s8, 0x2000
	s_addc_u32 s9, s9, 0
	global_load_dwordx4 v[138:141], v158, s[8:9] sc0 sc1
	s_add_u32 s8, s8, 0x2000
	s_addc_u32 s9, s9, 0
	s_waitcnt vmcnt(7)
	v_pk_add_f32 v[2:3], v[2:3], v[196:197]
	v_pk_add_f32 v[4:5], v[4:5], v[198:199]
	s_waitcnt vmcnt(6)
	v_pk_add_f32 v[6:7], v[6:7], v[200:201]
	v_pk_add_f32 v[8:9], v[8:9], v[202:203]
	s_waitcnt vmcnt(5)
	v_pk_add_f32 v[10:11], v[10:11], v[204:205]
	v_pk_add_f32 v[12:13], v[12:13], v[206:207]
	s_waitcnt vmcnt(4)
	v_pk_add_f32 v[14:15], v[14:15], v[208:209]
	v_pk_add_f32 v[16:17], v[16:17], v[210:211]
	s_waitcnt vmcnt(3)
	v_pk_add_f32 v[18:19], v[18:19], v[212:213]
	v_pk_add_f32 v[20:21], v[20:21], v[214:215]
	s_waitcnt vmcnt(2)
	v_pk_add_f32 v[22:23], v[22:23], v[46:47]
	v_pk_add_f32 v[24:25], v[24:25], v[48:49]
	s_waitcnt vmcnt(1)
	v_pk_add_f32 v[26:27], v[26:27], v[54:55]
	v_pk_add_f32 v[28:29], v[28:29], v[56:57]
	s_waitcnt vmcnt(0)
	v_pk_add_f32 v[30:31], v[30:31], v[138:139]
	v_pk_add_f32 v[32:33], v[32:33], v[140:141]
	global_load_dwordx4 v[196:199], v158, s[8:9] sc0 sc1
	s_add_u32 s8, s8, 0x2000
	s_addc_u32 s9, s9, 0
	global_load_dwordx4 v[200:203], v158, s[8:9] sc0 sc1
	s_add_u32 s8, s8, 0x2000
	s_addc_u32 s9, s9, 0
	global_load_dwordx4 v[204:207], v158, s[8:9] sc0 sc1
	s_add_u32 s8, s8, 0x2000
	s_addc_u32 s9, s9, 0
	global_load_dwordx4 v[208:211], v158, s[8:9] sc0 sc1
	s_add_u32 s8, s8, 0x2000
	s_addc_u32 s9, s9, 0
	global_load_dwordx4 v[212:215], v158, s[8:9] sc0 sc1
	s_add_u32 s8, s8, 0x2000
	s_addc_u32 s9, s9, 0
	global_load_dwordx4 v[46:49], v158, s[8:9] sc0 sc1
	s_add_u32 s8, s8, 0x2000
	s_addc_u32 s9, s9, 0
	global_load_dwordx4 v[54:57], v158, s[8:9] sc0 sc1
	s_add_u32 s8, s8, 0x2000
	s_addc_u32 s9, s9, 0
	global_load_dwordx4 v[138:141], v158, s[8:9] sc0 sc1
	s_add_u32 s8, s8, 0x2000
	s_addc_u32 s9, s9, 0
	s_waitcnt vmcnt(7)
	v_pk_add_f32 v[34:35], v[34:35], v[196:197]
	v_pk_add_f32 v[36:37], v[36:37], v[198:199]
	s_waitcnt vmcnt(6)
	v_pk_add_f32 v[38:39], v[38:39], v[200:201]
	v_pk_add_f32 v[40:41], v[40:41], v[202:203]
	s_waitcnt vmcnt(5)
	v_pk_add_f32 v[42:43], v[42:43], v[204:205]
	v_pk_add_f32 v[44:45], v[44:45], v[206:207]
	s_waitcnt vmcnt(4)
	v_pk_add_f32 v[50:51], v[50:51], v[208:209]
	v_pk_add_f32 v[52:53], v[52:53], v[210:211]
	s_waitcnt vmcnt(3)
	v_pk_add_f32 v[58:59], v[58:59], v[212:213]
	v_pk_add_f32 v[60:61], v[60:61], v[214:215]
	s_waitcnt vmcnt(2)
	v_pk_add_f32 v[62:63], v[62:63], v[46:47]
	v_pk_add_f32 v[64:65], v[64:65], v[48:49]
	s_waitcnt vmcnt(1)
	v_pk_add_f32 v[66:67], v[66:67], v[54:55]
	v_pk_add_f32 v[68:69], v[68:69], v[56:57]
	s_waitcnt vmcnt(0)
	v_pk_add_f32 v[70:71], v[70:71], v[138:139]
	v_pk_add_f32 v[72:73], v[72:73], v[140:141]
	global_load_dwordx4 v[196:199], v158, s[8:9] sc0 sc1
	s_add_u32 s8, s8, 0x2000
	s_addc_u32 s9, s9, 0
	global_load_dwordx4 v[200:203], v158, s[8:9] sc0 sc1
	s_add_u32 s8, s8, 0x2000
	s_addc_u32 s9, s9, 0
	global_load_dwordx4 v[204:207], v158, s[8:9] sc0 sc1
	s_add_u32 s8, s8, 0x2000
	s_addc_u32 s9, s9, 0
	global_load_dwordx4 v[208:211], v158, s[8:9] sc0 sc1
	s_add_u32 s8, s8, 0x2000
	s_addc_u32 s9, s9, 0
	global_load_dwordx4 v[212:215], v158, s[8:9] sc0 sc1
	s_add_u32 s8, s8, 0x2000
	s_addc_u32 s9, s9, 0
	global_load_dwordx4 v[46:49], v158, s[8:9] sc0 sc1
	s_add_u32 s8, s8, 0x2000
	s_addc_u32 s9, s9, 0
	global_load_dwordx4 v[54:57], v158, s[8:9] sc0 sc1
	s_add_u32 s8, s8, 0x2000
	s_addc_u32 s9, s9, 0
	global_load_dwordx4 v[138:141], v158, s[8:9] sc0 sc1
	s_add_u32 s8, s8, 0x2000
	s_addc_u32 s9, s9, 0
	s_waitcnt vmcnt(7)
	v_pk_add_f32 v[74:75], v[74:75], v[196:197]
	v_pk_add_f32 v[76:77], v[76:77], v[198:199]
	s_waitcnt vmcnt(6)
	v_pk_add_f32 v[78:79], v[78:79], v[200:201]
	v_pk_add_f32 v[80:81], v[80:81], v[202:203]
	s_waitcnt vmcnt(5)
	v_pk_add_f32 v[82:83], v[82:83], v[204:205]
	v_pk_add_f32 v[84:85], v[84:85], v[206:207]
	s_waitcnt vmcnt(4)
	v_pk_add_f32 v[86:87], v[86:87], v[208:209]
	v_pk_add_f32 v[88:89], v[88:89], v[210:211]
	s_waitcnt vmcnt(3)
; template <class Epi>
; __device__ __forceinline__ void gemm_phase(LAS unsigned char* lds, const int tid, const Gemm g, const Sched& S, const Epi& E) {
;     ...
;         if constexpr (!epi_after_drain<Epi>::value) keep = E(acc, cur, wr, wc, fr, fq);
	v_pk_add_f32 v[90:91], v[90:91], v[212:213]
	v_pk_add_f32 v[92:93], v[92:93], v[214:215]
	s_waitcnt vmcnt(2)
	v_pk_add_f32 v[94:95], v[94:95], v[46:47]
	v_pk_add_f32 v[96:97], v[96:97], v[48:49]
	s_waitcnt vmcnt(1)
	v_pk_add_f32 v[98:99], v[98:99], v[54:55]
	v_pk_add_f32 v[100:101], v[100:101], v[56:57]
	s_waitcnt vmcnt(0)
	v_pk_add_f32 v[102:103], v[102:103], v[138:139]
	v_pk_add_f32 v[104:105], v[104:105], v[140:141]
	global_load_dwordx4 v[196:199], v158, s[8:9] sc0 sc1
	s_add_u32 s8, s8, 0x2000
	s_addc_u32 s9, s9, 0
	global_load_dwordx4 v[200:203], v158, s[8:9] sc0 sc1
	s_add_u32 s8, s8, 0x2000
	s_addc_u32 s9, s9, 0
	global_load_dwordx4 v[204:207], v158, s[8:9] sc0 sc1
	s_add_u32 s8, s8, 0x2000
	s_addc_u32 s9, s9, 0
	global_load_dwordx4 v[208:211], v158, s[8:9] sc0 sc1
	s_add_u32 s8, s8, 0x2000
	s_addc_u32 s9, s9, 0
	global_load_dwordx4 v[212:215], v158, s[8:9] sc0 sc1
	s_add_u32 s8, s8, 0x2000
	s_addc_u32 s9, s9, 0
	global_load_dwordx4 v[46:49], v158, s[8:9] sc0 sc1
	s_add_u32 s8, s8, 0x2000
	s_addc_u32 s9, s9, 0
	global_load_dwordx4 v[54:57], v158, s[8:9] sc0 sc1
	s_add_u32 s8, s8, 0x2000
	s_addc_u32 s9, s9, 0
	global_load_dwordx4 v[138:141], v158, s[8:9] sc0 sc1
	s_add_u32 s8, s8, 0x2000
	s_addc_u32 s9, s9, 0
	s_waitcnt vmcnt(7)
	v_pk_add_f32 v[106:107], v[106:107], v[196:197]
	v_pk_add_f32 v[108:109], v[108:109], v[198:199]
	s_waitcnt vmcnt(6)
	v_pk_add_f32 v[110:111], v[110:111], v[200:201]
	v_pk_add_f32 v[112:113], v[112:113], v[202:203]
	s_waitcnt vmcnt(5)
	v_pk_add_f32 v[114:115], v[114:115], v[204:205]
	v_pk_add_f32 v[116:117], v[116:117], v[206:207]
	s_waitcnt vmcnt(4)
	v_pk_add_f32 v[118:119], v[118:119], v[208:209]
	v_pk_add_f32 v[120:121], v[120:121], v[210:211]
	s_waitcnt vmcnt(3)
	v_pk_add_f32 v[122:123], v[122:123], v[212:213]
	v_pk_add_f32 v[124:125], v[124:125], v[214:215]
	s_waitcnt vmcnt(2)
	v_pk_add_f32 v[126:127], v[126:127], v[46:47]
	v_pk_add_f32 v[128:129], v[128:129], v[48:49]
	s_waitcnt vmcnt(1)
	v_pk_add_f32 v[130:131], v[130:131], v[54:55]
	v_pk_add_f32 v[132:133], v[132:133], v[56:57]
	s_waitcnt vmcnt(0)
	v_pk_add_f32 v[134:135], v[134:135], v[138:139]
	v_pk_add_f32 v[136:137], v[136:137], v[140:141]
	s_add_u32 s8, s8, 0x3c0000
	s_addc_u32 s9, s9, 0
	global_load_dwordx4 v[196:199], v158, s[8:9] sc0 sc1
	s_add_u32 s8, s8, 0x2000
	s_addc_u32 s9, s9, 0
	global_load_dwordx4 v[200:203], v158, s[8:9] sc0 sc1
	s_add_u32 s8, s8, 0x2000
	s_addc_u32 s9, s9, 0
	global_load_dwordx4 v[204:207], v158, s[8:9] sc0 sc1
	s_add_u32 s8, s8, 0x2000
	s_addc_u32 s9, s9, 0
	global_load_dwordx4 v[208:211], v158, s[8:9] sc0 sc1
	s_add_u32 s8, s8, 0x2000
	s_addc_u32 s9, s9, 0
	global_load_dwordx4 v[212:215], v158, s[8:9] sc0 sc1
	s_add_u32 s8, s8, 0x2000
	s_addc_u32 s9, s9, 0
	global_load_dwordx4 v[46:49], v158, s[8:9] sc0 sc1
	s_add_u32 s8, s8, 0x2000
	s_addc_u32 s9, s9, 0
	global_load_dwordx4 v[54:57], v158, s[8:9] sc0 sc1
	s_add_u32 s8, s8, 0x2000
	s_addc_u32 s9, s9, 0
	global_load_dwordx4 v[138:141], v158, s[8:9] sc0 sc1
	s_add_u32 s8, s8, 0x2000
	s_addc_u32 s9, s9, 0
	s_waitcnt vmcnt(7)
	v_pk_add_f32 v[2:3], v[2:3], v[196:197]
	v_pk_add_f32 v[4:5], v[4:5], v[198:199]
	s_waitcnt vmcnt(6)
	v_pk_add_f32 v[6:7], v[6:7], v[200:201]
	v_pk_add_f32 v[8:9], v[8:9], v[202:203]
	s_waitcnt vmcnt(5)
	v_pk_add_f32 v[10:11], v[10:11], v[204:205]
	v_pk_add_f32 v[12:13], v[12:13], v[206:207]
	s_waitcnt vmcnt(4)
	v_pk_add_f32 v[14:15], v[14:15], v[208:209]
	v_pk_add_f32 v[16:17], v[16:17], v[210:211]
	s_waitcnt vmcnt(3)
	v_pk_add_f32 v[18:19], v[18:19], v[212:213]
	v_pk_add_f32 v[20:21], v[20:21], v[214:215]
	s_waitcnt vmcnt(2)
	v_pk_add_f32 v[22:23], v[22:23], v[46:47]
	v_pk_add_f32 v[24:25], v[24:25], v[48:49]
	s_waitcnt vmcnt(1)
	v_pk_add_f32 v[26:27], v[26:27], v[54:55]
	v_pk_add_f32 v[28:29], v[28:29], v[56:57]
	s_waitcnt vmcnt(0)
	v_pk_add_f32 v[30:31], v[30:31], v[138:139]
	v_pk_add_f32 v[32:33], v[32:33], v[140:141]
	global_load_dwordx4 v[196:199], v158, s[8:9] sc0 sc1
	s_add_u32 s8, s8, 0x2000
	s_addc_u32 s9, s9, 0
	global_load_dwordx4 v[200:203], v158, s[8:9] sc0 sc1
	s_add_u32 s8, s8, 0x2000
	s_addc_u32 s9, s9, 0
	global_load_dwordx4 v[204:207], v158, s[8:9] sc0 sc1
	s_add_u32 s8, s8, 0x2000
	s_addc_u32 s9, s9, 0
	global_load_dwordx4 v[208:211], v158, s[8:9] sc0 sc1
	s_add_u32 s8, s8, 0x2000
	s_addc_u32 s9, s9, 0
	global_load_dwordx4 v[212:215], v158, s[8:9] sc0 sc1
	s_add_u32 s8, s8, 0x2000
	s_addc_u32 s9, s9, 0
	global_load_dwordx4 v[46:49], v158, s[8:9] sc0 sc1
	s_add_u32 s8, s8, 0x2000
	s_addc_u32 s9, s9, 0
	global_load_dwordx4 v[54:57], v158, s[8:9] sc0 sc1
	s_add_u32 s8, s8, 0x2000
	s_addc_u32 s9, s9, 0
	global_load_dwordx4 v[138:141], v158, s[8:9] sc0 sc1
	s_add_u32 s8, s8, 0x2000
	s_addc_u32 s9, s9, 0
	s_waitcnt vmcnt(7)
	v_pk_add_f32 v[34:35], v[34:35], v[196:197]
	v_pk_add_f32 v[36:37], v[36:37], v[198:199]
	s_waitcnt vmcnt(6)
	v_pk_add_f32 v[38:39], v[38:39], v[200:201]
	v_pk_add_f32 v[40:41], v[40:41], v[202:203]
	s_waitcnt vmcnt(5)
	v_pk_add_f32 v[42:43], v[42:43], v[204:205]
	v_pk_add_f32 v[44:45], v[44:45], v[206:207]
	s_waitcnt vmcnt(4)
	v_pk_add_f32 v[50:51], v[50:51], v[208:209]
	v_pk_add_f32 v[52:53], v[52:53], v[210:211]
	s_waitcnt vmcnt(3)
	v_pk_add_f32 v[58:59], v[58:59], v[212:213]
	v_pk_add_f32 v[60:61], v[60:61], v[214:215]
	s_waitcnt vmcnt(2)
	v_pk_add_f32 v[62:63], v[62:63], v[46:47]
	v_pk_add_f32 v[64:65], v[64:65], v[48:49]
	s_waitcnt vmcnt(1)
	v_pk_add_f32 v[66:67], v[66:67], v[54:55]
	v_pk_add_f32 v[68:69], v[68:69], v[56:57]
	s_waitcnt vmcnt(0)
;     __device__ __forceinline__ bool operator()(f32x4 (&acc)[2][2][4][2], const Unit& u, int wr, int wc, int fr, int fq) const {
;         const int kv = u.pm >> 3; const int row0 = (u.pm & 7) * BM + wr * 64 + fr; const int col0 = wc * 32 + 8 * fq;
;         float bv[2][8];
; #pragma unroll
;         for (int bj = 0; bj < 2; ++bj)
; #pragma unroll
;             for (int j = 0; j < 8; ++j) bv[bj][j] = bh[kv * 256 + col0 + bj * HALF + j];
; #pragma unroll
;         for (int ai = 0; ai < 2; ++ai)
; #pragma unroll
;             for (int m = 0; m < 4; ++m) { bf16_t* rowp = hid + ((size_t)kv * 2048 + row0 + ai * HALF + m * 16) * 256 + col0;
	v_pk_add_f32 v[70:71], v[70:71], v[138:139]
	v_pk_add_f32 v[72:73], v[72:73], v[140:141]
	global_load_dwordx4 v[196:199], v158, s[8:9] sc0 sc1
	s_add_u32 s8, s8, 0x2000
	s_addc_u32 s9, s9, 0
	global_load_dwordx4 v[200:203], v158, s[8:9] sc0 sc1
	s_add_u32 s8, s8, 0x2000
	s_addc_u32 s9, s9, 0
	global_load_dwordx4 v[204:207], v158, s[8:9] sc0 sc1
	s_add_u32 s8, s8, 0x2000
	s_addc_u32 s9, s9, 0
	global_load_dwordx4 v[208:211], v158, s[8:9] sc0 sc1
	s_add_u32 s8, s8, 0x2000
	s_addc_u32 s9, s9, 0
	global_load_dwordx4 v[212:215], v158, s[8:9] sc0 sc1
	s_add_u32 s8, s8, 0x2000
	s_addc_u32 s9, s9, 0
	global_load_dwordx4 v[46:49], v158, s[8:9] sc0 sc1
	s_add_u32 s8, s8, 0x2000
	s_addc_u32 s9, s9, 0
	global_load_dwordx4 v[54:57], v158, s[8:9] sc0 sc1
	s_add_u32 s8, s8, 0x2000
	s_addc_u32 s9, s9, 0
	global_load_dwordx4 v[138:141], v158, s[8:9] sc0 sc1
	s_add_u32 s8, s8, 0x2000
	s_addc_u32 s9, s9, 0
	s_waitcnt vmcnt(7)
	v_pk_add_f32 v[74:75], v[74:75], v[196:197]
	v_pk_add_f32 v[76:77], v[76:77], v[198:199]
	s_waitcnt vmcnt(6)
	v_pk_add_f32 v[78:79], v[78:79], v[200:201]
	v_pk_add_f32 v[80:81], v[80:81], v[202:203]
	s_waitcnt vmcnt(5)
	v_pk_add_f32 v[82:83], v[82:83], v[204:205]
	v_pk_add_f32 v[84:85], v[84:85], v[206:207]
	s_waitcnt vmcnt(4)
	v_pk_add_f32 v[86:87], v[86:87], v[208:209]
	v_pk_add_f32 v[88:89], v[88:89], v[210:211]
	s_waitcnt vmcnt(3)
	v_pk_add_f32 v[90:91], v[90:91], v[212:213]
	v_pk_add_f32 v[92:93], v[92:93], v[214:215]
	s_waitcnt vmcnt(2)
	v_pk_add_f32 v[94:95], v[94:95], v[46:47]
	v_pk_add_f32 v[96:97], v[96:97], v[48:49]
	s_waitcnt vmcnt(1)
	v_pk_add_f32 v[98:99], v[98:99], v[54:55]
	v_pk_add_f32 v[100:101], v[100:101], v[56:57]
	s_waitcnt vmcnt(0)
	v_pk_add_f32 v[102:103], v[102:103], v[138:139]
	v_pk_add_f32 v[104:105], v[104:105], v[140:141]
	global_load_dwordx4 v[196:199], v158, s[8:9] sc0 sc1
	s_add_u32 s8, s8, 0x2000
	s_addc_u32 s9, s9, 0
	global_load_dwordx4 v[200:203], v158, s[8:9] sc0 sc1
	s_add_u32 s8, s8, 0x2000
	s_addc_u32 s9, s9, 0
	global_load_dwordx4 v[204:207], v158, s[8:9] sc0 sc1
	s_add_u32 s8, s8, 0x2000
	s_addc_u32 s9, s9, 0
	global_load_dwordx4 v[208:211], v158, s[8:9] sc0 sc1
	s_add_u32 s8, s8, 0x2000
	s_addc_u32 s9, s9, 0
	global_load_dwordx4 v[212:215], v158, s[8:9] sc0 sc1
	s_add_u32 s8, s8, 0x2000
	s_addc_u32 s9, s9, 0
	global_load_dwordx4 v[46:49], v158, s[8:9] sc0 sc1
	s_add_u32 s8, s8, 0x2000
	s_addc_u32 s9, s9, 0
	global_load_dwordx4 v[54:57], v158, s[8:9] sc0 sc1
	s_add_u32 s8, s8, 0x2000
	s_addc_u32 s9, s9, 0
	global_load_dwordx4 v[138:141], v158, s[8:9] sc0 sc1
	s_add_u32 s8, s8, 0x2000
	s_addc_u32 s9, s9, 0
	s_waitcnt vmcnt(7)
	v_pk_add_f32 v[106:107], v[106:107], v[196:197]
	v_pk_add_f32 v[108:109], v[108:109], v[198:199]
	s_waitcnt vmcnt(6)
	v_pk_add_f32 v[110:111], v[110:111], v[200:201]
	v_pk_add_f32 v[112:113], v[112:113], v[202:203]
	s_waitcnt vmcnt(5)
	v_pk_add_f32 v[114:115], v[114:115], v[204:205]
	v_pk_add_f32 v[116:117], v[116:117], v[206:207]
	s_waitcnt vmcnt(4)
	v_pk_add_f32 v[118:119], v[118:119], v[208:209]
	v_pk_add_f32 v[120:121], v[120:121], v[210:211]
	s_waitcnt vmcnt(3)
	v_pk_add_f32 v[122:123], v[122:123], v[212:213]
	v_pk_add_f32 v[124:125], v[124:125], v[214:215]
	s_waitcnt vmcnt(2)
	v_pk_add_f32 v[126:127], v[126:127], v[46:47]
	v_pk_add_f32 v[128:129], v[128:129], v[48:49]
	s_waitcnt vmcnt(1)
	v_pk_add_f32 v[130:131], v[130:131], v[54:55]
	v_pk_add_f32 v[132:133], v[132:133], v[56:57]
	s_waitcnt vmcnt(0)
	v_pk_add_f32 v[134:135], v[134:135], v[138:139]
	v_pk_add_f32 v[136:137], v[136:137], v[140:141]
	s_ashr_i32 s6, s22, 3
	s_lshl_b32 s7, s22, 8
	v_lshl_or_b32 v46, s6, 8, v150
	v_readlane_b32 s8, v252, 10
	s_and_b32 s7, s7, 0x700
	v_ashrrev_i32_e32 v47, 31, v46
	v_readlane_b32 s9, v252, 11
	v_lshlrev_b32_e32 v0, 1, v150
	s_mov_b32 s22, s37
	v_lshl_add_u64 v[162:163], v[46:47], 2, s[8:9]
	v_add_u32_e32 v46, s7, v164
	s_ashr_i32 s7, s6, 31
	v_ashrrev_i32_e32 v47, 31, v46
	s_lshl_b64 s[6:7], s[6:7], 20
	v_lshlrev_b64 v[46:47], 9, v[46:47]
	v_lshl_add_u64 v[160:161], v[46:47], 0, s[6:7]
	v_lshl_add_u64 v[46:47], s[78:79], 0, v[160:161]
	v_lshl_add_u64 v[158:159], v[46:47], 0, v[0:1]
	global_load_dwordx4 v[46:49], v[162:163], off offset:16
	global_load_dwordx4 v[54:57], v[162:163], off
	s_mov_b64 s[6:7], 0x10000
	s_mov_b64 s[8:9], s[2:3]
	s_waitcnt vmcnt(0)
; __device__ __forceinline__ unsigned pk2(float lo, float hi) { const f32x2 f = {lo, hi}; const bf16n2 v = __builtin_convertvector(f, bf16n2); return __builtin_bit_cast(unsigned, v); }
; __device__ __forceinline__ float sigmoidf_(float x) { return __builtin_amdgcn_rcpf(1.0f + __expf(-x)); }
;     __device__ __forceinline__ bool operator()(f32x4 (&acc)[2][2][4][2], const Unit& u, int wr, int wc, int fr, int fq) const {
;     ...
;             for (int j = 0; j < 8; ++j) bv[bj][j] = bh[kv * 256 + col0 + bj * HALF + j];
; #pragma unroll
;         for (int ai = 0; ai < 2; ++ai)
; #pragma unroll
;             for (int m = 0; m < 4; ++m) { bf16_t* rowp = hid + ((size_t)kv * 2048 + row0 + ai * HALF + m * 16) * 256 + col0;
; #pragma unroll
;                 for (int bj = 0; bj < 2; ++bj) { float o[8];
; #pragma unroll
;                     for (int j = 0; j < 8; ++j) { const float x = acc[ai][bj][m][j >> 2][j & 3] + bv[bj][j];
;                         o[j] = x * sigmoidf_(1.5957691216f * (x + 0.044715f * x * x * x)); }
;                     u32x4 w; w.x = pk2(o[0], o[1]); w.y = pk2(o[2], o[3]); w.z = pk2(o[4], o[5]); w.w = pk2(o[6], o[7]);
;                     *(u32x4*)(rowp + bj * HALF) = w; } }
	v_pk_add_f32 v[38:39], v[38:39], v[46:47]
	v_pk_add_f32 v[66:67], v[66:67], v[54:55]
	v_pk_add_f32 v[68:69], v[68:69], v[56:57]
	v_mul_f32_e32 v0, 0x3d372713, v66
	v_mul_f32_e32 v0, v66, v0
	v_fma_f32 v0, v66, v0, v66
	v_mul_f32_e32 v0, 0x3fcc422a, v0
	v_mul_f32_e32 v0, 0xbfb8aa3b, v0
	v_exp_f32_e32 v0, v0
	v_pk_add_f32 v[40:41], v[40:41], v[48:49]
	v_pk_add_f32 v[126:127], v[126:127], v[54:55]
	v_pk_add_f32 v[128:129], v[128:129], v[56:57]
	v_add_f32_e32 v0, 1.0, v0
	v_rcp_f32_e32 v138, v0
	v_mul_f32_e32 v0, 0x3d372713, v67
	v_mul_f32_e32 v0, v67, v0
	v_fma_f32 v0, v67, v0, v67
	v_mul_f32_e32 v0, 0x3fcc422a, v0
	v_mul_f32_e32 v0, 0xbfb8aa3b, v0
	v_exp_f32_e32 v0, v0
	v_pk_add_f32 v[122:123], v[122:123], v[46:47]
	v_pk_add_f32 v[110:111], v[110:111], v[54:55]
	v_pk_add_f32 v[112:113], v[112:113], v[56:57]
	v_add_f32_e32 v0, 1.0, v0
	v_rcp_f32_e32 v139, v0
	v_mul_f32_e32 v0, 0x3d372713, v68
	v_mul_f32_e32 v0, v68, v0
	v_fma_f32 v0, v68, v0, v68
	v_mul_f32_e32 v0, 0x3fcc422a, v0
	v_mul_f32_e32 v0, 0xbfb8aa3b, v0
	v_exp_f32_e32 v0, v0
	v_pk_mul_f32 v[66:67], v[66:67], v[138:139]
	v_pk_add_f32 v[106:107], v[106:107], v[46:47]
	v_pk_add_f32 v[94:95], v[94:95], v[54:55]
	v_add_f32_e32 v0, 1.0, v0
	v_rcp_f32_e32 v138, v0
	v_mul_f32_e32 v0, 0x3d372713, v69
	v_mul_f32_e32 v0, v69, v0
	v_fma_f32 v0, v69, v0, v69
	v_mul_f32_e32 v0, 0x3fcc422a, v0
	v_mul_f32_e32 v0, 0xbfb8aa3b, v0
	v_exp_f32_e32 v0, v0
	v_pk_add_f32 v[96:97], v[96:97], v[56:57]
	v_pk_add_f32 v[90:91], v[90:91], v[46:47]
	v_pk_add_f32 v[78:79], v[78:79], v[54:55]
	v_add_f32_e32 v0, 1.0, v0
	v_rcp_f32_e32 v139, v0
	v_mul_f32_e32 v0, 0x3d372713, v38
	v_mul_f32_e32 v0, v38, v0
	v_fma_f32 v0, v38, v0, v38
	v_mul_f32_e32 v0, 0x3fcc422a, v0
	v_mul_f32_e32 v0, 0xbfb8aa3b, v0
	v_exp_f32_e32 v0, v0
	v_pk_mul_f32 v[68:69], v[68:69], v[138:139]
	v_pk_add_f32 v[80:81], v[80:81], v[56:57]
	v_pk_add_f32 v[74:75], v[74:75], v[46:47]
	v_add_f32_e32 v0, 1.0, v0
	v_rcp_f32_e32 v138, v0
	v_mul_f32_e32 v0, 0x3d372713, v39
	v_mul_f32_e32 v0, v39, v0
	v_fma_f32 v0, v39, v0, v39
	v_mul_f32_e32 v0, 0x3fcc422a, v0
	v_mul_f32_e32 v0, 0xbfb8aa3b, v0
	v_exp_f32_e32 v0, v0
	v_pk_add_f32 v[58:59], v[58:59], v[54:55]
	v_pk_add_f32 v[60:61], v[60:61], v[56:57]
	v_pk_add_f32 v[50:51], v[50:51], v[46:47]
	v_add_f32_e32 v0, 1.0, v0
	v_rcp_f32_e32 v139, v0
	v_mul_f32_e32 v0, 0x3d372713, v40
	v_mul_f32_e32 v0, v40, v0
	v_fma_f32 v0, v40, v0, v40
	v_mul_f32_e32 v0, 0x3fcc422a, v0
	v_mul_f32_e32 v0, 0xbfb8aa3b, v0
	v_exp_f32_e32 v0, v0
	v_pk_mul_f32 v[38:39], v[38:39], v[138:139]
	v_pk_add_f32 v[30:31], v[30:31], v[54:55]
	v_cvt_pk_bf16_f32 v140, v38, v39
	v_add_f32_e32 v0, 1.0, v0
	v_rcp_f32_e32 v138, v0
	v_mul_f32_e32 v0, 0x3d372713, v41
	v_mul_f32_e32 v0, v41, v0
	v_fma_f32 v0, v41, v0, v41
	v_mul_f32_e32 v0, 0x3fcc422a, v0
	v_mul_f32_e32 v0, 0xbfb8aa3b, v0
	v_exp_f32_e32 v0, v0
	v_pk_add_f32 v[32:33], v[32:33], v[56:57]
	v_pk_add_f32 v[26:27], v[26:27], v[46:47]
	v_pk_add_f32 v[14:15], v[14:15], v[54:55]
	v_add_f32_e32 v0, 1.0, v0
	v_rcp_f32_e32 v139, v0
	v_pk_add_f32 v[16:17], v[16:17], v[56:57]
	v_pk_add_f32 v[10:11], v[10:11], v[46:47]
	v_pk_mul_f32 v[40:41], v[40:41], v[138:139]
	v_cvt_pk_bf16_f32 v138, v66, v67
	v_cvt_pk_bf16_f32 v139, v68, v69
	v_cvt_pk_bf16_f32 v141, v40, v41
	global_load_dwordx4 v[38:41], v[162:163], off offset:528
	global_load_dwordx4 v[66:69], v[162:163], off offset:512
	s_waitcnt vmcnt(0)
	v_pk_add_f32 v[130:131], v[130:131], v[38:39]
	v_pk_add_f32 v[134:135], v[134:135], v[66:67]
	v_pk_add_f32 v[136:137], v[136:137], v[68:69]
	v_mul_f32_e32 v0, 0x3d372713, v134
	v_mul_f32_e32 v0, v134, v0
	v_fma_f32 v0, v134, v0, v134
	v_mul_f32_e32 v0, 0x3fcc422a, v0
	v_mul_f32_e32 v0, 0xbfb8aa3b, v0
	v_exp_f32_e32 v0, v0
	global_store_dwordx4 v[158:159], v[138:141], off
	v_pk_add_f32 v[118:119], v[118:119], v[66:67]
	v_pk_add_f32 v[120:121], v[120:121], v[68:69]
	v_add_f32_e32 v0, 1.0, v0
	v_rcp_f32_e32 v162, v0
	v_mul_f32_e32 v0, 0x3d372713, v135
	v_mul_f32_e32 v0, v135, v0
	v_fma_f32 v0, v135, v0, v135
	v_mul_f32_e32 v0, 0x3fcc422a, v0
	v_mul_f32_e32 v0, 0xbfb8aa3b, v0
	v_exp_f32_e32 v0, v0
	v_pk_add_f32 v[114:115], v[114:115], v[38:39]
	v_pk_add_f32 v[102:103], v[102:103], v[66:67]
	v_pk_add_f32 v[104:105], v[104:105], v[68:69]
	v_add_f32_e32 v0, 1.0, v0
	v_rcp_f32_e32 v163, v0
	v_mul_f32_e32 v0, 0x3d372713, v136
	v_mul_f32_e32 v0, v136, v0
	v_fma_f32 v0, v136, v0, v136
	v_mul_f32_e32 v0, 0x3fcc422a, v0
	v_mul_f32_e32 v0, 0xbfb8aa3b, v0
	v_exp_f32_e32 v0, v0
	v_pk_mul_f32 v[134:135], v[134:135], v[162:163]
	v_pk_add_f32 v[98:99], v[98:99], v[38:39]
	v_pk_add_f32 v[86:87], v[86:87], v[66:67]
	v_add_f32_e32 v0, 1.0, v0
	v_rcp_f32_e32 v162, v0
	v_mul_f32_e32 v0, 0x3d372713, v137
	v_mul_f32_e32 v0, v137, v0
	v_fma_f32 v0, v137, v0, v137
	v_mul_f32_e32 v0, 0x3fcc422a, v0
	v_mul_f32_e32 v0, 0xbfb8aa3b, v0
	v_exp_f32_e32 v0, v0
	v_pk_add_f32 v[88:89], v[88:89], v[68:69]
	v_pk_add_f32 v[82:83], v[82:83], v[38:39]
	v_pk_add_f32 v[70:71], v[70:71], v[66:67]
	v_add_f32_e32 v0, 1.0, v0
	v_rcp_f32_e32 v163, v0
	v_mul_f32_e32 v0, 0x3d372713, v130
	v_mul_f32_e32 v0, v130, v0
	v_fma_f32 v0, v130, v0, v130
	v_mul_f32_e32 v0, 0x3fcc422a, v0
	v_mul_f32_e32 v0, 0xbfb8aa3b, v0
	v_exp_f32_e32 v0, v0
	v_pk_mul_f32 v[136:137], v[136:137], v[162:163]
	v_pk_add_f32 v[72:73], v[72:73], v[68:69]
	v_pk_add_f32 v[62:63], v[62:63], v[38:39]
	v_add_f32_e32 v0, 1.0, v0
	v_rcp_f32_e32 v162, v0
	v_mul_f32_e32 v0, 0x3d372713, v131
	v_mul_f32_e32 v0, v131, v0
	v_fma_f32 v0, v131, v0, v131
	v_mul_f32_e32 v0, 0x3fcc422a, v0
	v_mul_f32_e32 v0, 0xbfb8aa3b, v0
	v_exp_f32_e32 v0, v0
	v_pk_add_f32 v[42:43], v[42:43], v[66:67]
; __device__ __forceinline__ unsigned pk2(float lo, float hi) { const f32x2 f = {lo, hi}; const bf16n2 v = __builtin_convertvector(f, bf16n2); return __builtin_bit_cast(unsigned, v); }
; __device__ __forceinline__ float sigmoidf_(float x) { return __builtin_amdgcn_rcpf(1.0f + __expf(-x)); }
;     __device__ __forceinline__ bool operator()(f32x4 (&acc)[2][2][4][2], const Unit& u, int wr, int wc, int fr, int fq) const {
;     ...
;             for (int j = 0; j < 8; ++j) bv[bj][j] = bh[kv * 256 + col0 + bj * HALF + j];
; #pragma unroll
;         for (int ai = 0; ai < 2; ++ai)
; #pragma unroll
;             for (int m = 0; m < 4; ++m) { bf16_t* rowp = hid + ((size_t)kv * 2048 + row0 + ai * HALF + m * 16) * 256 + col0;
; #pragma unroll
;                 for (int bj = 0; bj < 2; ++bj) { float o[8];
; #pragma unroll
;                     for (int j = 0; j < 8; ++j) { const float x = acc[ai][bj][m][j >> 2][j & 3] + bv[bj][j];
;                         o[j] = x * sigmoidf_(1.5957691216f * (x + 0.044715f * x * x * x)); }
;                     u32x4 w; w.x = pk2(o[0], o[1]); w.y = pk2(o[2], o[3]); w.z = pk2(o[4], o[5]); w.w = pk2(o[6], o[7]);
;                     *(u32x4*)(rowp + bj * HALF) = w; } }
	v_pk_add_f32 v[44:45], v[44:45], v[68:69]
	v_pk_add_f32 v[34:35], v[34:35], v[38:39]
	v_add_f32_e32 v0, 1.0, v0
	v_rcp_f32_e32 v163, v0
	v_pk_add_f32 v[22:23], v[22:23], v[66:67]
	v_pk_add_f32 v[24:25], v[24:25], v[68:69]
	v_pk_add_f32 v[18:19], v[18:19], v[38:39]
	v_pk_mul_f32 v[162:163], v[130:131], v[162:163]
	v_pk_add_f32 v[130:131], v[132:133], v[40:41]
	v_pk_add_f32 v[6:7], v[6:7], v[66:67]
	v_mul_f32_e32 v0, 0x3d372713, v130
	v_mul_f32_e32 v0, v130, v0
	v_fma_f32 v0, v130, v0, v130
	v_mul_f32_e32 v0, 0x3fcc422a, v0
	v_mul_f32_e32 v0, 0xbfb8aa3b, v0
	v_exp_f32_e32 v0, v0
	v_pk_add_f32 v[8:9], v[8:9], v[68:69]
	v_pk_add_f32 v[2:3], v[2:3], v[38:39]
	v_add_f32_e32 v0, 1.0, v0
	v_rcp_f32_e32 v132, v0
	v_mul_f32_e32 v0, 0x3d372713, v131
	v_mul_f32_e32 v0, v131, v0
	v_fma_f32 v0, v131, v0, v131
	v_mul_f32_e32 v0, 0x3fcc422a, v0
	v_mul_f32_e32 v0, 0xbfb8aa3b, v0
	v_exp_f32_e32 v0, v0
	s_nop 0
	v_add_f32_e32 v0, 1.0, v0
	v_rcp_f32_e32 v133, v0
	v_mul_f32_e32 v0, 0x3d372713, v126
	v_mul_f32_e32 v0, v126, v0
	v_fma_f32 v0, v126, v0, v126
	v_mul_f32_e32 v0, 0x3fcc422a, v0
	v_mul_f32_e32 v0, 0xbfb8aa3b, v0
	v_exp_f32_e32 v0, v0
	v_pk_mul_f32 v[138:139], v[130:131], v[132:133]
	v_cvt_pk_bf16_f32 v130, v134, v135
	v_cvt_pk_bf16_f32 v131, v136, v137
	v_cvt_pk_bf16_f32 v132, v162, v163
	v_cvt_pk_bf16_f32 v133, v138, v139
	v_add_f32_e32 v0, 1.0, v0
	global_store_dwordx4 v[158:159], v[130:133], off offset:256
	s_nop 1
	v_rcp_f32_e32 v132, v0
	v_mul_f32_e32 v0, 0x3d372713, v127
	v_mul_f32_e32 v0, v127, v0
	v_fma_f32 v0, v127, v0, v127
	v_mul_f32_e32 v0, 0x3fcc422a, v0
	v_mul_f32_e32 v0, 0xbfb8aa3b, v0
	v_exp_f32_e32 v0, v0
	v_or_b32_e32 v130, 0x2000, v160
	v_mov_b32_e32 v131, v161
	v_lshl_add_u64 v[130:131], v[152:153], 0, v[130:131]
	v_add_f32_e32 v0, 1.0, v0
	v_rcp_f32_e32 v133, v0
	v_mul_f32_e32 v0, 0x3d372713, v128
	v_mul_f32_e32 v0, v128, v0
	v_fma_f32 v0, v128, v0, v128
	v_mul_f32_e32 v0, 0x3fcc422a, v0
	v_mul_f32_e32 v0, 0xbfb8aa3b, v0
	v_exp_f32_e32 v0, v0
	v_pk_mul_f32 v[126:127], v[126:127], v[132:133]
	v_add_f32_e32 v0, 1.0, v0
	v_rcp_f32_e32 v132, v0
	v_mul_f32_e32 v0, 0x3d372713, v129
	v_mul_f32_e32 v0, v129, v0
	v_fma_f32 v0, v129, v0, v129
	v_mul_f32_e32 v0, 0x3fcc422a, v0
	v_mul_f32_e32 v0, 0xbfb8aa3b, v0
	v_exp_f32_e32 v0, v0
	s_nop 0
	v_add_f32_e32 v0, 1.0, v0
	v_rcp_f32_e32 v133, v0
	v_mul_f32_e32 v0, 0x3d372713, v122
	v_mul_f32_e32 v0, v122, v0
	v_fma_f32 v0, v122, v0, v122
	v_mul_f32_e32 v0, 0x3fcc422a, v0
	v_mul_f32_e32 v0, 0xbfb8aa3b, v0
	v_exp_f32_e32 v0, v0
	v_pk_mul_f32 v[128:129], v[128:129], v[132:133]
	v_add_f32_e32 v0, 1.0, v0
	v_rcp_f32_e32 v132, v0
	v_mul_f32_e32 v0, 0x3d372713, v123
	v_mul_f32_e32 v0, v123, v0
	v_fma_f32 v0, v123, v0, v123
	v_mul_f32_e32 v0, 0x3fcc422a, v0
	v_mul_f32_e32 v0, 0xbfb8aa3b, v0
	v_exp_f32_e32 v0, v0
	s_nop 0
	v_add_f32_e32 v0, 1.0, v0
	v_rcp_f32_e32 v133, v0
	s_nop 0
	v_pk_mul_f32 v[132:133], v[122:123], v[132:133]
	v_pk_add_f32 v[122:123], v[124:125], v[48:49]
	s_nop 0
	v_mul_f32_e32 v0, 0x3d372713, v122
	v_mul_f32_e32 v0, v122, v0
	v_fma_f32 v0, v122, v0, v122
	v_mul_f32_e32 v0, 0x3fcc422a, v0
	v_mul_f32_e32 v0, 0xbfb8aa3b, v0
	v_exp_f32_e32 v0, v0
	s_nop 0
	v_add_f32_e32 v0, 1.0, v0
	v_rcp_f32_e32 v124, v0
	v_mul_f32_e32 v0, 0x3d372713, v123
	v_mul_f32_e32 v0, v123, v0
	v_fma_f32 v0, v123, v0, v123
	v_mul_f32_e32 v0, 0x3fcc422a, v0
	v_mul_f32_e32 v0, 0xbfb8aa3b, v0
	v_exp_f32_e32 v0, v0
	s_nop 0
	v_add_f32_e32 v0, 1.0, v0
	v_rcp_f32_e32 v125, v0
	v_mul_f32_e32 v0, 0x3d372713, v118
	v_mul_f32_e32 v0, v118, v0
	v_fma_f32 v0, v118, v0, v118
	v_mul_f32_e32 v0, 0x3fcc422a, v0
	v_mul_f32_e32 v0, 0xbfb8aa3b, v0
	v_exp_f32_e32 v0, v0
	v_pk_mul_f32 v[134:135], v[122:123], v[124:125]
	v_cvt_pk_bf16_f32 v122, v126, v127
	v_cvt_pk_bf16_f32 v123, v128, v129
	v_cvt_pk_bf16_f32 v124, v132, v133
	v_cvt_pk_bf16_f32 v125, v134, v135
	v_add_f32_e32 v0, 1.0, v0
	global_store_dwordx4 v[130:131], v[122:125], off
	s_nop 1
	v_rcp_f32_e32 v122, v0
	v_mul_f32_e32 v0, 0x3d372713, v119
	v_mul_f32_e32 v0, v119, v0
	v_fma_f32 v0, v119, v0, v119
	v_mul_f32_e32 v0, 0x3fcc422a, v0
	v_mul_f32_e32 v0, 0xbfb8aa3b, v0
	v_exp_f32_e32 v0, v0
	s_nop 0
	v_add_f32_e32 v0, 1.0, v0
	v_rcp_f32_e32 v123, v0
	v_mul_f32_e32 v0, 0x3d372713, v120
	v_mul_f32_e32 v0, v120, v0
	v_fma_f32 v0, v120, v0, v120
	v_mul_f32_e32 v0, 0x3fcc422a, v0
	v_mul_f32_e32 v0, 0xbfb8aa3b, v0
	v_exp_f32_e32 v0, v0
	v_pk_mul_f32 v[118:119], v[118:119], v[122:123]
	v_add_f32_e32 v0, 1.0, v0
	v_rcp_f32_e32 v122, v0
	v_mul_f32_e32 v0, 0x3d372713, v121
	v_mul_f32_e32 v0, v121, v0
	v_fma_f32 v0, v121, v0, v121
	v_mul_f32_e32 v0, 0x3fcc422a, v0
	v_mul_f32_e32 v0, 0xbfb8aa3b, v0
	v_exp_f32_e32 v0, v0
	s_nop 0
	v_add_f32_e32 v0, 1.0, v0
	v_rcp_f32_e32 v123, v0
	v_mul_f32_e32 v0, 0x3d372713, v114
	v_mul_f32_e32 v0, v114, v0
	v_fma_f32 v0, v114, v0, v114
	v_mul_f32_e32 v0, 0x3fcc422a, v0
	v_mul_f32_e32 v0, 0xbfb8aa3b, v0
	v_exp_f32_e32 v0, v0
	v_pk_mul_f32 v[120:121], v[120:121], v[122:123]
	v_add_f32_e32 v0, 1.0, v0
	v_rcp_f32_e32 v122, v0
	v_mul_f32_e32 v0, 0x3d372713, v115
	v_mul_f32_e32 v0, v115, v0
	v_fma_f32 v0, v115, v0, v115
	v_mul_f32_e32 v0, 0x3fcc422a, v0
	v_mul_f32_e32 v0, 0xbfb8aa3b, v0
	v_exp_f32_e32 v0, v0
	s_nop 0
	v_add_f32_e32 v0, 1.0, v0
	v_rcp_f32_e32 v123, v0
	s_nop 0
	v_pk_mul_f32 v[122:123], v[114:115], v[122:123]
	v_pk_add_f32 v[114:115], v[116:117], v[40:41]
	s_nop 0
	v_mul_f32_e32 v0, 0x3d372713, v114
	v_mul_f32_e32 v0, v114, v0
	v_fma_f32 v0, v114, v0, v114
	v_mul_f32_e32 v0, 0x3fcc422a, v0
	v_mul_f32_e32 v0, 0xbfb8aa3b, v0
	v_exp_f32_e32 v0, v0
	s_nop 0
	v_add_f32_e32 v0, 1.0, v0
	v_rcp_f32_e32 v116, v0
	v_mul_f32_e32 v0, 0x3d372713, v115
; __device__ __forceinline__ unsigned pk2(float lo, float hi) { const f32x2 f = {lo, hi}; const bf16n2 v = __builtin_convertvector(f, bf16n2); return __builtin_bit_cast(unsigned, v); }
; __device__ __forceinline__ float sigmoidf_(float x) { return __builtin_amdgcn_rcpf(1.0f + __expf(-x)); }
;     __device__ __forceinline__ bool operator()(f32x4 (&acc)[2][2][4][2], const Unit& u, int wr, int wc, int fr, int fq) const {
;     ...
;             for (int j = 0; j < 8; ++j) bv[bj][j] = bh[kv * 256 + col0 + bj * HALF + j];
; #pragma unroll
;         for (int ai = 0; ai < 2; ++ai)
; #pragma unroll
;             for (int m = 0; m < 4; ++m) { bf16_t* rowp = hid + ((size_t)kv * 2048 + row0 + ai * HALF + m * 16) * 256 + col0;
; #pragma unroll
;                 for (int bj = 0; bj < 2; ++bj) { float o[8];
; #pragma unroll
;                     for (int j = 0; j < 8; ++j) { const float x = acc[ai][bj][m][j >> 2][j & 3] + bv[bj][j];
;                         o[j] = x * sigmoidf_(1.5957691216f * (x + 0.044715f * x * x * x)); }
;                     u32x4 w; w.x = pk2(o[0], o[1]); w.y = pk2(o[2], o[3]); w.z = pk2(o[4], o[5]); w.w = pk2(o[6], o[7]);
;                     *(u32x4*)(rowp + bj * HALF) = w; } }
	v_mul_f32_e32 v0, v115, v0
	v_fma_f32 v0, v115, v0, v115
	v_mul_f32_e32 v0, 0x3fcc422a, v0
	v_mul_f32_e32 v0, 0xbfb8aa3b, v0
	v_exp_f32_e32 v0, v0
	s_nop 0
	v_add_f32_e32 v0, 1.0, v0
	v_rcp_f32_e32 v117, v0
	v_mul_f32_e32 v0, 0x3d372713, v110
	v_mul_f32_e32 v0, v110, v0
	v_fma_f32 v0, v110, v0, v110
	v_mul_f32_e32 v0, 0x3fcc422a, v0
	v_mul_f32_e32 v0, 0xbfb8aa3b, v0
	v_exp_f32_e32 v0, v0
	v_pk_mul_f32 v[124:125], v[114:115], v[116:117]
	v_cvt_pk_bf16_f32 v114, v118, v119
	v_cvt_pk_bf16_f32 v115, v120, v121
	v_cvt_pk_bf16_f32 v116, v122, v123
	v_cvt_pk_bf16_f32 v117, v124, v125
	v_add_f32_e32 v0, 1.0, v0
	global_store_dwordx4 v[130:131], v[114:117], off offset:256
	s_nop 1
	v_rcp_f32_e32 v116, v0
	v_mul_f32_e32 v0, 0x3d372713, v111
	v_mul_f32_e32 v0, v111, v0
	v_fma_f32 v0, v111, v0, v111
	v_mul_f32_e32 v0, 0x3fcc422a, v0
	v_mul_f32_e32 v0, 0xbfb8aa3b, v0
	v_exp_f32_e32 v0, v0
	v_or_b32_e32 v114, 0x4000, v160
	v_mov_b32_e32 v115, v161
	v_lshl_add_u64 v[114:115], v[152:153], 0, v[114:115]
	v_add_f32_e32 v0, 1.0, v0
	v_rcp_f32_e32 v117, v0
	v_mul_f32_e32 v0, 0x3d372713, v112
	v_mul_f32_e32 v0, v112, v0
	v_fma_f32 v0, v112, v0, v112
	v_mul_f32_e32 v0, 0x3fcc422a, v0
	v_mul_f32_e32 v0, 0xbfb8aa3b, v0
	v_exp_f32_e32 v0, v0
	v_pk_mul_f32 v[110:111], v[110:111], v[116:117]
	v_or_b32_e32 v160, 0x6000, v160
	v_add_f32_e32 v0, 1.0, v0
	v_rcp_f32_e32 v116, v0
	v_mul_f32_e32 v0, 0x3d372713, v113
	v_mul_f32_e32 v0, v113, v0
	v_fma_f32 v0, v113, v0, v113
	v_mul_f32_e32 v0, 0x3fcc422a, v0
	v_mul_f32_e32 v0, 0xbfb8aa3b, v0
	v_exp_f32_e32 v0, v0
	s_nop 0
	v_add_f32_e32 v0, 1.0, v0
	v_rcp_f32_e32 v117, v0
	v_mul_f32_e32 v0, 0x3d372713, v106
	v_mul_f32_e32 v0, v106, v0
	v_fma_f32 v0, v106, v0, v106
	v_mul_f32_e32 v0, 0x3fcc422a, v0
	v_mul_f32_e32 v0, 0xbfb8aa3b, v0
	v_exp_f32_e32 v0, v0
	v_pk_mul_f32 v[112:113], v[112:113], v[116:117]
	v_add_f32_e32 v0, 1.0, v0
	v_rcp_f32_e32 v116, v0
	v_mul_f32_e32 v0, 0x3d372713, v107
	v_mul_f32_e32 v0, v107, v0
	v_fma_f32 v0, v107, v0, v107
	v_mul_f32_e32 v0, 0x3fcc422a, v0
	v_mul_f32_e32 v0, 0xbfb8aa3b, v0
	v_exp_f32_e32 v0, v0
	s_nop 0
	v_add_f32_e32 v0, 1.0, v0
	v_rcp_f32_e32 v117, v0
	s_nop 0
	v_pk_mul_f32 v[116:117], v[106:107], v[116:117]
	v_pk_add_f32 v[106:107], v[108:109], v[48:49]
	s_nop 0
	v_mul_f32_e32 v0, 0x3d372713, v106
	v_mul_f32_e32 v0, v106, v0
	v_fma_f32 v0, v106, v0, v106
	v_mul_f32_e32 v0, 0x3fcc422a, v0
	v_mul_f32_e32 v0, 0xbfb8aa3b, v0
	v_exp_f32_e32 v0, v0
	s_nop 0
	v_add_f32_e32 v0, 1.0, v0
	v_rcp_f32_e32 v108, v0
	v_mul_f32_e32 v0, 0x3d372713, v107
	v_mul_f32_e32 v0, v107, v0
	v_fma_f32 v0, v107, v0, v107
	v_mul_f32_e32 v0, 0x3fcc422a, v0
	v_mul_f32_e32 v0, 0xbfb8aa3b, v0
	v_exp_f32_e32 v0, v0
	s_nop 0
	v_add_f32_e32 v0, 1.0, v0
	v_rcp_f32_e32 v109, v0
	v_mul_f32_e32 v0, 0x3d372713, v102
	v_mul_f32_e32 v0, v102, v0
	v_fma_f32 v0, v102, v0, v102
	v_mul_f32_e32 v0, 0x3fcc422a, v0
	v_mul_f32_e32 v0, 0xbfb8aa3b, v0
	v_exp_f32_e32 v0, v0
	v_pk_mul_f32 v[118:119], v[106:107], v[108:109]
	v_cvt_pk_bf16_f32 v106, v110, v111
	v_cvt_pk_bf16_f32 v107, v112, v113
	v_cvt_pk_bf16_f32 v108, v116, v117
	v_cvt_pk_bf16_f32 v109, v118, v119
	v_add_f32_e32 v0, 1.0, v0
	global_store_dwordx4 v[114:115], v[106:109], off
	s_nop 1
	v_rcp_f32_e32 v106, v0
	v_mul_f32_e32 v0, 0x3d372713, v103
	v_mul_f32_e32 v0, v103, v0
	v_fma_f32 v0, v103, v0, v103
	v_mul_f32_e32 v0, 0x3fcc422a, v0
	v_mul_f32_e32 v0, 0xbfb8aa3b, v0
	v_exp_f32_e32 v0, v0
	s_nop 0
	v_add_f32_e32 v0, 1.0, v0
	v_rcp_f32_e32 v107, v0
	v_mul_f32_e32 v0, 0x3d372713, v104
	v_mul_f32_e32 v0, v104, v0
	v_fma_f32 v0, v104, v0, v104
	v_mul_f32_e32 v0, 0x3fcc422a, v0
	v_mul_f32_e32 v0, 0xbfb8aa3b, v0
	v_exp_f32_e32 v0, v0
	v_pk_mul_f32 v[102:103], v[102:103], v[106:107]
	v_add_f32_e32 v0, 1.0, v0
	v_rcp_f32_e32 v106, v0
	v_mul_f32_e32 v0, 0x3d372713, v105
	v_mul_f32_e32 v0, v105, v0
	v_fma_f32 v0, v105, v0, v105
	v_mul_f32_e32 v0, 0x3fcc422a, v0
	v_mul_f32_e32 v0, 0xbfb8aa3b, v0
	v_exp_f32_e32 v0, v0
	s_nop 0
	v_add_f32_e32 v0, 1.0, v0
	v_rcp_f32_e32 v107, v0
	v_mul_f32_e32 v0, 0x3d372713, v98
	v_mul_f32_e32 v0, v98, v0
	v_fma_f32 v0, v98, v0, v98
	v_mul_f32_e32 v0, 0x3fcc422a, v0
	v_mul_f32_e32 v0, 0xbfb8aa3b, v0
	v_exp_f32_e32 v0, v0
	v_pk_mul_f32 v[104:105], v[104:105], v[106:107]
	v_add_f32_e32 v0, 1.0, v0
	v_rcp_f32_e32 v106, v0
	v_mul_f32_e32 v0, 0x3d372713, v99
	v_mul_f32_e32 v0, v99, v0
	v_fma_f32 v0, v99, v0, v99
	v_mul_f32_e32 v0, 0x3fcc422a, v0
	v_mul_f32_e32 v0, 0xbfb8aa3b, v0
	v_exp_f32_e32 v0, v0
	s_nop 0
	v_add_f32_e32 v0, 1.0, v0
	v_rcp_f32_e32 v107, v0
	s_nop 0
	v_pk_mul_f32 v[106:107], v[98:99], v[106:107]
	v_pk_add_f32 v[98:99], v[100:101], v[40:41]
	s_nop 0
	v_mul_f32_e32 v0, 0x3d372713, v98
	v_mul_f32_e32 v0, v98, v0
	v_fma_f32 v0, v98, v0, v98
	v_mul_f32_e32 v0, 0x3fcc422a, v0
	v_mul_f32_e32 v0, 0xbfb8aa3b, v0
	v_exp_f32_e32 v0, v0
	s_nop 0
	v_add_f32_e32 v0, 1.0, v0
	v_rcp_f32_e32 v100, v0
	v_mul_f32_e32 v0, 0x3d372713, v99
	v_mul_f32_e32 v0, v99, v0
	v_fma_f32 v0, v99, v0, v99
	v_mul_f32_e32 v0, 0x3fcc422a, v0
	v_mul_f32_e32 v0, 0xbfb8aa3b, v0
	v_exp_f32_e32 v0, v0
	s_nop 0
	v_add_f32_e32 v0, 1.0, v0
	v_rcp_f32_e32 v101, v0
	v_mul_f32_e32 v0, 0x3d372713, v94
	v_mul_f32_e32 v0, v94, v0
	v_fma_f32 v0, v94, v0, v94
	v_mul_f32_e32 v0, 0x3fcc422a, v0
	v_mul_f32_e32 v0, 0xbfb8aa3b, v0
	v_exp_f32_e32 v0, v0
	v_pk_mul_f32 v[108:109], v[98:99], v[100:101]
	v_cvt_pk_bf16_f32 v98, v102, v103
	v_cvt_pk_bf16_f32 v99, v104, v105
	v_cvt_pk_bf16_f32 v100, v106, v107
	v_cvt_pk_bf16_f32 v101, v108, v109
	v_add_f32_e32 v0, 1.0, v0
	global_store_dwordx4 v[114:115], v[98:101], off offset:256
	s_nop 1
	v_rcp_f32_e32 v100, v0
	v_mul_f32_e32 v0, 0x3d372713, v95
; __device__ __forceinline__ unsigned pk2(float lo, float hi) { const f32x2 f = {lo, hi}; const bf16n2 v = __builtin_convertvector(f, bf16n2); return __builtin_bit_cast(unsigned, v); }
; __device__ __forceinline__ float sigmoidf_(float x) { return __builtin_amdgcn_rcpf(1.0f + __expf(-x)); }
;     __device__ __forceinline__ bool operator()(f32x4 (&acc)[2][2][4][2], const Unit& u, int wr, int wc, int fr, int fq) const {
;     ...
;             for (int j = 0; j < 8; ++j) bv[bj][j] = bh[kv * 256 + col0 + bj * HALF + j];
; #pragma unroll
;         for (int ai = 0; ai < 2; ++ai)
; #pragma unroll
;             for (int m = 0; m < 4; ++m) { bf16_t* rowp = hid + ((size_t)kv * 2048 + row0 + ai * HALF + m * 16) * 256 + col0;
; #pragma unroll
;                 for (int bj = 0; bj < 2; ++bj) { float o[8];
; #pragma unroll
;                     for (int j = 0; j < 8; ++j) { const float x = acc[ai][bj][m][j >> 2][j & 3] + bv[bj][j];
;                         o[j] = x * sigmoidf_(1.5957691216f * (x + 0.044715f * x * x * x)); }
;                     u32x4 w; w.x = pk2(o[0], o[1]); w.y = pk2(o[2], o[3]); w.z = pk2(o[4], o[5]); w.w = pk2(o[6], o[7]);
;                     *(u32x4*)(rowp + bj * HALF) = w; } }
	v_mul_f32_e32 v0, v95, v0
	v_fma_f32 v0, v95, v0, v95
	v_mul_f32_e32 v0, 0x3fcc422a, v0
	v_mul_f32_e32 v0, 0xbfb8aa3b, v0
	v_exp_f32_e32 v0, v0
	v_lshl_add_u64 v[98:99], v[152:153], 0, v[160:161]
	v_add_f32_e32 v0, 1.0, v0
	v_rcp_f32_e32 v101, v0
	v_mul_f32_e32 v0, 0x3d372713, v96
	v_mul_f32_e32 v0, v96, v0
	v_fma_f32 v0, v96, v0, v96
	v_mul_f32_e32 v0, 0x3fcc422a, v0
	v_mul_f32_e32 v0, 0xbfb8aa3b, v0
	v_exp_f32_e32 v0, v0
	v_pk_mul_f32 v[94:95], v[94:95], v[100:101]
	v_add_f32_e32 v0, 1.0, v0
	v_rcp_f32_e32 v100, v0
	v_mul_f32_e32 v0, 0x3d372713, v97
	v_mul_f32_e32 v0, v97, v0
	v_fma_f32 v0, v97, v0, v97
	v_mul_f32_e32 v0, 0x3fcc422a, v0
	v_mul_f32_e32 v0, 0xbfb8aa3b, v0
	v_exp_f32_e32 v0, v0
	s_nop 0
	v_add_f32_e32 v0, 1.0, v0
	v_rcp_f32_e32 v101, v0
	v_mul_f32_e32 v0, 0x3d372713, v90
	v_mul_f32_e32 v0, v90, v0
	v_fma_f32 v0, v90, v0, v90
	v_mul_f32_e32 v0, 0x3fcc422a, v0
	v_mul_f32_e32 v0, 0xbfb8aa3b, v0
	v_exp_f32_e32 v0, v0
	v_pk_mul_f32 v[96:97], v[96:97], v[100:101]
	v_add_f32_e32 v0, 1.0, v0
	v_rcp_f32_e32 v100, v0
	v_mul_f32_e32 v0, 0x3d372713, v91
	v_mul_f32_e32 v0, v91, v0
	v_fma_f32 v0, v91, v0, v91
	v_mul_f32_e32 v0, 0x3fcc422a, v0
	v_mul_f32_e32 v0, 0xbfb8aa3b, v0
	v_exp_f32_e32 v0, v0
	s_nop 0
	v_add_f32_e32 v0, 1.0, v0
	v_rcp_f32_e32 v101, v0
	s_nop 0
	v_pk_mul_f32 v[100:101], v[90:91], v[100:101]
	v_pk_add_f32 v[90:91], v[92:93], v[48:49]
	s_nop 0
	v_mul_f32_e32 v0, 0x3d372713, v90
	v_mul_f32_e32 v0, v90, v0
	v_fma_f32 v0, v90, v0, v90
	v_mul_f32_e32 v0, 0x3fcc422a, v0
	v_mul_f32_e32 v0, 0xbfb8aa3b, v0
	v_exp_f32_e32 v0, v0
	s_nop 0
	v_add_f32_e32 v0, 1.0, v0
	v_rcp_f32_e32 v92, v0
	v_mul_f32_e32 v0, 0x3d372713, v91
	v_mul_f32_e32 v0, v91, v0
	v_fma_f32 v0, v91, v0, v91
	v_mul_f32_e32 v0, 0x3fcc422a, v0
	v_mul_f32_e32 v0, 0xbfb8aa3b, v0
	v_exp_f32_e32 v0, v0
	s_nop 0
	v_add_f32_e32 v0, 1.0, v0
	v_rcp_f32_e32 v93, v0
	v_mul_f32_e32 v0, 0x3d372713, v86
	v_mul_f32_e32 v0, v86, v0
	v_fma_f32 v0, v86, v0, v86
	v_mul_f32_e32 v0, 0x3fcc422a, v0
	v_mul_f32_e32 v0, 0xbfb8aa3b, v0
	v_exp_f32_e32 v0, v0
	v_pk_mul_f32 v[102:103], v[90:91], v[92:93]
	v_cvt_pk_bf16_f32 v90, v94, v95
	v_cvt_pk_bf16_f32 v91, v96, v97
	v_cvt_pk_bf16_f32 v92, v100, v101
	v_cvt_pk_bf16_f32 v93, v102, v103
	v_add_f32_e32 v0, 1.0, v0
	global_store_dwordx4 v[98:99], v[90:93], off
	s_nop 1
	v_rcp_f32_e32 v90, v0
	v_mul_f32_e32 v0, 0x3d372713, v87
	v_mul_f32_e32 v0, v87, v0
	v_fma_f32 v0, v87, v0, v87
	v_mul_f32_e32 v0, 0x3fcc422a, v0
	v_mul_f32_e32 v0, 0xbfb8aa3b, v0
	v_exp_f32_e32 v0, v0
	s_nop 0
	v_add_f32_e32 v0, 1.0, v0
	v_rcp_f32_e32 v91, v0
	v_mul_f32_e32 v0, 0x3d372713, v88
	v_mul_f32_e32 v0, v88, v0
	v_fma_f32 v0, v88, v0, v88
	v_mul_f32_e32 v0, 0x3fcc422a, v0
	v_mul_f32_e32 v0, 0xbfb8aa3b, v0
	v_exp_f32_e32 v0, v0
	v_pk_mul_f32 v[86:87], v[86:87], v[90:91]
	v_add_f32_e32 v0, 1.0, v0
	v_rcp_f32_e32 v90, v0
	v_mul_f32_e32 v0, 0x3d372713, v89
	v_mul_f32_e32 v0, v89, v0
	v_fma_f32 v0, v89, v0, v89
	v_mul_f32_e32 v0, 0x3fcc422a, v0
	v_mul_f32_e32 v0, 0xbfb8aa3b, v0
	v_exp_f32_e32 v0, v0
	s_nop 0
	v_add_f32_e32 v0, 1.0, v0
	v_rcp_f32_e32 v91, v0
	v_mul_f32_e32 v0, 0x3d372713, v82
	v_mul_f32_e32 v0, v82, v0
	v_fma_f32 v0, v82, v0, v82
	v_mul_f32_e32 v0, 0x3fcc422a, v0
	v_mul_f32_e32 v0, 0xbfb8aa3b, v0
	v_exp_f32_e32 v0, v0
	v_pk_mul_f32 v[88:89], v[88:89], v[90:91]
	v_add_f32_e32 v0, 1.0, v0
	v_rcp_f32_e32 v90, v0
	v_mul_f32_e32 v0, 0x3d372713, v83
	v_mul_f32_e32 v0, v83, v0
	v_fma_f32 v0, v83, v0, v83
	v_mul_f32_e32 v0, 0x3fcc422a, v0
	v_mul_f32_e32 v0, 0xbfb8aa3b, v0
	v_exp_f32_e32 v0, v0
	s_nop 0
	v_add_f32_e32 v0, 1.0, v0
	v_rcp_f32_e32 v91, v0
	s_nop 0
	v_pk_mul_f32 v[90:91], v[82:83], v[90:91]
	v_pk_add_f32 v[82:83], v[84:85], v[40:41]
	s_nop 0
	v_mul_f32_e32 v0, 0x3d372713, v82
	v_mul_f32_e32 v0, v82, v0
	v_fma_f32 v0, v82, v0, v82
	v_mul_f32_e32 v0, 0x3fcc422a, v0
	v_mul_f32_e32 v0, 0xbfb8aa3b, v0
	v_exp_f32_e32 v0, v0
	s_nop 0
	v_add_f32_e32 v0, 1.0, v0
	v_rcp_f32_e32 v84, v0
	v_mul_f32_e32 v0, 0x3d372713, v83
	v_mul_f32_e32 v0, v83, v0
	v_fma_f32 v0, v83, v0, v83
	v_mul_f32_e32 v0, 0x3fcc422a, v0
	v_mul_f32_e32 v0, 0xbfb8aa3b, v0
	v_exp_f32_e32 v0, v0
	s_nop 0
	v_add_f32_e32 v0, 1.0, v0
	v_rcp_f32_e32 v85, v0
	v_mul_f32_e32 v0, 0x3d372713, v78
	v_mul_f32_e32 v0, v78, v0
	v_fma_f32 v0, v78, v0, v78
	v_mul_f32_e32 v0, 0x3fcc422a, v0
	v_mul_f32_e32 v0, 0xbfb8aa3b, v0
	v_exp_f32_e32 v0, v0
	v_pk_mul_f32 v[92:93], v[82:83], v[84:85]
	v_cvt_pk_bf16_f32 v82, v86, v87
	v_cvt_pk_bf16_f32 v83, v88, v89
	v_cvt_pk_bf16_f32 v84, v90, v91
	v_cvt_pk_bf16_f32 v85, v92, v93
	v_add_f32_e32 v0, 1.0, v0
	global_store_dwordx4 v[98:99], v[82:85], off offset:256
	s_nop 1
	v_rcp_f32_e32 v84, v0
	v_mul_f32_e32 v0, 0x3d372713, v79
	v_mul_f32_e32 v0, v79, v0
	v_fma_f32 v0, v79, v0, v79
	v_mul_f32_e32 v0, 0x3fcc422a, v0
	v_mul_f32_e32 v0, 0xbfb8aa3b, v0
	v_exp_f32_e32 v0, v0
	v_lshl_add_u64 v[82:83], v[158:159], 0, s[6:7]
	s_mov_b32 s6, 0x10000
	v_add_f32_e32 v0, 1.0, v0
	v_rcp_f32_e32 v85, v0
	v_mul_f32_e32 v0, 0x3d372713, v80
	v_mul_f32_e32 v0, v80, v0
	v_fma_f32 v0, v80, v0, v80
	v_mul_f32_e32 v0, 0x3fcc422a, v0
	v_mul_f32_e32 v0, 0xbfb8aa3b, v0
	v_exp_f32_e32 v0, v0
	v_pk_mul_f32 v[78:79], v[78:79], v[84:85]
	v_add_f32_e32 v0, 1.0, v0
	v_rcp_f32_e32 v84, v0
	v_mul_f32_e32 v0, 0x3d372713, v81
	v_mul_f32_e32 v0, v81, v0
	v_fma_f32 v0, v81, v0, v81
	v_mul_f32_e32 v0, 0x3fcc422a, v0
	v_mul_f32_e32 v0, 0xbfb8aa3b, v0
	v_exp_f32_e32 v0, v0
	s_nop 0
	v_add_f32_e32 v0, 1.0, v0
	v_rcp_f32_e32 v85, v0
	v_mul_f32_e32 v0, 0x3d372713, v74
	v_mul_f32_e32 v0, v74, v0
	v_fma_f32 v0, v74, v0, v74
	v_mul_f32_e32 v0, 0x3fcc422a, v0
	v_mul_f32_e32 v0, 0xbfb8aa3b, v0
	v_exp_f32_e32 v0, v0
; __device__ __forceinline__ unsigned pk2(float lo, float hi) { const f32x2 f = {lo, hi}; const bf16n2 v = __builtin_convertvector(f, bf16n2); return __builtin_bit_cast(unsigned, v); }
; __device__ __forceinline__ float sigmoidf_(float x) { return __builtin_amdgcn_rcpf(1.0f + __expf(-x)); }
;     __device__ __forceinline__ bool operator()(f32x4 (&acc)[2][2][4][2], const Unit& u, int wr, int wc, int fr, int fq) const {
;     ...
;             for (int j = 0; j < 8; ++j) bv[bj][j] = bh[kv * 256 + col0 + bj * HALF + j];
; #pragma unroll
;         for (int ai = 0; ai < 2; ++ai)
; #pragma unroll
;             for (int m = 0; m < 4; ++m) { bf16_t* rowp = hid + ((size_t)kv * 2048 + row0 + ai * HALF + m * 16) * 256 + col0;
; #pragma unroll
;                 for (int bj = 0; bj < 2; ++bj) { float o[8];
; #pragma unroll
;                     for (int j = 0; j < 8; ++j) { const float x = acc[ai][bj][m][j >> 2][j & 3] + bv[bj][j];
;                         o[j] = x * sigmoidf_(1.5957691216f * (x + 0.044715f * x * x * x)); }
;                     u32x4 w; w.x = pk2(o[0], o[1]); w.y = pk2(o[2], o[3]); w.z = pk2(o[4], o[5]); w.w = pk2(o[6], o[7]);
;                     *(u32x4*)(rowp + bj * HALF) = w; } }
	v_pk_mul_f32 v[80:81], v[80:81], v[84:85]
	v_add_f32_e32 v0, 1.0, v0
	v_rcp_f32_e32 v84, v0
	v_mul_f32_e32 v0, 0x3d372713, v75
	v_mul_f32_e32 v0, v75, v0
	v_fma_f32 v0, v75, v0, v75
	v_mul_f32_e32 v0, 0x3fcc422a, v0
	v_mul_f32_e32 v0, 0xbfb8aa3b, v0
	v_exp_f32_e32 v0, v0
	s_nop 0
	v_add_f32_e32 v0, 1.0, v0
	v_rcp_f32_e32 v85, v0
	s_nop 0
	v_pk_mul_f32 v[84:85], v[74:75], v[84:85]
	v_pk_add_f32 v[74:75], v[76:77], v[48:49]
	s_nop 0
	v_mul_f32_e32 v0, 0x3d372713, v74
	v_mul_f32_e32 v0, v74, v0
	v_fma_f32 v0, v74, v0, v74
	v_mul_f32_e32 v0, 0x3fcc422a, v0
	v_mul_f32_e32 v0, 0xbfb8aa3b, v0
	v_exp_f32_e32 v0, v0
	s_nop 0
	v_add_f32_e32 v0, 1.0, v0
	v_rcp_f32_e32 v76, v0
	v_mul_f32_e32 v0, 0x3d372713, v75
	v_mul_f32_e32 v0, v75, v0
	v_fma_f32 v0, v75, v0, v75
	v_mul_f32_e32 v0, 0x3fcc422a, v0
	v_mul_f32_e32 v0, 0xbfb8aa3b, v0
	v_exp_f32_e32 v0, v0
	s_nop 0
	v_add_f32_e32 v0, 1.0, v0
	v_rcp_f32_e32 v77, v0
	v_mul_f32_e32 v0, 0x3d372713, v70
	v_mul_f32_e32 v0, v70, v0
	v_fma_f32 v0, v70, v0, v70
	v_mul_f32_e32 v0, 0x3fcc422a, v0
	v_mul_f32_e32 v0, 0xbfb8aa3b, v0
	v_exp_f32_e32 v0, v0
	v_pk_mul_f32 v[86:87], v[74:75], v[76:77]
	v_cvt_pk_bf16_f32 v74, v78, v79
	v_add_co_u32_e32 v78, vcc, s6, v158
	v_cvt_pk_bf16_f32 v75, v80, v81
	v_cvt_pk_bf16_f32 v76, v84, v85
	v_cvt_pk_bf16_f32 v77, v86, v87
	v_addc_co_u32_e32 v79, vcc, 0, v159, vcc
	v_add_f32_e32 v0, 1.0, v0
	global_store_dwordx4 v[78:79], v[74:77], off
	s_mov_b64 s[6:7], 0x12000
	s_nop 0
	v_rcp_f32_e32 v74, v0
	v_mul_f32_e32 v0, 0x3d372713, v71
	v_mul_f32_e32 v0, v71, v0
	v_fma_f32 v0, v71, v0, v71
	v_mul_f32_e32 v0, 0x3fcc422a, v0
	v_mul_f32_e32 v0, 0xbfb8aa3b, v0
	v_exp_f32_e32 v0, v0
	s_nop 0
	v_add_f32_e32 v0, 1.0, v0
	v_rcp_f32_e32 v75, v0
	v_mul_f32_e32 v0, 0x3d372713, v72
	v_mul_f32_e32 v0, v72, v0
	v_fma_f32 v0, v72, v0, v72
	v_mul_f32_e32 v0, 0x3fcc422a, v0
	v_mul_f32_e32 v0, 0xbfb8aa3b, v0
	v_exp_f32_e32 v0, v0
	v_pk_mul_f32 v[70:71], v[70:71], v[74:75]
	v_add_f32_e32 v0, 1.0, v0
	v_rcp_f32_e32 v74, v0
	v_mul_f32_e32 v0, 0x3d372713, v73
	v_mul_f32_e32 v0, v73, v0
	v_fma_f32 v0, v73, v0, v73
	v_mul_f32_e32 v0, 0x3fcc422a, v0
	v_mul_f32_e32 v0, 0xbfb8aa3b, v0
	v_exp_f32_e32 v0, v0
	s_nop 0
	v_add_f32_e32 v0, 1.0, v0
	v_rcp_f32_e32 v75, v0
	v_mul_f32_e32 v0, 0x3d372713, v62
	v_mul_f32_e32 v0, v62, v0
	v_fma_f32 v0, v62, v0, v62
	v_mul_f32_e32 v0, 0x3fcc422a, v0
	v_mul_f32_e32 v0, 0xbfb8aa3b, v0
	v_exp_f32_e32 v0, v0
	v_pk_mul_f32 v[72:73], v[72:73], v[74:75]
	v_add_f32_e32 v0, 1.0, v0
	v_rcp_f32_e32 v74, v0
	v_mul_f32_e32 v0, 0x3d372713, v63
	v_mul_f32_e32 v0, v63, v0
	v_fma_f32 v0, v63, v0, v63
	v_mul_f32_e32 v0, 0x3fcc422a, v0
	v_mul_f32_e32 v0, 0xbfb8aa3b, v0
	v_exp_f32_e32 v0, v0
	s_nop 0
	v_add_f32_e32 v0, 1.0, v0
	v_rcp_f32_e32 v75, v0
	s_nop 0
	v_pk_mul_f32 v[74:75], v[62:63], v[74:75]
	v_pk_add_f32 v[62:63], v[64:65], v[40:41]
	s_nop 0
	v_mul_f32_e32 v0, 0x3d372713, v62
	v_mul_f32_e32 v0, v62, v0
	v_fma_f32 v0, v62, v0, v62
	v_mul_f32_e32 v0, 0x3fcc422a, v0
	v_mul_f32_e32 v0, 0xbfb8aa3b, v0
	v_exp_f32_e32 v0, v0
	s_nop 0
	v_add_f32_e32 v0, 1.0, v0
	v_rcp_f32_e32 v64, v0
	v_mul_f32_e32 v0, 0x3d372713, v63
	v_mul_f32_e32 v0, v63, v0
	v_fma_f32 v0, v63, v0, v63
	v_mul_f32_e32 v0, 0x3fcc422a, v0
	v_mul_f32_e32 v0, 0xbfb8aa3b, v0
	v_exp_f32_e32 v0, v0
	s_nop 0
	v_add_f32_e32 v0, 1.0, v0
	v_rcp_f32_e32 v65, v0
	v_mul_f32_e32 v0, 0x3d372713, v58
	v_mul_f32_e32 v0, v58, v0
	v_fma_f32 v0, v58, v0, v58
	v_mul_f32_e32 v0, 0x3fcc422a, v0
	v_mul_f32_e32 v0, 0xbfb8aa3b, v0
	v_exp_f32_e32 v0, v0
	v_pk_mul_f32 v[76:77], v[62:63], v[64:65]
	v_cvt_pk_bf16_f32 v62, v70, v71
	v_cvt_pk_bf16_f32 v63, v72, v73
	v_cvt_pk_bf16_f32 v64, v74, v75
	v_cvt_pk_bf16_f32 v65, v76, v77
	v_add_f32_e32 v0, 1.0, v0
	global_store_dwordx4 v[82:83], v[62:65], off offset:256
	s_nop 1
	v_rcp_f32_e32 v64, v0
	v_mul_f32_e32 v0, 0x3d372713, v59
	v_mul_f32_e32 v0, v59, v0
	v_fma_f32 v0, v59, v0, v59
	v_mul_f32_e32 v0, 0x3fcc422a, v0
	v_mul_f32_e32 v0, 0xbfb8aa3b, v0
	v_exp_f32_e32 v0, v0
	v_lshl_add_u64 v[62:63], v[158:159], 0, s[6:7]
	s_mov_b32 s6, 0x12000
	v_add_f32_e32 v0, 1.0, v0
	v_rcp_f32_e32 v65, v0
	v_mul_f32_e32 v0, 0x3d372713, v60
	v_mul_f32_e32 v0, v60, v0
	v_fma_f32 v0, v60, v0, v60
	v_mul_f32_e32 v0, 0x3fcc422a, v0
	v_mul_f32_e32 v0, 0xbfb8aa3b, v0
	v_exp_f32_e32 v0, v0
	v_pk_mul_f32 v[58:59], v[58:59], v[64:65]
	v_add_f32_e32 v0, 1.0, v0
	v_rcp_f32_e32 v64, v0
	v_mul_f32_e32 v0, 0x3d372713, v61
	v_mul_f32_e32 v0, v61, v0
	v_fma_f32 v0, v61, v0, v61
	v_mul_f32_e32 v0, 0x3fcc422a, v0
	v_mul_f32_e32 v0, 0xbfb8aa3b, v0
	v_exp_f32_e32 v0, v0
	s_nop 0
	v_add_f32_e32 v0, 1.0, v0
	v_rcp_f32_e32 v65, v0
	v_mul_f32_e32 v0, 0x3d372713, v50
	v_mul_f32_e32 v0, v50, v0
	v_fma_f32 v0, v50, v0, v50
	v_mul_f32_e32 v0, 0x3fcc422a, v0
	v_mul_f32_e32 v0, 0xbfb8aa3b, v0
	v_exp_f32_e32 v0, v0
	v_pk_mul_f32 v[60:61], v[60:61], v[64:65]
	v_add_f32_e32 v0, 1.0, v0
	v_rcp_f32_e32 v64, v0
	v_mul_f32_e32 v0, 0x3d372713, v51
	v_mul_f32_e32 v0, v51, v0
	v_fma_f32 v0, v51, v0, v51
	v_mul_f32_e32 v0, 0x3fcc422a, v0
	v_mul_f32_e32 v0, 0xbfb8aa3b, v0
	v_exp_f32_e32 v0, v0
	s_nop 0
	v_add_f32_e32 v0, 1.0, v0
	v_rcp_f32_e32 v65, v0
	s_nop 0
	v_pk_mul_f32 v[64:65], v[50:51], v[64:65]
	v_pk_add_f32 v[50:51], v[52:53], v[48:49]
	s_nop 0
	v_mul_f32_e32 v0, 0x3d372713, v50
	v_mul_f32_e32 v0, v50, v0
	v_fma_f32 v0, v50, v0, v50
	v_mul_f32_e32 v0, 0x3fcc422a, v0
	v_mul_f32_e32 v0, 0xbfb8aa3b, v0
	v_exp_f32_e32 v0, v0
	s_nop 0
	v_add_f32_e32 v0, 1.0, v0
	v_rcp_f32_e32 v52, v0
	v_mul_f32_e32 v0, 0x3d372713, v51
	v_mul_f32_e32 v0, v51, v0
	v_fma_f32 v0, v51, v0, v51
	v_mul_f32_e32 v0, 0x3fcc422a, v0
	v_mul_f32_e32 v0, 0xbfb8aa3b, v0
	v_exp_f32_e32 v0, v0
; __device__ __forceinline__ unsigned pk2(float lo, float hi) { const f32x2 f = {lo, hi}; const bf16n2 v = __builtin_convertvector(f, bf16n2); return __builtin_bit_cast(unsigned, v); }
; __device__ __forceinline__ float sigmoidf_(float x) { return __builtin_amdgcn_rcpf(1.0f + __expf(-x)); }
;     __device__ __forceinline__ bool operator()(f32x4 (&acc)[2][2][4][2], const Unit& u, int wr, int wc, int fr, int fq) const {
;     ...
;             for (int j = 0; j < 8; ++j) bv[bj][j] = bh[kv * 256 + col0 + bj * HALF + j];
; #pragma unroll
;         for (int ai = 0; ai < 2; ++ai)
; #pragma unroll
;             for (int m = 0; m < 4; ++m) { bf16_t* rowp = hid + ((size_t)kv * 2048 + row0 + ai * HALF + m * 16) * 256 + col0;
; #pragma unroll
;                 for (int bj = 0; bj < 2; ++bj) { float o[8];
; #pragma unroll
;                     for (int j = 0; j < 8; ++j) { const float x = acc[ai][bj][m][j >> 2][j & 3] + bv[bj][j];
;                         o[j] = x * sigmoidf_(1.5957691216f * (x + 0.044715f * x * x * x)); }
;                     u32x4 w; w.x = pk2(o[0], o[1]); w.y = pk2(o[2], o[3]); w.z = pk2(o[4], o[5]); w.w = pk2(o[6], o[7]);
;                     *(u32x4*)(rowp + bj * HALF) = w; } }
	s_nop 0
	v_add_f32_e32 v0, 1.0, v0
	v_rcp_f32_e32 v53, v0
	v_mul_f32_e32 v0, 0x3d372713, v42
	v_mul_f32_e32 v0, v42, v0
	v_fma_f32 v0, v42, v0, v42
	v_mul_f32_e32 v0, 0x3fcc422a, v0
	v_mul_f32_e32 v0, 0xbfb8aa3b, v0
	v_exp_f32_e32 v0, v0
	v_pk_mul_f32 v[70:71], v[50:51], v[52:53]
	v_cvt_pk_bf16_f32 v50, v58, v59
	v_add_co_u32_e32 v58, vcc, s6, v158
	v_cvt_pk_bf16_f32 v51, v60, v61
	v_cvt_pk_bf16_f32 v52, v64, v65
	v_cvt_pk_bf16_f32 v53, v70, v71
	v_addc_co_u32_e32 v59, vcc, 0, v159, vcc
	v_add_f32_e32 v0, 1.0, v0
	global_store_dwordx4 v[58:59], v[50:53], off
	s_mov_b64 s[6:7], 0x14000
	s_nop 0
	v_rcp_f32_e32 v50, v0
	v_mul_f32_e32 v0, 0x3d372713, v43
	v_mul_f32_e32 v0, v43, v0
	v_fma_f32 v0, v43, v0, v43
	v_mul_f32_e32 v0, 0x3fcc422a, v0
	v_mul_f32_e32 v0, 0xbfb8aa3b, v0
	v_exp_f32_e32 v0, v0
	s_nop 0
	v_add_f32_e32 v0, 1.0, v0
	v_rcp_f32_e32 v51, v0
	v_mul_f32_e32 v0, 0x3d372713, v44
	v_mul_f32_e32 v0, v44, v0
	v_fma_f32 v0, v44, v0, v44
	v_mul_f32_e32 v0, 0x3fcc422a, v0
	v_mul_f32_e32 v0, 0xbfb8aa3b, v0
	v_exp_f32_e32 v0, v0
	v_pk_mul_f32 v[42:43], v[42:43], v[50:51]
	v_add_f32_e32 v0, 1.0, v0
	v_rcp_f32_e32 v50, v0
	v_mul_f32_e32 v0, 0x3d372713, v45
	v_mul_f32_e32 v0, v45, v0
	v_fma_f32 v0, v45, v0, v45
	v_mul_f32_e32 v0, 0x3fcc422a, v0
	v_mul_f32_e32 v0, 0xbfb8aa3b, v0
	v_exp_f32_e32 v0, v0
	s_nop 0
	v_add_f32_e32 v0, 1.0, v0
	v_rcp_f32_e32 v51, v0
	v_mul_f32_e32 v0, 0x3d372713, v34
	v_mul_f32_e32 v0, v34, v0
	v_fma_f32 v0, v34, v0, v34
	v_mul_f32_e32 v0, 0x3fcc422a, v0
	v_mul_f32_e32 v0, 0xbfb8aa3b, v0
	v_exp_f32_e32 v0, v0
	v_pk_mul_f32 v[44:45], v[44:45], v[50:51]
	v_add_f32_e32 v0, 1.0, v0
	v_rcp_f32_e32 v50, v0
	v_mul_f32_e32 v0, 0x3d372713, v35
	v_mul_f32_e32 v0, v35, v0
	v_fma_f32 v0, v35, v0, v35
	v_mul_f32_e32 v0, 0x3fcc422a, v0
	v_mul_f32_e32 v0, 0xbfb8aa3b, v0
	v_exp_f32_e32 v0, v0
	s_nop 0
	v_add_f32_e32 v0, 1.0, v0
	v_rcp_f32_e32 v51, v0
	s_nop 0
	v_pk_mul_f32 v[50:51], v[34:35], v[50:51]
	v_pk_add_f32 v[34:35], v[36:37], v[40:41]
	s_nop 0
	v_mul_f32_e32 v0, 0x3d372713, v34
	v_mul_f32_e32 v0, v34, v0
	v_fma_f32 v0, v34, v0, v34
	v_mul_f32_e32 v0, 0x3fcc422a, v0
	v_mul_f32_e32 v0, 0xbfb8aa3b, v0
	v_exp_f32_e32 v0, v0
	s_nop 0
	v_add_f32_e32 v0, 1.0, v0
	v_rcp_f32_e32 v36, v0
	v_mul_f32_e32 v0, 0x3d372713, v35
	v_mul_f32_e32 v0, v35, v0
	v_fma_f32 v0, v35, v0, v35
	v_mul_f32_e32 v0, 0x3fcc422a, v0
	v_mul_f32_e32 v0, 0xbfb8aa3b, v0
	v_exp_f32_e32 v0, v0
	s_nop 0
	v_add_f32_e32 v0, 1.0, v0
	v_rcp_f32_e32 v37, v0
	v_mul_f32_e32 v0, 0x3d372713, v30
	v_mul_f32_e32 v0, v30, v0
	v_fma_f32 v0, v30, v0, v30
	v_mul_f32_e32 v0, 0x3fcc422a, v0
	v_mul_f32_e32 v0, 0xbfb8aa3b, v0
	v_exp_f32_e32 v0, v0
	v_pk_mul_f32 v[52:53], v[34:35], v[36:37]
	v_cvt_pk_bf16_f32 v34, v42, v43
	v_cvt_pk_bf16_f32 v35, v44, v45
	v_cvt_pk_bf16_f32 v36, v50, v51
	v_cvt_pk_bf16_f32 v37, v52, v53
	v_add_f32_e32 v0, 1.0, v0
	global_store_dwordx4 v[62:63], v[34:37], off offset:256
	s_nop 1
	v_rcp_f32_e32 v36, v0
	v_mul_f32_e32 v0, 0x3d372713, v31
	v_mul_f32_e32 v0, v31, v0
	v_fma_f32 v0, v31, v0, v31
	v_mul_f32_e32 v0, 0x3fcc422a, v0
	v_mul_f32_e32 v0, 0xbfb8aa3b, v0
	v_exp_f32_e32 v0, v0
	v_lshl_add_u64 v[34:35], v[158:159], 0, s[6:7]
	s_mov_b32 s6, 0x14000
	v_add_f32_e32 v0, 1.0, v0
	v_rcp_f32_e32 v37, v0
	v_mul_f32_e32 v0, 0x3d372713, v32
	v_mul_f32_e32 v0, v32, v0
	v_fma_f32 v0, v32, v0, v32
	v_mul_f32_e32 v0, 0x3fcc422a, v0
	v_mul_f32_e32 v0, 0xbfb8aa3b, v0
	v_exp_f32_e32 v0, v0
	v_pk_mul_f32 v[30:31], v[30:31], v[36:37]
	v_add_f32_e32 v0, 1.0, v0
	v_rcp_f32_e32 v36, v0
	v_mul_f32_e32 v0, 0x3d372713, v33
	v_mul_f32_e32 v0, v33, v0
	v_fma_f32 v0, v33, v0, v33
	v_mul_f32_e32 v0, 0x3fcc422a, v0
	v_mul_f32_e32 v0, 0xbfb8aa3b, v0
	v_exp_f32_e32 v0, v0
	s_nop 0
	v_add_f32_e32 v0, 1.0, v0
	v_rcp_f32_e32 v37, v0
	v_mul_f32_e32 v0, 0x3d372713, v26
	v_mul_f32_e32 v0, v26, v0
	v_fma_f32 v0, v26, v0, v26
	v_mul_f32_e32 v0, 0x3fcc422a, v0
	v_mul_f32_e32 v0, 0xbfb8aa3b, v0
	v_exp_f32_e32 v0, v0
	v_pk_mul_f32 v[32:33], v[32:33], v[36:37]
	v_add_f32_e32 v0, 1.0, v0
	v_rcp_f32_e32 v36, v0
	v_mul_f32_e32 v0, 0x3d372713, v27
	v_mul_f32_e32 v0, v27, v0
	v_fma_f32 v0, v27, v0, v27
	v_mul_f32_e32 v0, 0x3fcc422a, v0
	v_mul_f32_e32 v0, 0xbfb8aa3b, v0
	v_exp_f32_e32 v0, v0
	s_nop 0
	v_add_f32_e32 v0, 1.0, v0
	v_rcp_f32_e32 v37, v0
	s_nop 0
	v_pk_mul_f32 v[36:37], v[26:27], v[36:37]
	v_pk_add_f32 v[26:27], v[28:29], v[48:49]
	s_nop 0
	v_mul_f32_e32 v0, 0x3d372713, v26
	v_mul_f32_e32 v0, v26, v0
	v_fma_f32 v0, v26, v0, v26
	v_mul_f32_e32 v0, 0x3fcc422a, v0
	v_mul_f32_e32 v0, 0xbfb8aa3b, v0
	v_exp_f32_e32 v0, v0
	s_nop 0
	v_add_f32_e32 v0, 1.0, v0
	v_rcp_f32_e32 v28, v0
	v_mul_f32_e32 v0, 0x3d372713, v27
	v_mul_f32_e32 v0, v27, v0
	v_fma_f32 v0, v27, v0, v27
	v_mul_f32_e32 v0, 0x3fcc422a, v0
	v_mul_f32_e32 v0, 0xbfb8aa3b, v0
	v_exp_f32_e32 v0, v0
	s_nop 0
	v_add_f32_e32 v0, 1.0, v0
	v_rcp_f32_e32 v29, v0
	v_mul_f32_e32 v0, 0x3d372713, v22
	v_mul_f32_e32 v0, v22, v0
	v_fma_f32 v0, v22, v0, v22
	v_mul_f32_e32 v0, 0x3fcc422a, v0
	v_mul_f32_e32 v0, 0xbfb8aa3b, v0
	v_exp_f32_e32 v0, v0
	v_pk_mul_f32 v[42:43], v[26:27], v[28:29]
	v_cvt_pk_bf16_f32 v26, v30, v31
	v_add_co_u32_e32 v30, vcc, s6, v158
	v_cvt_pk_bf16_f32 v27, v32, v33
	v_cvt_pk_bf16_f32 v28, v36, v37
	v_cvt_pk_bf16_f32 v29, v42, v43
	v_addc_co_u32_e32 v31, vcc, 0, v159, vcc
	v_add_f32_e32 v0, 1.0, v0
	global_store_dwordx4 v[30:31], v[26:29], off
	s_mov_b64 s[6:7], 0x16000
	s_nop 0
	v_rcp_f32_e32 v26, v0
	v_mul_f32_e32 v0, 0x3d372713, v23
	v_mul_f32_e32 v0, v23, v0
	v_fma_f32 v0, v23, v0, v23
	v_mul_f32_e32 v0, 0x3fcc422a, v0
	v_mul_f32_e32 v0, 0xbfb8aa3b, v0
	v_exp_f32_e32 v0, v0
	s_nop 0
	v_add_f32_e32 v0, 1.0, v0
; __device__ __forceinline__ unsigned pk2(float lo, float hi) { const f32x2 f = {lo, hi}; const bf16n2 v = __builtin_convertvector(f, bf16n2); return __builtin_bit_cast(unsigned, v); }
; __device__ __forceinline__ float sigmoidf_(float x) { return __builtin_amdgcn_rcpf(1.0f + __expf(-x)); }
;     __device__ __forceinline__ bool operator()(f32x4 (&acc)[2][2][4][2], const Unit& u, int wr, int wc, int fr, int fq) const {
;     ...
;             for (int j = 0; j < 8; ++j) bv[bj][j] = bh[kv * 256 + col0 + bj * HALF + j];
; #pragma unroll
;         for (int ai = 0; ai < 2; ++ai)
; #pragma unroll
;             for (int m = 0; m < 4; ++m) { bf16_t* rowp = hid + ((size_t)kv * 2048 + row0 + ai * HALF + m * 16) * 256 + col0;
; #pragma unroll
;                 for (int bj = 0; bj < 2; ++bj) { float o[8];
; #pragma unroll
;                     for (int j = 0; j < 8; ++j) { const float x = acc[ai][bj][m][j >> 2][j & 3] + bv[bj][j];
;                         o[j] = x * sigmoidf_(1.5957691216f * (x + 0.044715f * x * x * x)); }
;                     u32x4 w; w.x = pk2(o[0], o[1]); w.y = pk2(o[2], o[3]); w.z = pk2(o[4], o[5]); w.w = pk2(o[6], o[7]);
;                     *(u32x4*)(rowp + bj * HALF) = w; } }
	v_rcp_f32_e32 v27, v0
	v_mul_f32_e32 v0, 0x3d372713, v24
	v_mul_f32_e32 v0, v24, v0
	v_fma_f32 v0, v24, v0, v24
	v_mul_f32_e32 v0, 0x3fcc422a, v0
	v_mul_f32_e32 v0, 0xbfb8aa3b, v0
	v_exp_f32_e32 v0, v0
	v_pk_mul_f32 v[22:23], v[22:23], v[26:27]
	v_add_f32_e32 v0, 1.0, v0
	v_rcp_f32_e32 v26, v0
	v_mul_f32_e32 v0, 0x3d372713, v25
	v_mul_f32_e32 v0, v25, v0
	v_fma_f32 v0, v25, v0, v25
	v_mul_f32_e32 v0, 0x3fcc422a, v0
	v_mul_f32_e32 v0, 0xbfb8aa3b, v0
	v_exp_f32_e32 v0, v0
	s_nop 0
	v_add_f32_e32 v0, 1.0, v0
	v_rcp_f32_e32 v27, v0
	v_mul_f32_e32 v0, 0x3d372713, v18
	v_mul_f32_e32 v0, v18, v0
	v_fma_f32 v0, v18, v0, v18
	v_mul_f32_e32 v0, 0x3fcc422a, v0
	v_mul_f32_e32 v0, 0xbfb8aa3b, v0
	v_exp_f32_e32 v0, v0
	v_pk_mul_f32 v[24:25], v[24:25], v[26:27]
	v_add_f32_e32 v0, 1.0, v0
	v_rcp_f32_e32 v26, v0
	v_mul_f32_e32 v0, 0x3d372713, v19
	v_mul_f32_e32 v0, v19, v0
	v_fma_f32 v0, v19, v0, v19
	v_mul_f32_e32 v0, 0x3fcc422a, v0
	v_mul_f32_e32 v0, 0xbfb8aa3b, v0
	v_exp_f32_e32 v0, v0
	s_nop 0
	v_add_f32_e32 v0, 1.0, v0
	v_rcp_f32_e32 v27, v0
	s_nop 0
	v_pk_mul_f32 v[26:27], v[18:19], v[26:27]
	v_pk_add_f32 v[18:19], v[20:21], v[40:41]
	s_nop 0
	v_mul_f32_e32 v0, 0x3d372713, v18
	v_mul_f32_e32 v0, v18, v0
	v_fma_f32 v0, v18, v0, v18
	v_mul_f32_e32 v0, 0x3fcc422a, v0
	v_mul_f32_e32 v0, 0xbfb8aa3b, v0
	v_exp_f32_e32 v0, v0
	s_nop 0
	v_add_f32_e32 v0, 1.0, v0
	v_rcp_f32_e32 v20, v0
	v_mul_f32_e32 v0, 0x3d372713, v19
	v_mul_f32_e32 v0, v19, v0
	v_fma_f32 v0, v19, v0, v19
	v_mul_f32_e32 v0, 0x3fcc422a, v0
	v_mul_f32_e32 v0, 0xbfb8aa3b, v0
	v_exp_f32_e32 v0, v0
	s_nop 0
	v_add_f32_e32 v0, 1.0, v0
	v_rcp_f32_e32 v21, v0
	v_mul_f32_e32 v0, 0x3d372713, v14
	v_mul_f32_e32 v0, v14, v0
	v_fma_f32 v0, v14, v0, v14
	v_mul_f32_e32 v0, 0x3fcc422a, v0
	v_mul_f32_e32 v0, 0xbfb8aa3b, v0
	v_exp_f32_e32 v0, v0
	v_pk_mul_f32 v[28:29], v[18:19], v[20:21]
	v_cvt_pk_bf16_f32 v18, v22, v23
	v_cvt_pk_bf16_f32 v19, v24, v25
	v_cvt_pk_bf16_f32 v20, v26, v27
	v_cvt_pk_bf16_f32 v21, v28, v29
	v_add_f32_e32 v0, 1.0, v0
	global_store_dwordx4 v[34:35], v[18:21], off offset:256
	s_nop 1
	v_rcp_f32_e32 v20, v0
	v_mul_f32_e32 v0, 0x3d372713, v15
	v_mul_f32_e32 v0, v15, v0
	v_fma_f32 v0, v15, v0, v15
	v_mul_f32_e32 v0, 0x3fcc422a, v0
	v_mul_f32_e32 v0, 0xbfb8aa3b, v0
	v_exp_f32_e32 v0, v0
	v_lshl_add_u64 v[18:19], v[158:159], 0, s[6:7]
	s_mov_b32 s6, 0x16000
	v_add_f32_e32 v0, 1.0, v0
	v_rcp_f32_e32 v21, v0
	v_mul_f32_e32 v0, 0x3d372713, v16
	v_mul_f32_e32 v0, v16, v0
	v_fma_f32 v0, v16, v0, v16
	v_mul_f32_e32 v0, 0x3fcc422a, v0
	v_mul_f32_e32 v0, 0xbfb8aa3b, v0
	v_exp_f32_e32 v0, v0
	v_pk_mul_f32 v[14:15], v[14:15], v[20:21]
	v_add_f32_e32 v0, 1.0, v0
	v_rcp_f32_e32 v20, v0
	v_mul_f32_e32 v0, 0x3d372713, v17
	v_mul_f32_e32 v0, v17, v0
	v_fma_f32 v0, v17, v0, v17
	v_mul_f32_e32 v0, 0x3fcc422a, v0
	v_mul_f32_e32 v0, 0xbfb8aa3b, v0
	v_exp_f32_e32 v0, v0
	s_nop 0
	v_add_f32_e32 v0, 1.0, v0
	v_rcp_f32_e32 v21, v0
	v_mul_f32_e32 v0, 0x3d372713, v10
	v_mul_f32_e32 v0, v10, v0
	v_fma_f32 v0, v10, v0, v10
	v_mul_f32_e32 v0, 0x3fcc422a, v0
	v_mul_f32_e32 v0, 0xbfb8aa3b, v0
	v_exp_f32_e32 v0, v0
	v_pk_mul_f32 v[16:17], v[16:17], v[20:21]
	v_add_f32_e32 v0, 1.0, v0
	v_rcp_f32_e32 v20, v0
	v_mul_f32_e32 v0, 0x3d372713, v11
	v_mul_f32_e32 v0, v11, v0
	v_fma_f32 v0, v11, v0, v11
	v_mul_f32_e32 v0, 0x3fcc422a, v0
	v_mul_f32_e32 v0, 0xbfb8aa3b, v0
	v_exp_f32_e32 v0, v0
	s_nop 0
	v_add_f32_e32 v0, 1.0, v0
	v_rcp_f32_e32 v21, v0
	s_nop 0
	v_pk_mul_f32 v[20:21], v[10:11], v[20:21]
	v_pk_add_f32 v[10:11], v[12:13], v[48:49]
	s_nop 0
	v_mul_f32_e32 v0, 0x3d372713, v10
	v_mul_f32_e32 v0, v10, v0
	v_fma_f32 v0, v10, v0, v10
	v_mul_f32_e32 v0, 0x3fcc422a, v0
	v_mul_f32_e32 v0, 0xbfb8aa3b, v0
	v_exp_f32_e32 v0, v0
	s_nop 0
	v_add_f32_e32 v0, 1.0, v0
	v_rcp_f32_e32 v12, v0
	v_mul_f32_e32 v0, 0x3d372713, v11
	v_mul_f32_e32 v0, v11, v0
	v_fma_f32 v0, v11, v0, v11
	v_mul_f32_e32 v0, 0x3fcc422a, v0
	v_mul_f32_e32 v0, 0xbfb8aa3b, v0
	v_exp_f32_e32 v0, v0
	s_nop 0
	v_add_f32_e32 v0, 1.0, v0
	v_rcp_f32_e32 v13, v0
	v_mul_f32_e32 v0, 0x3d372713, v6
	v_mul_f32_e32 v0, v6, v0
	v_fma_f32 v0, v6, v0, v6
	v_mul_f32_e32 v0, 0x3fcc422a, v0
	v_mul_f32_e32 v0, 0xbfb8aa3b, v0
	v_exp_f32_e32 v0, v0
	v_pk_mul_f32 v[22:23], v[10:11], v[12:13]
	v_cvt_pk_bf16_f32 v10, v14, v15
	v_add_co_u32_e32 v14, vcc, s6, v158
	v_cvt_pk_bf16_f32 v11, v16, v17
	v_cvt_pk_bf16_f32 v12, v20, v21
	v_cvt_pk_bf16_f32 v13, v22, v23
	v_addc_co_u32_e32 v15, vcc, 0, v159, vcc
	v_add_f32_e32 v0, 1.0, v0
	global_store_dwordx4 v[14:15], v[10:13], off
	s_and_b64 vcc, exec, s[0:1]
	s_mov_b64 s[6:7], s[4:5]
	v_rcp_f32_e32 v10, v0
	v_mul_f32_e32 v0, 0x3d372713, v7
	v_mul_f32_e32 v0, v7, v0
	v_fma_f32 v0, v7, v0, v7
	v_mul_f32_e32 v0, 0x3fcc422a, v0
	v_mul_f32_e32 v0, 0xbfb8aa3b, v0
	v_exp_f32_e32 v0, v0
	s_nop 0
	v_add_f32_e32 v0, 1.0, v0
	v_rcp_f32_e32 v11, v0
	v_mul_f32_e32 v0, 0x3d372713, v8
	v_mul_f32_e32 v0, v8, v0
	v_fma_f32 v0, v8, v0, v8
	v_mul_f32_e32 v0, 0x3fcc422a, v0
	v_mul_f32_e32 v0, 0xbfb8aa3b, v0
	v_exp_f32_e32 v0, v0
	v_pk_mul_f32 v[6:7], v[6:7], v[10:11]
	v_add_f32_e32 v0, 1.0, v0
	v_rcp_f32_e32 v10, v0
	v_mul_f32_e32 v0, 0x3d372713, v9
	v_mul_f32_e32 v0, v9, v0
	v_fma_f32 v0, v9, v0, v9
	v_mul_f32_e32 v0, 0x3fcc422a, v0
	v_mul_f32_e32 v0, 0xbfb8aa3b, v0
	v_exp_f32_e32 v0, v0
	s_nop 0
	v_add_f32_e32 v0, 1.0, v0
	v_rcp_f32_e32 v11, v0
	v_mul_f32_e32 v0, 0x3d372713, v2
	v_mul_f32_e32 v0, v2, v0
	v_fma_f32 v0, v2, v0, v2
	v_mul_f32_e32 v0, 0x3fcc422a, v0
	v_mul_f32_e32 v0, 0xbfb8aa3b, v0
	v_exp_f32_e32 v0, v0
	v_pk_mul_f32 v[8:9], v[8:9], v[10:11]
	v_add_f32_e32 v0, 1.0, v0
	v_rcp_f32_e32 v10, v0
	v_mul_f32_e32 v0, 0x3d372713, v3
	v_mul_f32_e32 v0, v3, v0
	v_fma_f32 v0, v3, v0, v3
	v_mul_f32_e32 v0, 0x3fcc422a, v0
	v_mul_f32_e32 v0, 0xbfb8aa3b, v0
	v_exp_f32_e32 v0, v0
	s_nop 0
	v_add_f32_e32 v0, 1.0, v0
	v_rcp_f32_e32 v11, v0
	s_nop 0
	v_pk_mul_f32 v[10:11], v[2:3], v[10:11]
	v_pk_add_f32 v[2:3], v[4:5], v[40:41]
	s_nop 0
	v_mul_f32_e32 v0, 0x3d372713, v2
	v_mul_f32_e32 v0, v2, v0
	v_fma_f32 v0, v2, v0, v2
	v_mul_f32_e32 v0, 0x3fcc422a, v0
	v_mul_f32_e32 v0, 0xbfb8aa3b, v0
	v_exp_f32_e32 v0, v0
	s_nop 0
	v_add_f32_e32 v0, 1.0, v0
	v_rcp_f32_e32 v4, v0
	v_mul_f32_e32 v0, 0x3d372713, v3
	v_mul_f32_e32 v0, v3, v0
	v_fma_f32 v0, v3, v0, v3
	v_mul_f32_e32 v0, 0x3fcc422a, v0
	v_mul_f32_e32 v0, 0xbfb8aa3b, v0
	v_exp_f32_e32 v0, v0
	s_nop 0
	v_add_f32_e32 v0, 1.0, v0
	v_rcp_f32_e32 v5, v0
	s_nop 0
	v_pk_mul_f32 v[12:13], v[2:3], v[4:5]
	v_cvt_pk_bf16_f32 v2, v6, v7
	v_cvt_pk_bf16_f32 v3, v8, v9
	v_cvt_pk_bf16_f32 v4, v10, v11
	v_cvt_pk_bf16_f32 v5, v12, v13
	global_store_dwordx4 v[18:19], v[2:5], off offset:256
	s_cbranch_vccz .LBB0_482

; #define PHASE_END   } if (gp + 1 < hi) xcd_barrier(bar); } ++gp;
; #define RELAUNDER() do { asm volatile("" : "+v"(pc.tid), "+s"(pc.bid)); pc.lane = pc.tid & 63; pc.wave = __builtin_amdgcn_readfirstlane(pc.tid >> 6); } while (0)
; __device__ __forceinline__ void phase_lora_a(const Ctx& c, const Args& a, int layer, const bf16_t* proj, bf16_t* alora) {
;     ...
;     for (int t = c.bid * 16 + rloc; t < T; t += c.G * 16) {
;         const int col = PC_ZW + sub * 8; float cur[8], prv[8];
;         unpack8(*(const u32x4*)(proj + (size_t)t * PLD + col), cur);
;         if (t > 0) unpack8(*(const u32x4*)(proj + (size_t)(t - 1) * PLD + col), prv); else {
; #pragma unroll
;             for (int k = 0; k < 8; ++k) prv[k] = 0.f; }
; __global__ void __launch_bounds__(512, 2) fwd_kernel(Args args) {
;     ...
;                 RELAUNDER();
;                 if (c.bid >= 16) { Ctx cv = c; cv.bid = c.bid - 16; cv.G = c.G - 16; phase_lora_a(cv, args, layer, proj, alora); vt_transpose(cv, proj, vtb); } } PHASE_END
.LBB0_493:
	s_barrier
	v_readlane_b32 s6, v251, 0
	s_sub_i32 s6, s6, 16
	s_cmp_lt_u32 s6, 48
	s_cbranch_scc0 .Lsk_noflag
	v_readlane_b32 s6, v251, 0
	s_and_b32 s6, s6, 15
	s_lshl_b32 s6, s6, 6
	s_addk_i32 s6, 0x4000
	v_readlane_b32 s11, v252, 29
	v_readlane_b32 s13, v252, 30
	s_add_u32 s11, s11, s6
	s_addc_u32 s13, s13, 0
	v_mov_b32_e32 v160, s11
	v_mov_b32_e32 v161, s13
	v_cmp_eq_u32_e32 vcc, 0, v151
	s_and_saveexec_b64 s[8:9], vcc
	v_mov_b32_e32 v159, 1
	global_atomic_add v[160:161], v159, off
	s_waitcnt vmcnt(0)
	s_or_b64 exec, exec, s[8:9]
.Lsk_noflag:
.LBB0_494:
	v_readlane_b32 s16, v252, 47
	s_cmp_lt_i32 s14, 64
	v_readlane_b32 s11, v252, 20
	v_readlane_b32 s12, v253, 43
	v_readlane_b32 s17, v252, 48
	v_readlane_b32 s13, v253, 44
	s_cbranch_scc1 .LBB0_503
	v_readlane_b32 s0, v253, 9
	v_readlane_b32 s1, v253, 10
	s_add_i32 s10, s14, -64
	v_mov_b32_e32 v0, s0
	ds_read_b32 v0, v0
	v_ashrrev_i32_e32 v11, 5, v151
	v_lshl_add_u32 v10, s10, 4, v11
	s_movk_i32 s2, 0x4000
	v_cmp_gt_i32_e32 vcc, s2, v10
	s_waitcnt lgkmcnt(0)
	v_readfirstlane_b32 s0, v0
	v_mov_b32_e32 v0, s1
	ds_read_b32 v0, v0
	s_waitcnt lgkmcnt(0)
	v_readfirstlane_b32 s1, v0
	s_and_saveexec_b64 s[4:5], vcc
	s_cbranch_execz .LBB0_500
	v_readlane_b32 s2, v254, 24
	s_add_u32 s0, s0, s2
	v_and_b32_e32 v12, 31, v151
	s_addc_u32 s1, s1, 0
	v_lshlrev_b32_e32 v0, 5, v12
	v_lshl_add_u64 v[2:3], s[0:1], 0, v[0:1]
	v_add_co_u32_e32 v6, vcc, 0x1000, v2
	v_lshl_add_u32 v11, s14, 4, v11
	s_nop 0
	v_addc_co_u32_e32 v7, vcc, 0, v3, vcc
	flat_load_dwordx4 v[2:5], v[6:7] offset:2048
	s_nop 0
	flat_load_dwordx4 v[6:9], v[6:7] offset:2064
	v_add_u32_e32 v20, 0xfffffbff, v11
	v_ashrrev_i32_e32 v11, 31, v10
	v_lshlrev_b32_e32 v0, 4, v12
	v_cmp_gt_u32_e32 vcc, 8, v12
	v_cmp_gt_u32_e64 s[0:1], 16, v12
	v_lshlrev_b64 v[12:13], 9, v[10:11]
	v_readlane_b32 s2, v252, 18
	v_or_b32_e32 v12, v12, v0
	v_readlane_b32 s3, v252, 19
	v_lshlrev_b64 v[10:11], 13, v[10:11]
	v_or_b32_e32 v10, v10, v0
	v_lshl_add_u64 v[16:17], s[2:3], 0, v[12:13]
	v_readlane_b32 s2, v252, 49
	v_readlane_b32 s3, v252, 50
	v_lshl_add_u64 v[14:15], s[80:81], 0, v[0:1]
	s_mov_b64 s[6:7], 0
	v_lshl_add_u64 v[18:19], s[2:3], 0, v[10:11]
	v_mov_b32_e32 v0, v20
	s_branch .LBB0_498

; #define LAS __attribute__((address_space(3)))
; __device__ __forceinline__ void vt_transpose(const Ctx& c, const bf16_t* proj, bf16_t* vt) {
;     LAS bf16_t* tl = (LAS bf16_t*)c.lds;
;     for (int it = c.bid; it < 3 * 2 * 256; it += c.G) {
;         const int which = it / 512, g = (it >> 8) & 1, tt = it & 255;
;         const int col = (which == 0 ? PC_VS : (which == 1 ? PC_VW : PC_SV)) + g * 64;
;         { const int tok = c.tid >> 3, ch = c.tid & 7; const u32x4 w = *(const u32x4*)(proj + (size_t)(tt * 64 + tok) * PLD + col + ch * 8);
;           *(LAS u32x4*)(tl + tok * 72 + ch * 8) = w; }
.LBB0_500:
	s_or_b64 exec, exec, s[4:5]
	s_cmpk_gt_i32 s14, 0x63f
	s_cbranch_scc1 .LBB0_503
	v_ashrrev_i32_e32 v2, 3, v151
	v_mul_lo_u32 v3, v2, s67
	v_lshlrev_b32_e32 v0, 3, v151
	v_add_u32_e32 v4, 0, v3
	s_movk_i32 s0, 0xff72
	v_and_b32_e32 v0, 56, v0
	v_mad_u64_u32 v[8:9], s[0:1], v2, s0, v[4:5]
	v_ashrrev_i32_e32 v3, 31, v2
	v_lshl_add_u32 v6, v0, 1, v4
	v_mul_u32_u24_e32 v7, 0x90, v0
	v_lshlrev_b64 v[4:5], 15, v[2:3]
	s_lshl_b32 s0, s14, 6
	v_lshl_add_u64 v[4:5], s[82:83], 0, v[4:5]
	s_addk_i32 s0, 0xf000
	v_lshlrev_b32_e32 v0, 1, v0
	v_add_u32_e32 v3, v8, v7
	v_readlane_b32 s5, v252, 52
	s_mov_b32 s6, 0x5040100
	s_mov_b32 s7, s10
	s_min_i32 s15, s10, 0x5ff
	s_bfe_u32 s1, s15, 0x10008
	s_add_i32 s2, s15, 0x1ff
	s_and_b32 s3, s15, 0xfffffe00
	s_cmpk_eq_i32 s3, 0x200
	s_movk_i32 s3, 0xb80
	s_cselect_b32 s3, s3, 0xf80
	s_cmpk_gt_u32 s2, 0x3fe
	s_cselect_b32 s2, s3, 0xa80
	s_lshl_b32 s4, s15, 6
	s_and_b32 s4, s4, 0x3fc0
	v_add_u32_e32 v116, s4, v2
	v_ashrrev_i32_e32 v117, 31, v116
	v_lshlrev_b64 v[116:117], 13, v[116:117]
	s_lshl_b32 s2, s2, 1
	s_lshl_b32 s3, s1, 7
	v_lshl_add_u64 v[116:117], s[80:81], 0, v[116:117]
	s_or_b32 s42, s3, s2
	v_lshl_add_u64 v[116:117], v[116:117], 0, s[42:43]
	v_lshl_add_u64 v[116:117], v[116:117], 0, v[0:1]
	global_load_dwordx4 v[84:87], v[116:117], off
	s_add_i32 s10, s10, s11
	s_min_i32 s15, s10, 0x5ff
	s_bfe_u32 s1, s15, 0x10008
	s_add_i32 s2, s15, 0x1ff
	s_and_b32 s3, s15, 0xfffffe00
	s_cmpk_eq_i32 s3, 0x200
	s_movk_i32 s3, 0xb80
	s_cselect_b32 s3, s3, 0xf80
	s_cmpk_gt_u32 s2, 0x3fe
	s_cselect_b32 s2, s3, 0xa80
	s_lshl_b32 s4, s15, 6
	s_and_b32 s4, s4, 0x3fc0
	v_add_u32_e32 v118, s4, v2
	v_ashrrev_i32_e32 v119, 31, v118
	v_lshlrev_b64 v[118:119], 13, v[118:119]
	s_lshl_b32 s2, s2, 1
	s_lshl_b32 s3, s1, 7
	v_lshl_add_u64 v[118:119], s[80:81], 0, v[118:119]
	s_or_b32 s42, s3, s2
	v_lshl_add_u64 v[118:119], v[118:119], 0, s[42:43]
	v_lshl_add_u64 v[118:119], v[118:119], 0, v[0:1]
	global_load_dwordx4 v[88:91], v[118:119], off
	s_add_i32 s10, s10, s11
	s_min_i32 s15, s10, 0x5ff
	s_bfe_u32 s1, s15, 0x10008
	s_add_i32 s2, s15, 0x1ff
	s_and_b32 s3, s15, 0xfffffe00
	s_cmpk_eq_i32 s3, 0x200
	s_movk_i32 s3, 0xb80
	s_cselect_b32 s3, s3, 0xf80
	s_cmpk_gt_u32 s2, 0x3fe
	s_cselect_b32 s2, s3, 0xa80
	s_lshl_b32 s4, s15, 6
	s_and_b32 s4, s4, 0x3fc0
	v_add_u32_e32 v116, s4, v2
	v_ashrrev_i32_e32 v117, 31, v116
	v_lshlrev_b64 v[116:117], 13, v[116:117]
	s_lshl_b32 s2, s2, 1
	s_lshl_b32 s3, s1, 7
	v_lshl_add_u64 v[116:117], s[80:81], 0, v[116:117]
	s_or_b32 s42, s3, s2
	v_lshl_add_u64 v[116:117], v[116:117], 0, s[42:43]
	v_lshl_add_u64 v[116:117], v[116:117], 0, v[0:1]
	global_load_dwordx4 v[92:95], v[116:117], off
	s_add_i32 s10, s10, s11
	s_min_i32 s15, s10, 0x5ff
	s_bfe_u32 s1, s15, 0x10008
	s_add_i32 s2, s15, 0x1ff
	s_and_b32 s3, s15, 0xfffffe00
	s_cmpk_eq_i32 s3, 0x200
	s_movk_i32 s3, 0xb80
	s_cselect_b32 s3, s3, 0xf80
	s_cmpk_gt_u32 s2, 0x3fe
	s_cselect_b32 s2, s3, 0xa80
	s_lshl_b32 s4, s15, 6
	s_and_b32 s4, s4, 0x3fc0
	v_add_u32_e32 v118, s4, v2
	v_ashrrev_i32_e32 v119, 31, v118
	v_lshlrev_b64 v[118:119], 13, v[118:119]
	s_lshl_b32 s2, s2, 1
	s_lshl_b32 s3, s1, 7
	v_lshl_add_u64 v[118:119], s[80:81], 0, v[118:119]
	s_or_b32 s42, s3, s2
	v_lshl_add_u64 v[118:119], v[118:119], 0, s[42:43]
	v_lshl_add_u64 v[118:119], v[118:119], 0, v[0:1]
	global_load_dwordx4 v[96:99], v[118:119], off
	s_add_i32 s10, s10, s11
	s_min_i32 s15, s10, 0x5ff
	s_bfe_u32 s1, s15, 0x10008
	s_add_i32 s2, s15, 0x1ff
	s_and_b32 s3, s15, 0xfffffe00
	s_cmpk_eq_i32 s3, 0x200
	s_movk_i32 s3, 0xb80
	s_cselect_b32 s3, s3, 0xf80
	s_cmpk_gt_u32 s2, 0x3fe
	s_cselect_b32 s2, s3, 0xa80
	s_lshl_b32 s4, s15, 6
	s_and_b32 s4, s4, 0x3fc0
	v_add_u32_e32 v116, s4, v2
	v_ashrrev_i32_e32 v117, 31, v116
	v_lshlrev_b64 v[116:117], 13, v[116:117]
	s_lshl_b32 s2, s2, 1
	s_lshl_b32 s3, s1, 7
	v_lshl_add_u64 v[116:117], s[80:81], 0, v[116:117]
	s_or_b32 s42, s3, s2
	v_lshl_add_u64 v[116:117], v[116:117], 0, s[42:43]
	v_lshl_add_u64 v[116:117], v[116:117], 0, v[0:1]
	global_load_dwordx4 v[100:103], v[116:117], off
	s_add_i32 s10, s10, s11
	s_min_i32 s15, s10, 0x5ff
	s_bfe_u32 s1, s15, 0x10008
	s_add_i32 s2, s15, 0x1ff
	s_and_b32 s3, s15, 0xfffffe00
	s_cmpk_eq_i32 s3, 0x200
	s_movk_i32 s3, 0xb80
	s_cselect_b32 s3, s3, 0xf80
	s_cmpk_gt_u32 s2, 0x3fe
	s_cselect_b32 s2, s3, 0xa80
	s_lshl_b32 s4, s15, 6
	s_and_b32 s4, s4, 0x3fc0
	v_add_u32_e32 v118, s4, v2
	v_ashrrev_i32_e32 v119, 31, v118
	v_lshlrev_b64 v[118:119], 13, v[118:119]
	s_lshl_b32 s2, s2, 1
	s_lshl_b32 s3, s1, 7
	v_lshl_add_u64 v[118:119], s[80:81], 0, v[118:119]
	s_or_b32 s42, s3, s2
	v_lshl_add_u64 v[118:119], v[118:119], 0, s[42:43]
	v_lshl_add_u64 v[118:119], v[118:119], 0, v[0:1]
	global_load_dwordx4 v[104:107], v[118:119], off
	s_add_i32 s10, s10, s11
	s_min_i32 s15, s10, 0x5ff
	s_bfe_u32 s1, s15, 0x10008
	s_add_i32 s2, s15, 0x1ff
	s_and_b32 s3, s15, 0xfffffe00
	s_cmpk_eq_i32 s3, 0x200
	s_movk_i32 s3, 0xb80
	s_cselect_b32 s3, s3, 0xf80
	s_cmpk_gt_u32 s2, 0x3fe
	s_cselect_b32 s2, s3, 0xa80
	s_lshl_b32 s4, s15, 6
	s_and_b32 s4, s4, 0x3fc0
	v_add_u32_e32 v116, s4, v2
	v_ashrrev_i32_e32 v117, 31, v116
	v_lshlrev_b64 v[116:117], 13, v[116:117]
	s_lshl_b32 s2, s2, 1
	s_lshl_b32 s3, s1, 7
	v_lshl_add_u64 v[116:117], s[80:81], 0, v[116:117]
	s_or_b32 s42, s3, s2
	v_lshl_add_u64 v[116:117], v[116:117], 0, s[42:43]
	v_lshl_add_u64 v[116:117], v[116:117], 0, v[0:1]
	global_load_dwordx4 v[108:111], v[116:117], off
	s_add_i32 s10, s10, s11
	s_min_i32 s15, s10, 0x5ff
	s_bfe_u32 s1, s15, 0x10008
	s_add_i32 s2, s15, 0x1ff
	s_and_b32 s3, s15, 0xfffffe00
	s_cmpk_eq_i32 s3, 0x200
	s_movk_i32 s3, 0xb80
	s_cselect_b32 s3, s3, 0xf80
	s_cmpk_gt_u32 s2, 0x3fe
	s_cselect_b32 s2, s3, 0xa80
	s_lshl_b32 s4, s15, 6
	s_and_b32 s4, s4, 0x3fc0
	v_add_u32_e32 v118, s4, v2
	v_ashrrev_i32_e32 v119, 31, v118
	v_lshlrev_b64 v[118:119], 13, v[118:119]
	s_lshl_b32 s2, s2, 1
	s_lshl_b32 s3, s1, 7
	v_lshl_add_u64 v[118:119], s[80:81], 0, v[118:119]
	s_or_b32 s42, s3, s2
	v_lshl_add_u64 v[118:119], v[118:119], 0, s[42:43]
	v_lshl_add_u64 v[118:119], v[118:119], 0, v[0:1]
	global_load_dwordx4 v[112:115], v[118:119], off
	s_add_i32 s10, s10, s11
	s_mov_b32 s10, s7
	s_cmpk_lt_i32 s10, 0x600
	s_cbranch_scc0 .LBB0_503
; #define LAS __attribute__((address_space(3)))
; __device__ __forceinline__ void vt_transpose(const Ctx& c, const bf16_t* proj, bf16_t* vt) {
;     ...
;     for (int it = c.bid; it < 3 * 2 * 256; it += c.G) {
;         const int which = it / 512, g = (it >> 8) & 1, tt = it & 255;
;         const int col = (which == 0 ? PC_VS : (which == 1 ? PC_VW : PC_SV)) + g * 64;
;         { const int tok = c.tid >> 3, ch = c.tid & 7; const u32x4 w = *(const u32x4*)(proj + (size_t)(tt * 64 + tok) * PLD + col + ch * 8);
;           *(LAS u32x4*)(tl + tok * 72 + ch * 8) = w; }
;         __syncthreads();
;         { const int d = c.tid >> 3, ch = c.tid & 7; unsigned short e[8];
; #pragma unroll
;           for (int k = 0; k < 8; ++k) e[k] = tl[(ch * 8 + k) * 72 + d];
;           u32x4 w; w.x = e[0] | ((unsigned)e[1] << 16); w.y = e[2] | ((unsigned)e[3] << 16); w.z = e[4] | ((unsigned)e[5] << 16); w.w = e[6] | ((unsigned)e[7] << 16);
;           *(u32x4*)(vt + ((size_t)(which * 2 + g) * 64 + d) * T + tt * 64 + ch * 8) = w; }
;         __syncthreads();
	s_bfe_u32 s1, s10, 0x10008
	s_lshl_b32 s4, s10, 6
	s_and_b32 s4, s4, 0x3fc0
	s_ashr_i32 s2, s10, 31
	s_lshr_b32 s2, s2, 23
	s_add_i32 s2, s10, s2
	s_ashr_i32 s2, s2, 9
	s_lshl_b32 s2, s2, 1
	s_or_b32 s2, s2, s1
	s_ashr_i32 s3, s2, 31
	s_lshl_b64 s[2:3], s[2:3], 21
	s_lshl_b32 s42, s4, 1
	s_add_i32 s10, s10, s11
	s_waitcnt vmcnt(7)
	ds_write_b128 v6, v[84:87]
	s_waitcnt lgkmcnt(0)
	s_barrier
	ds_read_u16 v7, v3
	ds_read_u16 v8, v3 offset:144
	ds_read_u16 v9, v3 offset:288
	ds_read_u16 v12, v3 offset:432
	ds_read_u16 v10, v3 offset:576
	ds_read_u16 v13, v3 offset:720
	ds_read_u16 v11, v3 offset:864
	ds_read_u16 v14, v3 offset:1008
	s_waitcnt lgkmcnt(4)
	v_perm_b32 v9, v12, v9, s6
	v_perm_b32 v8, v8, v7, s6
	s_waitcnt lgkmcnt(2)
	v_perm_b32 v10, v13, v10, s6
	v_lshl_add_u64 v[12:13], v[4:5], 0, s[2:3]
	v_lshl_add_u64 v[12:13], v[12:13], 0, s[42:43]
	s_waitcnt lgkmcnt(0)
	v_perm_b32 v11, v14, v11, s6
	v_lshl_add_u64 v[12:13], v[12:13], 0, v[0:1]
	global_store_dwordx4 v[12:13], v[8:11], off
	s_barrier
	s_cmpk_lt_i32 s10, 0x600
	s_cbranch_scc0 .LBB0_503
	s_bfe_u32 s1, s10, 0x10008
	s_lshl_b32 s4, s10, 6
	s_and_b32 s4, s4, 0x3fc0
	s_ashr_i32 s2, s10, 31
	s_lshr_b32 s2, s2, 23
	s_add_i32 s2, s10, s2
	s_ashr_i32 s2, s2, 9
	s_lshl_b32 s2, s2, 1
	s_or_b32 s2, s2, s1
	s_ashr_i32 s3, s2, 31
	s_lshl_b64 s[2:3], s[2:3], 21
	s_lshl_b32 s42, s4, 1
	s_add_i32 s10, s10, s11
	s_waitcnt vmcnt(6)
	ds_write_b128 v6, v[88:91]
	s_waitcnt lgkmcnt(0)
	s_barrier
	ds_read_u16 v7, v3
	ds_read_u16 v8, v3 offset:144
	ds_read_u16 v9, v3 offset:288
	ds_read_u16 v12, v3 offset:432
	ds_read_u16 v10, v3 offset:576
	ds_read_u16 v13, v3 offset:720
	ds_read_u16 v11, v3 offset:864
	ds_read_u16 v14, v3 offset:1008
	s_waitcnt lgkmcnt(4)
	v_perm_b32 v9, v12, v9, s6
	v_perm_b32 v8, v8, v7, s6
	s_waitcnt lgkmcnt(2)
	v_perm_b32 v10, v13, v10, s6
	v_lshl_add_u64 v[12:13], v[4:5], 0, s[2:3]
	v_lshl_add_u64 v[12:13], v[12:13], 0, s[42:43]
	s_waitcnt lgkmcnt(0)
	v_perm_b32 v11, v14, v11, s6
	v_lshl_add_u64 v[12:13], v[12:13], 0, v[0:1]
	global_store_dwordx4 v[12:13], v[8:11], off
	s_barrier
	s_cmpk_lt_i32 s10, 0x600
	s_cbranch_scc0 .LBB0_503
	s_bfe_u32 s1, s10, 0x10008
	s_lshl_b32 s4, s10, 6
	s_and_b32 s4, s4, 0x3fc0
	s_ashr_i32 s2, s10, 31
	s_lshr_b32 s2, s2, 23
	s_add_i32 s2, s10, s2
	s_ashr_i32 s2, s2, 9
	s_lshl_b32 s2, s2, 1
	s_or_b32 s2, s2, s1
	s_ashr_i32 s3, s2, 31
	s_lshl_b64 s[2:3], s[2:3], 21
	s_lshl_b32 s42, s4, 1
	s_add_i32 s10, s10, s11
	s_waitcnt vmcnt(5)
	ds_write_b128 v6, v[92:95]
	s_waitcnt lgkmcnt(0)
	s_barrier
	ds_read_u16 v7, v3
	ds_read_u16 v8, v3 offset:144
	ds_read_u16 v9, v3 offset:288
	ds_read_u16 v12, v3 offset:432
	ds_read_u16 v10, v3 offset:576
	ds_read_u16 v13, v3 offset:720
	ds_read_u16 v11, v3 offset:864
	ds_read_u16 v14, v3 offset:1008
	s_waitcnt lgkmcnt(4)
	v_perm_b32 v9, v12, v9, s6
	v_perm_b32 v8, v8, v7, s6
	s_waitcnt lgkmcnt(2)
	v_perm_b32 v10, v13, v10, s6
	v_lshl_add_u64 v[12:13], v[4:5], 0, s[2:3]
	v_lshl_add_u64 v[12:13], v[12:13], 0, s[42:43]
	s_waitcnt lgkmcnt(0)
	v_perm_b32 v11, v14, v11, s6
	v_lshl_add_u64 v[12:13], v[12:13], 0, v[0:1]
	global_store_dwordx4 v[12:13], v[8:11], off
	s_barrier
	s_cmpk_lt_i32 s10, 0x600
	s_cbranch_scc0 .LBB0_503
	s_bfe_u32 s1, s10, 0x10008
	s_lshl_b32 s4, s10, 6
	s_and_b32 s4, s4, 0x3fc0
	s_ashr_i32 s2, s10, 31
	s_lshr_b32 s2, s2, 23
	s_add_i32 s2, s10, s2
	s_ashr_i32 s2, s2, 9
	s_lshl_b32 s2, s2, 1
	s_or_b32 s2, s2, s1
	s_ashr_i32 s3, s2, 31
	s_lshl_b64 s[2:3], s[2:3], 21
	s_lshl_b32 s42, s4, 1
	s_add_i32 s10, s10, s11
	s_waitcnt vmcnt(4)
	ds_write_b128 v6, v[96:99]
	s_waitcnt lgkmcnt(0)
	s_barrier
	ds_read_u16 v7, v3
	ds_read_u16 v8, v3 offset:144
	ds_read_u16 v9, v3 offset:288
	ds_read_u16 v12, v3 offset:432
	ds_read_u16 v10, v3 offset:576
	ds_read_u16 v13, v3 offset:720
	ds_read_u16 v11, v3 offset:864
	ds_read_u16 v14, v3 offset:1008
	s_waitcnt lgkmcnt(4)
	v_perm_b32 v9, v12, v9, s6
	v_perm_b32 v8, v8, v7, s6
	s_waitcnt lgkmcnt(2)
	v_perm_b32 v10, v13, v10, s6
	v_lshl_add_u64 v[12:13], v[4:5], 0, s[2:3]
	v_lshl_add_u64 v[12:13], v[12:13], 0, s[42:43]
	s_waitcnt lgkmcnt(0)
	v_perm_b32 v11, v14, v11, s6
	v_lshl_add_u64 v[12:13], v[12:13], 0, v[0:1]
	global_store_dwordx4 v[12:13], v[8:11], off
	s_barrier
	s_cmpk_lt_i32 s10, 0x600
	s_cbranch_scc0 .LBB0_503
; #define LAS __attribute__((address_space(3)))
; __device__ __forceinline__ void vt_transpose(const Ctx& c, const bf16_t* proj, bf16_t* vt) {
;     ...
;     for (int it = c.bid; it < 3 * 2 * 256; it += c.G) {
;         const int which = it / 512, g = (it >> 8) & 1, tt = it & 255;
;         const int col = (which == 0 ? PC_VS : (which == 1 ? PC_VW : PC_SV)) + g * 64;
;         { const int tok = c.tid >> 3, ch = c.tid & 7; const u32x4 w = *(const u32x4*)(proj + (size_t)(tt * 64 + tok) * PLD + col + ch * 8);
;           *(LAS u32x4*)(tl + tok * 72 + ch * 8) = w; }
;         __syncthreads();
;         { const int d = c.tid >> 3, ch = c.tid & 7; unsigned short e[8];
; #pragma unroll
;           for (int k = 0; k < 8; ++k) e[k] = tl[(ch * 8 + k) * 72 + d];
;           u32x4 w; w.x = e[0] | ((unsigned)e[1] << 16); w.y = e[2] | ((unsigned)e[3] << 16); w.z = e[4] | ((unsigned)e[5] << 16); w.w = e[6] | ((unsigned)e[7] << 16);
;           *(u32x4*)(vt + ((size_t)(which * 2 + g) * 64 + d) * T + tt * 64 + ch * 8) = w; }
;         __syncthreads();
	s_bfe_u32 s1, s10, 0x10008
	s_lshl_b32 s4, s10, 6
	s_and_b32 s4, s4, 0x3fc0
	s_ashr_i32 s2, s10, 31
	s_lshr_b32 s2, s2, 23
	s_add_i32 s2, s10, s2
	s_ashr_i32 s2, s2, 9
	s_lshl_b32 s2, s2, 1
	s_or_b32 s2, s2, s1
	s_ashr_i32 s3, s2, 31
	s_lshl_b64 s[2:3], s[2:3], 21
	s_lshl_b32 s42, s4, 1
	s_add_i32 s10, s10, s11
	s_waitcnt vmcnt(3)
	ds_write_b128 v6, v[100:103]
	s_waitcnt lgkmcnt(0)
	s_barrier
	ds_read_u16 v7, v3
	ds_read_u16 v8, v3 offset:144
	ds_read_u16 v9, v3 offset:288
	ds_read_u16 v12, v3 offset:432
	ds_read_u16 v10, v3 offset:576
	ds_read_u16 v13, v3 offset:720
	ds_read_u16 v11, v3 offset:864
	ds_read_u16 v14, v3 offset:1008
	s_waitcnt lgkmcnt(4)
	v_perm_b32 v9, v12, v9, s6
	v_perm_b32 v8, v8, v7, s6
	s_waitcnt lgkmcnt(2)
	v_perm_b32 v10, v13, v10, s6
	v_lshl_add_u64 v[12:13], v[4:5], 0, s[2:3]
	v_lshl_add_u64 v[12:13], v[12:13], 0, s[42:43]
	s_waitcnt lgkmcnt(0)
	v_perm_b32 v11, v14, v11, s6
	v_lshl_add_u64 v[12:13], v[12:13], 0, v[0:1]
	global_store_dwordx4 v[12:13], v[8:11], off
	s_barrier
	s_cmpk_lt_i32 s10, 0x600
	s_cbranch_scc0 .LBB0_503
	s_bfe_u32 s1, s10, 0x10008
	s_lshl_b32 s4, s10, 6
	s_and_b32 s4, s4, 0x3fc0
	s_ashr_i32 s2, s10, 31
	s_lshr_b32 s2, s2, 23
	s_add_i32 s2, s10, s2
	s_ashr_i32 s2, s2, 9
	s_lshl_b32 s2, s2, 1
	s_or_b32 s2, s2, s1
	s_ashr_i32 s3, s2, 31
	s_lshl_b64 s[2:3], s[2:3], 21
	s_lshl_b32 s42, s4, 1
	s_add_i32 s10, s10, s11
	s_waitcnt vmcnt(2)
	ds_write_b128 v6, v[104:107]
	s_waitcnt lgkmcnt(0)
	s_barrier
	ds_read_u16 v7, v3
	ds_read_u16 v8, v3 offset:144
	ds_read_u16 v9, v3 offset:288
	ds_read_u16 v12, v3 offset:432
	ds_read_u16 v10, v3 offset:576
	ds_read_u16 v13, v3 offset:720
	ds_read_u16 v11, v3 offset:864
	ds_read_u16 v14, v3 offset:1008
	s_waitcnt lgkmcnt(4)
	v_perm_b32 v9, v12, v9, s6
	v_perm_b32 v8, v8, v7, s6
	s_waitcnt lgkmcnt(2)
	v_perm_b32 v10, v13, v10, s6
	v_lshl_add_u64 v[12:13], v[4:5], 0, s[2:3]
	v_lshl_add_u64 v[12:13], v[12:13], 0, s[42:43]
	s_waitcnt lgkmcnt(0)
	v_perm_b32 v11, v14, v11, s6
	v_lshl_add_u64 v[12:13], v[12:13], 0, v[0:1]
	global_store_dwordx4 v[12:13], v[8:11], off
	s_barrier
	s_cmpk_lt_i32 s10, 0x600
	s_cbranch_scc0 .LBB0_503
	s_bfe_u32 s1, s10, 0x10008
	s_lshl_b32 s4, s10, 6
	s_and_b32 s4, s4, 0x3fc0
	s_ashr_i32 s2, s10, 31
	s_lshr_b32 s2, s2, 23
	s_add_i32 s2, s10, s2
	s_ashr_i32 s2, s2, 9
	s_lshl_b32 s2, s2, 1
	s_or_b32 s2, s2, s1
	s_ashr_i32 s3, s2, 31
	s_lshl_b64 s[2:3], s[2:3], 21
	s_lshl_b32 s42, s4, 1
	s_add_i32 s10, s10, s11
	s_waitcnt vmcnt(1)
	ds_write_b128 v6, v[108:111]
	s_waitcnt lgkmcnt(0)
	s_barrier
	ds_read_u16 v7, v3
	ds_read_u16 v8, v3 offset:144
	ds_read_u16 v9, v3 offset:288
	ds_read_u16 v12, v3 offset:432
	ds_read_u16 v10, v3 offset:576
	ds_read_u16 v13, v3 offset:720
	ds_read_u16 v11, v3 offset:864
	ds_read_u16 v14, v3 offset:1008
	s_waitcnt lgkmcnt(4)
	v_perm_b32 v9, v12, v9, s6
	v_perm_b32 v8, v8, v7, s6
	s_waitcnt lgkmcnt(2)
	v_perm_b32 v10, v13, v10, s6
	v_lshl_add_u64 v[12:13], v[4:5], 0, s[2:3]
	v_lshl_add_u64 v[12:13], v[12:13], 0, s[42:43]
	s_waitcnt lgkmcnt(0)
	v_perm_b32 v11, v14, v11, s6
	v_lshl_add_u64 v[12:13], v[12:13], 0, v[0:1]
	global_store_dwordx4 v[12:13], v[8:11], off
	s_barrier
	s_cmpk_lt_i32 s10, 0x600
	s_cbranch_scc0 .LBB0_503
	s_bfe_u32 s1, s10, 0x10008
	s_lshl_b32 s4, s10, 6
	s_and_b32 s4, s4, 0x3fc0
	s_ashr_i32 s2, s10, 31
	s_lshr_b32 s2, s2, 23
	s_add_i32 s2, s10, s2
	s_ashr_i32 s2, s2, 9
	s_lshl_b32 s2, s2, 1
	s_or_b32 s2, s2, s1
	s_ashr_i32 s3, s2, 31
	s_lshl_b64 s[2:3], s[2:3], 21
	s_lshl_b32 s42, s4, 1
	s_add_i32 s10, s10, s11
	s_waitcnt vmcnt(0)
	ds_write_b128 v6, v[112:115]
	s_waitcnt lgkmcnt(0)
	s_barrier
	ds_read_u16 v7, v3
	ds_read_u16 v8, v3 offset:144
	ds_read_u16 v9, v3 offset:288
	ds_read_u16 v12, v3 offset:432
	ds_read_u16 v10, v3 offset:576
	ds_read_u16 v13, v3 offset:720
	ds_read_u16 v11, v3 offset:864
	ds_read_u16 v14, v3 offset:1008
	s_waitcnt lgkmcnt(4)
	v_perm_b32 v9, v12, v9, s6
	v_perm_b32 v8, v8, v7, s6
	s_waitcnt lgkmcnt(2)
	v_perm_b32 v10, v13, v10, s6
	v_lshl_add_u64 v[12:13], v[4:5], 0, s[2:3]
	v_lshl_add_u64 v[12:13], v[12:13], 0, s[42:43]
	s_waitcnt lgkmcnt(0)
	v_perm_b32 v11, v14, v11, s6
	v_lshl_add_u64 v[12:13], v[12:13], 0, v[0:1]
	global_store_dwordx4 v[12:13], v[8:11], off
	s_barrier
	s_lshl_b32 s0, s10, 6
	s_cmpk_lt_i32 s10, 0x600
	s_cbranch_scc0 .LBB0_503
